# conversion loop: next tile's loads stay in flight (counted vmcnt 30..16 copy on the has-next path, edge waits 24/8)
# speedup vs baseline: 1.0057x; 1.0027x over previous
; #define LAS __attribute__((address_space(3)))
; __device__ __forceinline__ TrItem tr_decode(const Args& a, int it) {
;     unsigned char* ws = a.ws;
;     constexpr int T_IN = 32 * (INCOLS / 64), T_OUT = 32 * (DM / 64), T_GU1 = 32 * (4096 / 64), T_DN1 = 32 * (DM / 64);
;     TrItem t; int r = it;
;     if (r < T_IN) { const int kb = r & 31, nb = r >> 5; t.N = INCOLS; t.src = a.in[I_WIN] + (size_t)(64 * kb) * INCOLS + 64 * nb; t.dst = (bf16*)(ws + WS_WIN) + (size_t)(64 * nb) * DM + 64 * kb; return t; } r -= T_IN;
;     if (r < T_OUT) { const int kb = r & 31, nb = r >> 5; t.N = DM; t.src = a.in[I_WOUT] + (size_t)(64 * kb) * DM + 64 * nb; t.dst = (bf16*)(ws + WS_WOUT) + (size_t)(64 * nb) * DM + 64 * kb; return t; } r -= T_OUT;
;     if (r < NEXP * T_GU1) { const int e = r / T_GU1, q = r % T_GU1, kb = q & 31, nb = q >> 5, n0 = 64 * nb;
;         const int drow0 = n0 < 2048 ? (n0 >> 7) * 256 + (n0 & 127) : ((n0 - 2048) >> 7) * 256 + 128 + ((n0 - 2048) & 127);
;         t.N = 4096; t.src = a.in[I_WGU] + (size_t)e * DM * 4096 + (size_t)(64 * kb) * 4096 + n0; t.dst = (bf16*)(ws + WS_WGU) + (size_t)e * 4096 * DM + (size_t)drow0 * DM + 64 * kb; return t; } r -= NEXP * T_GU1;
;     { const int e = r / T_DN1, q = r % T_DN1, kb = q & 31, nb = q >> 5;
;         t.N = DM; t.src = a.in[I_WDN] + (size_t)e * DM * DM + (size_t)(64 * kb) * DM + 64 * nb; t.dst = (bf16*)(ws + WS_WDN) + (size_t)e * DM * DM + (size_t)(64 * nb) * DM + 64 * kb; return t; }
; }
; __device__ __forceinline__ void tr_load(const TrItem& t, f32x4 (&ra)[8], f32x4 (&rb)[8], int lane) {
;     const int q = lane >> 4, n4 = lane & 15;
;     const float* p = t.src + (size_t)(2 * q) * t.N + 4 * n4;
; #pragma unroll
;     for (int i = 0; i < 8; ++i) { ra[i] = __builtin_nontemporal_load((const f32x4*)(p + (size_t)(8 * i) * t.N)); rb[i] = __builtin_nontemporal_load((const f32x4*)(p + (size_t)(8 * i + 1) * t.N)); }
; }
; __device__ __forceinline__ void conv_items(const Args& a, LAS unsigned char* lds, int it0, int it1, int vcu, int G, int lane, int wave) {
;     LAS unsigned* scr = (LAS unsigned*)(lds + wave * 16384);
;     const int gw = vcu * NWAVES + wave, NGW = G * NWAVES;
;     f32x4 ra[8], rb[8], na[8], nb_[8];
;     int it = it0 + gw;
;     if (it >= it1) return;
;     TrItem cur = tr_decode(a, it);
;     tr_load(cur, ra, rb, lane);
.LBB0_69:
	s_lshl_b32 s0, s1, 3
	v_readlane_b32 s1, v246, 11
	s_lshl_b32 s2, s1, 3
	s_add_i32 s4, s0, s3
	s_cmpk_gt_i32 s4, 0xfff
	s_cbranch_scc1 .LBB0_110
	s_lshl_b32 s0, s4, 6
	s_and_b32 s14, s0, 0x7c0
	s_lshl_b32 s3, s4, 1
	s_lshl_b32 s0, s14, 13
	s_add_u32 s5, s40, s0
	s_addc_u32 s8, s41, 0
	s_and_b32 s0, s3, 0x1fc0
	s_mov_b32 s7, 0
	s_add_i32 s6, s0, 0xffffe800
	s_lshl_b64 s[0:1], s[6:7], 2
	v_readlane_b32 s52, v246, 14
	s_add_u32 s15, s5, s0
	v_readlane_b32 s58, v246, 20
	v_readlane_b32 s59, v246, 21
	s_addc_u32 s16, s8, s1
	s_mul_i32 s0, s14, 0x6000
	s_mov_b64 s[18:19], s[58:59]
	s_add_u32 s5, s18, s0
	s_addc_u32 s10, s19, 0
	s_and_b32 s0, s3, 0xffffffc0
	s_ashr_i32 s1, s0, 31
	s_lshl_b64 s[8:9], s[0:1], 2
	s_add_u32 s8, s5, s8
	s_addc_u32 s9, s10, s9
	s_add_u32 s3, s92, 0x70800000
	s_addc_u32 s5, s93, 0
	s_add_u32 s44, s92, 0x50800000
	s_addc_u32 s45, s93, 0
	s_add_u32 s10, s92, 0x1a00000
	s_addc_u32 s11, s93, 0
	s_add_u32 s12, s92, 0x200000
	s_addc_u32 s13, s93, 0
	s_cmpk_lt_i32 s4, 0xc00
	s_cselect_b32 s0, s0, s6
	s_mov_b32 s6, 0x200000
	s_cselect_b32 s6, s6, 0x1a00000
	s_cselect_b32 s8, s8, s15
	s_movk_i32 s15, 0x1800
	s_cselect_b32 s1, s1, 0
	s_cselect_b32 s9, s9, s16
	s_cselect_b32 s15, s15, 0x800
	s_add_u32 s6, s92, s6
	s_waitcnt lgkmcnt(0)
	v_lshrrev_b32_e32 v2, 2, v194
	s_addc_u32 s16, s93, 0
	s_lshl_b64 s[0:1], s[0:1], 12
	v_lshlrev_b32_e32 v67, 2, v194
	v_and_b32_e32 v68, 12, v2
	s_add_u32 s0, s6, s0
	v_mul_u32_u24_e32 v2, s15, v131
	v_and_b32_e32 v142, 60, v67
	v_mov_b32_e32 v145, 0
	s_addc_u32 s1, s16, s1
	s_lshl_b32 s6, s14, 1
	v_lshlrev_b32_e32 v144, 2, v2
	s_add_u32 s16, s0, s6
	v_lshl_add_u64 v[2:3], s[8:9], 0, v[144:145]
	v_lshlrev_b32_e32 v144, 2, v142
	s_addc_u32 s17, s1, 0
	v_lshl_add_u64 v[2:3], v[2:3], 0, v[144:145]
	s_lshl_b32 s6, s15, 2
	v_lshl_add_u64 v[10:11], v[2:3], 0, s[6:7]
	s_mul_i32 s0, s15, 28
	s_mov_b32 s1, s7
	global_load_dwordx4 v[2:5], v[2:3], off nt
	s_nop 0
	global_load_dwordx4 v[6:9], v[10:11], off nt
	v_lshl_add_u64 v[10:11], v[10:11], 0, s[0:1]
	v_lshl_add_u64 v[18:19], v[10:11], 0, s[6:7]
	global_load_dwordx4 v[10:13], v[10:11], off nt
	s_nop 0
	global_load_dwordx4 v[14:17], v[18:19], off nt
	v_lshl_add_u64 v[18:19], v[18:19], 0, s[0:1]
	v_lshl_add_u64 v[26:27], v[18:19], 0, s[6:7]
	global_load_dwordx4 v[18:21], v[18:19], off nt
	s_nop 0
	global_load_dwordx4 v[22:25], v[26:27], off nt
	v_lshl_add_u64 v[26:27], v[26:27], 0, s[0:1]
	v_lshl_add_u64 v[34:35], v[26:27], 0, s[6:7]
	v_lshl_add_u64 v[38:39], v[34:35], 0, s[0:1]
	v_lshl_add_u64 v[42:43], v[38:39], 0, s[6:7]
	v_lshl_add_u64 v[46:47], v[42:43], 0, s[0:1]
	v_lshl_add_u64 v[50:51], v[46:47], 0, s[6:7]
	v_lshl_add_u64 v[54:55], v[50:51], 0, s[0:1]
	v_lshl_add_u64 v[58:59], v[54:55], 0, s[6:7]
	v_lshl_add_u64 v[62:63], v[58:59], 0, s[0:1]
	global_load_dwordx4 v[26:29], v[26:27], off nt
	s_nop 0
	global_load_dwordx4 v[30:33], v[34:35], off nt
	v_or_b32_e32 v78, 8, v66
	global_load_dwordx4 v[34:37], v[38:39], off nt
	v_bitop3_b32 v80, v78, 28, v67 bitop3:0x48
	global_load_dwordx4 v[38:41], v[42:43], off nt
	v_lshlrev_b32_e32 v1, 9, v0
	global_load_dwordx4 v[42:45], v[46:47], off nt
	v_lshlrev_b32_e32 v79, 7, v78
	global_load_dwordx4 v[46:49], v[50:51], off nt
	v_lshlrev_b32_e32 v80, 2, v80
	global_load_dwordx4 v[50:53], v[54:55], off nt
	v_lshlrev_b32_e32 v150, 12, v78
	global_load_dwordx4 v[54:57], v[58:59], off nt
	v_or_b32_e32 v78, 16, v66
	global_load_dwordx4 v[58:61], v[62:63], off nt
	v_lshl_add_u64 v[62:63], v[62:63], 0, s[6:7]
	global_load_dwordx4 v[62:65], v[62:63], off nt
	v_and_b32_e32 v1, 0x1e00, v1
	v_add3_u32 v143, s33, v79, v80
	v_bitop3_b32 v80, v78, 28, v67 bitop3:0x48
	v_add3_u32 v68, s33, v1, v68
	v_lshlrev_b32_e32 v1, 4, v0
	v_mov_b32_e32 v70, 0x70
	s_movk_i32 s1, 0x50
	v_lshlrev_b32_e32 v79, 7, v78
	v_lshlrev_b32_e32 v80, 2, v80
	v_lshlrev_b32_e32 v152, 12, v78
	v_or_b32_e32 v78, 24, v66
	s_movk_i32 s0, 0x70
	v_bitop3_b32 v75, v1, s1, v70 bitop3:0x6c
	s_movk_i32 s1, 0x60
	v_add3_u32 v147, s33, v79, v80
	v_bitop3_b32 v80, v78, 28, v67 bitop3:0x48
	v_and_b32_e32 v69, 0x70, v1
	v_bitop3_b32 v71, v1, 16, v70 bitop3:0x6c
	v_bitop3_b32 v72, v1, 32, v70 bitop3:0x6c
	v_bitop3_b32 v73, v1, 48, v70 bitop3:0x6c
	v_bitop3_b32 v74, v1, 64, v70 bitop3:0x6c
	v_bitop3_b32 v70, v1, s1, v70 bitop3:0x6c
	v_bitop3_b32 v76, v1, s0, v1 bitop3:0xc
	v_lshlrev_b32_e32 v1, 3, v0
	v_bitop3_b32 v77, v66, 28, v67 bitop3:0x48
	v_lshlrev_b32_e32 v79, 7, v78
	v_lshlrev_b32_e32 v80, 2, v80
	v_lshlrev_b32_e32 v154, 12, v78
	v_or_b32_e32 v78, 32, v66
	v_and_b32_e32 v146, 56, v1
	v_lshlrev_b32_e32 v1, 7, v66
	v_lshlrev_b32_e32 v77, 2, v77
	v_add3_u32 v164, s33, v79, v80
	v_lshlrev_b32_e32 v79, 7, v78
	v_add3_u32 v1, s33, v1, v77
	v_add3_u32 v165, s33, v79, v77
	v_or_b32_e32 v77, 40, v66
	v_bitop3_b32 v79, v77, 28, v67 bitop3:0x48
	v_lshlrev_b32_e32 v148, 12, v66
	v_lshlrev_b32_e32 v156, 12, v78
	v_lshlrev_b32_e32 v78, 7, v77
	v_lshlrev_b32_e32 v79, 2, v79
	v_lshlrev_b32_e32 v158, 12, v77
	v_or_b32_e32 v77, 48, v66
	v_or_b32_e32 v66, 56, v66
	v_add3_u32 v166, s33, v78, v79
	v_bitop3_b32 v79, v77, 28, v67 bitop3:0x48
	v_bitop3_b32 v67, v66, 28, v67 bitop3:0x48
	v_lshlrev_b32_e32 v78, 7, v77
	v_lshlrev_b32_e32 v79, 2, v79
	v_lshlrev_b32_e32 v160, 12, v77
	v_lshlrev_b32_e32 v77, 7, v66
	v_lshlrev_b32_e32 v67, 2, v67
	v_readlane_b32 s0, v246, 11
	v_mov_b32_e32 v149, v145
	v_mov_b32_e32 v151, v145
	v_mov_b32_e32 v153, v145
	v_mov_b32_e32 v155, v145
	v_mov_b32_e32 v157, v145
	v_mov_b32_e32 v159, v145
	v_add3_u32 v167, s33, v78, v79
	v_mov_b32_e32 v161, v145
	v_add3_u32 v168, s33, v77, v67
	v_lshlrev_b32_e32 v162, 12, v66
	v_mov_b32_e32 v163, v145
	s_lshl_b32 s33, s0, 4
	v_add_u32_e32 v169, v68, v69
	v_add_u32_e32 v170, v68, v71
	v_add_u32_e32 v171, v68, v72
	v_add_u32_e32 v172, v68, v73
	v_add_u32_e32 v173, v68, v74
	v_add_u32_e32 v174, v68, v75
	v_add_u32_e32 v175, v68, v70
	v_add_u32_e32 v176, v68, v76
	s_mov_b32 s30, s4
	v_readlane_b32 s53, v246, 15
	v_readlane_b32 s54, v246, 16
	v_readlane_b32 s55, v246, 17
	v_readlane_b32 s56, v246, 18
	v_readlane_b32 s57, v246, 19
	v_readlane_b32 s60, v246, 22
	v_readlane_b32 s61, v246, 23
	v_readlane_b32 s62, v246, 24
	v_readlane_b32 s63, v246, 25
	v_readlane_b32 s64, v246, 26
	v_readlane_b32 s65, v246, 27
	v_readlane_b32 s66, v246, 28
	v_readlane_b32 s67, v246, 29
	s_branch .LBB0_73
; #define LAS __attribute__((address_space(3)))
; #define LDS_WAIT() asm volatile("s_waitcnt lgkmcnt(0)" ::: "memory")
; __device__ __forceinline__ unsigned cvt2bf(float lo, float hi) { const f32x2_t v = {lo, hi}; const bf16x2_t r = __builtin_convertvector(v, bf16x2_t); return __builtin_bit_cast(unsigned, r); }
; __device__ __forceinline__ void tr_store(const TrItem& t, const f32x4 (&ra)[8], const f32x4 (&rb)[8], LAS unsigned* scr, int lane) {
;     const int q = lane >> 4, n4 = lane & 15;
; #pragma unroll
;     for (int i = 0; i < 8; ++i)
; #pragma unroll
;         for (int j = 0; j < 4; ++j) scr[(4 * n4 + j) * 32 + ((i ^ (n4 & 7)) << 2) + q] = cvt2bf(ra[i][j], rb[i][j]);
;     LDS_WAIT(); asm volatile("" ::: "memory");
;     const int nr = lane >> 3, ch = lane & 7;
; #pragma unroll
;     for (int i = 0; i < 8; ++i) { const int n = nr + 8 * i; const v4u v = *(const LAS v4u*)(scr + n * 32 + ((ch ^ ((n >> 2) & 7)) << 2));
;         __builtin_nontemporal_store(v, (v4u*)(t.dst + (size_t)n * DM + 8 * ch)); }
;     LDS_WAIT(); asm volatile("" ::: "memory");
; }
; __device__ __forceinline__ void conv_items(const Args& a, LAS unsigned char* lds, int it0, int it1, int vcu, int G, int lane, int wave) {
;     ...
;         it = nx; nx = it + NGW; has = nx < it1;
.Lcvw_0:
	s_waitcnt vmcnt(8)
.LBB0_71:
	v_cvt_pk_bf16_f32 v177, v66, v90
	v_cvt_pk_bf16_f32 v178, v67, v91
	ds_write2_b32 v169, v177, v178 offset1:32
	v_cvt_pk_bf16_f32 v177, v68, v92
	v_cvt_pk_bf16_f32 v178, v69, v93
	ds_write2_b32 v169, v177, v178 offset0:64 offset1:96
	v_cvt_pk_bf16_f32 v177, v70, v106
	v_cvt_pk_bf16_f32 v178, v71, v107
	ds_write2_b32 v170, v177, v178 offset1:32
	v_cvt_pk_bf16_f32 v177, v72, v108
	v_cvt_pk_bf16_f32 v178, v73, v109
	ds_write2_b32 v170, v177, v178 offset0:64 offset1:96
	v_cvt_pk_bf16_f32 v177, v74, v114
	v_cvt_pk_bf16_f32 v178, v75, v115
	ds_write2_b32 v171, v177, v178 offset1:32
	v_cvt_pk_bf16_f32 v177, v76, v116
	v_cvt_pk_bf16_f32 v178, v77, v117
	ds_write2_b32 v171, v177, v178 offset0:64 offset1:96
	v_cvt_pk_bf16_f32 v177, v78, v122
	v_cvt_pk_bf16_f32 v178, v79, v123
	ds_write2_b32 v172, v177, v178 offset1:32
	v_cvt_pk_bf16_f32 v177, v80, v124
	v_cvt_pk_bf16_f32 v178, v81, v125
	ds_write2_b32 v172, v177, v178 offset0:64 offset1:96
	v_cvt_pk_bf16_f32 v177, v82, v102
	v_cvt_pk_bf16_f32 v178, v83, v103
	ds_write2_b32 v173, v177, v178 offset1:32
	v_cvt_pk_bf16_f32 v177, v84, v104
	v_cvt_pk_bf16_f32 v178, v85, v105
	ds_write2_b32 v173, v177, v178 offset0:64 offset1:96
	v_cvt_pk_bf16_f32 v177, v86, v110
	v_cvt_pk_bf16_f32 v178, v87, v111
	ds_write2_b32 v174, v177, v178 offset1:32
	v_cvt_pk_bf16_f32 v177, v88, v112
	v_cvt_pk_bf16_f32 v178, v89, v113
	ds_write2_b32 v174, v177, v178 offset0:64 offset1:96
	v_cvt_pk_bf16_f32 v177, v94, v118
	v_cvt_pk_bf16_f32 v178, v95, v119
	s_lshl_b64 s[0:1], s[0:1], 12
	ds_write2_b32 v175, v177, v178 offset1:32
	v_cvt_pk_bf16_f32 v177, v96, v120
	v_cvt_pk_bf16_f32 v178, v97, v121
	s_add_u32 s6, s24, s0
	ds_write2_b32 v175, v177, v178 offset0:64 offset1:96
	v_cvt_pk_bf16_f32 v177, v98, v126
	v_cvt_pk_bf16_f32 v178, v99, v127
	s_addc_u32 s8, s25, s1
	s_lshl_b64 s[0:1], s[16:17], 1
	ds_write2_b32 v176, v177, v178 offset1:32
	v_cvt_pk_bf16_f32 v177, v100, v128
	v_cvt_pk_bf16_f32 v178, v101, v129
	s_add_u32 s16, s6, s0
	ds_write2_b32 v176, v177, v178 offset0:64 offset1:96
	s_addc_u32 s17, s8, s1
	s_add_i32 s30, s52, s2
	s_lshl_b64 s[0:1], s[18:19], 12
	s_waitcnt lgkmcnt(0)
	s_add_u32 s6, s22, s0
	s_addc_u32 s8, s23, s1
	s_lshl_b64 s[0:1], s[20:21], 1
	ds_read_b128 v[178:181], v1
	ds_read_b128 v[182:185], v143
	s_add_u32 s0, s6, s0
	s_addc_u32 s1, s8, s1
	v_lshl_add_u64 v[190:191], s[0:1], 0, v[144:145]
	v_lshl_add_u64 v[186:187], v[190:191], 0, v[148:149]
	s_waitcnt lgkmcnt(1)
	global_store_dwordx4 v[186:187], v[178:181], off nt
	ds_read_b128 v[178:181], v147
	v_lshl_add_u64 v[186:187], v[190:191], 0, v[150:151]
	s_waitcnt lgkmcnt(1)
	global_store_dwordx4 v[186:187], v[182:185], off nt
	ds_read_b128 v[182:185], v164
	v_lshl_add_u64 v[186:187], v[190:191], 0, v[152:153]
	s_waitcnt lgkmcnt(1)
	global_store_dwordx4 v[186:187], v[178:181], off nt
	ds_read_b128 v[178:181], v165
	v_lshl_add_u64 v[186:187], v[190:191], 0, v[154:155]
	s_waitcnt lgkmcnt(1)
	global_store_dwordx4 v[186:187], v[182:185], off nt
	v_lshl_add_u64 v[186:187], v[190:191], 0, v[156:157]
	ds_read_b128 v[182:185], v166
	s_waitcnt lgkmcnt(1)
	global_store_dwordx4 v[186:187], v[178:181], off nt
	ds_read_b128 v[178:181], v167
	ds_read_b128 v[186:189], v168
	v_lshl_add_u64 v[192:193], v[190:191], 0, v[158:159]
	s_waitcnt lgkmcnt(2)
	global_store_dwordx4 v[192:193], v[182:185], off nt
	s_cmpk_gt_i32 s30, 0xfff
	s_cselect_b64 s[0:1], -1, 0
	v_lshl_add_u64 v[182:183], v[190:191], 0, v[160:161]
	s_waitcnt lgkmcnt(1)
	global_store_dwordx4 v[182:183], v[178:181], off nt
	s_nop 1
	v_lshl_add_u64 v[178:179], v[190:191], 0, v[162:163]
	s_waitcnt lgkmcnt(0)
	global_store_dwordx4 v[178:179], v[186:189], off nt
	s_waitcnt lgkmcnt(0)

; #define LAS __attribute__((address_space(3)))
; __device__ __forceinline__ unsigned cvt2bf(float lo, float hi) { const f32x2_t v = {lo, hi}; const bf16x2_t r = __builtin_convertvector(v, bf16x2_t); return __builtin_bit_cast(unsigned, r); }
; __device__ __forceinline__ void tr_load(const TrItem& t, f32x4 (&ra)[8], f32x4 (&rb)[8], int lane) {
;     const int q = lane >> 4, n4 = lane & 15;
;     const float* p = t.src + (size_t)(2 * q) * t.N + 4 * n4;
; #pragma unroll
;     for (int i = 0; i < 8; ++i) { ra[i] = __builtin_nontemporal_load((const f32x4*)(p + (size_t)(8 * i) * t.N)); rb[i] = __builtin_nontemporal_load((const f32x4*)(p + (size_t)(8 * i + 1) * t.N)); }
; }
; __device__ __forceinline__ void tr_store(const TrItem& t, const f32x4 (&ra)[8], const f32x4 (&rb)[8], LAS unsigned* scr, int lane) {
;     const int q = lane >> 4, n4 = lane & 15;
; #pragma unroll
;     for (int i = 0; i < 8; ++i)
; #pragma unroll
;         for (int j = 0; j < 4; ++j) scr[(4 * n4 + j) * 32 + ((i ^ (n4 & 7)) << 2) + q] = cvt2bf(ra[i][j], rb[i][j]);
; __device__ __forceinline__ void conv_items(const Args& a, LAS unsigned char* lds, int it0, int it1, int vcu, int G, int lane, int wave) {
;     ...
;         int nx = it + NGW; bool has = nx < it1;
;         TrItem nxt = tr_decode(a, has ? nx : it);
;         if (has) tr_load(nxt, na, nb_, lane);
;         tr_store(cur, ra, rb, scr, lane);
.LBB0_88:
	v_mul_u32_u24_e32 v66, s28, v131
	v_lshlrev_b32_e32 v144, 2, v66
	v_lshl_add_u64 v[66:67], s[26:27], 0, v[144:145]
	v_lshlrev_b32_e32 v144, 2, v142
	v_lshl_add_u64 v[66:67], v[66:67], 0, v[144:145]
	s_lshl_b64 s[8:9], s[28:29], 2
	v_lshl_add_u64 v[70:71], v[66:67], 0, s[8:9]
	s_mul_i32 s6, s28, 28
	global_load_dwordx4 v[66:69], v[66:67], off nt
	s_nop 0
	global_load_dwordx4 v[90:93], v[70:71], off nt
	v_lshl_add_u64 v[70:71], v[70:71], 0, s[6:7]
	v_lshl_add_u64 v[74:75], v[70:71], 0, s[8:9]
	global_load_dwordx4 v[70:73], v[70:71], off nt
	s_nop 0
	global_load_dwordx4 v[106:109], v[74:75], off nt
	v_lshl_add_u64 v[74:75], v[74:75], 0, s[6:7]
	v_lshl_add_u64 v[78:79], v[74:75], 0, s[8:9]
	global_load_dwordx4 v[74:77], v[74:75], off nt
	s_nop 0
	global_load_dwordx4 v[114:117], v[78:79], off nt
	v_lshl_add_u64 v[78:79], v[78:79], 0, s[6:7]
	v_lshl_add_u64 v[82:83], v[78:79], 0, s[8:9]
	v_lshl_add_u64 v[86:87], v[82:83], 0, s[6:7]
	global_load_dwordx4 v[78:81], v[78:79], off nt
	s_nop 0
	global_load_dwordx4 v[122:125], v[82:83], off nt
	s_nop 0
	global_load_dwordx4 v[82:85], v[86:87], off nt
	v_lshl_add_u64 v[86:87], v[86:87], 0, s[8:9]
	v_lshl_add_u64 v[94:95], v[86:87], 0, s[6:7]
	global_load_dwordx4 v[102:105], v[86:87], off nt
	s_nop 0
	global_load_dwordx4 v[86:89], v[94:95], off nt
	v_lshl_add_u64 v[94:95], v[94:95], 0, s[8:9]
	v_lshl_add_u64 v[98:99], v[94:95], 0, s[6:7]
	global_load_dwordx4 v[110:113], v[94:95], off nt
	s_nop 0
	global_load_dwordx4 v[94:97], v[98:99], off nt
	v_lshl_add_u64 v[98:99], v[98:99], 0, s[8:9]
	v_lshl_add_u64 v[126:127], v[98:99], 0, s[6:7]
	global_load_dwordx4 v[118:121], v[98:99], off nt
	s_nop 0
	global_load_dwordx4 v[98:101], v[126:127], off nt
	v_lshl_add_u64 v[126:127], v[126:127], 0, s[8:9]
	global_load_dwordx4 v[126:129], v[126:127], off nt
	s_waitcnt vmcnt(30)
	v_cvt_pk_bf16_f32 v144, v2, v6
	v_cvt_pk_bf16_f32 v177, v3, v7
	ds_write2_b32 v169, v144, v177 offset1:32
	v_cvt_pk_bf16_f32 v144, v4, v8
	v_cvt_pk_bf16_f32 v177, v5, v9
	ds_write2_b32 v169, v144, v177 offset0:64 offset1:96
	s_waitcnt vmcnt(28)
	v_cvt_pk_bf16_f32 v144, v10, v14
	v_cvt_pk_bf16_f32 v177, v11, v15
	ds_write2_b32 v170, v144, v177 offset1:32
	v_cvt_pk_bf16_f32 v144, v12, v16
	v_cvt_pk_bf16_f32 v177, v13, v17
	ds_write2_b32 v170, v144, v177 offset0:64 offset1:96
	s_waitcnt vmcnt(26)
	v_cvt_pk_bf16_f32 v144, v18, v22
	v_cvt_pk_bf16_f32 v177, v19, v23
	ds_write2_b32 v171, v144, v177 offset1:32
	v_cvt_pk_bf16_f32 v144, v20, v24
	v_cvt_pk_bf16_f32 v177, v21, v25
	ds_write2_b32 v171, v144, v177 offset0:64 offset1:96
	s_waitcnt vmcnt(24)
	v_cvt_pk_bf16_f32 v144, v26, v30
	v_cvt_pk_bf16_f32 v177, v27, v31
	ds_write2_b32 v172, v144, v177 offset1:32
	v_cvt_pk_bf16_f32 v144, v28, v32
	v_cvt_pk_bf16_f32 v177, v29, v33
	ds_write2_b32 v172, v144, v177 offset0:64 offset1:96
	s_waitcnt vmcnt(22)
	v_cvt_pk_bf16_f32 v144, v34, v38
	v_cvt_pk_bf16_f32 v177, v35, v39
	ds_write2_b32 v173, v144, v177 offset1:32
	v_cvt_pk_bf16_f32 v144, v36, v40
	v_cvt_pk_bf16_f32 v177, v37, v41
	ds_write2_b32 v173, v144, v177 offset0:64 offset1:96
	s_waitcnt vmcnt(20)
	v_cvt_pk_bf16_f32 v144, v42, v46
	v_cvt_pk_bf16_f32 v177, v43, v47
	ds_write2_b32 v174, v144, v177 offset1:32
	v_cvt_pk_bf16_f32 v144, v44, v48
	v_cvt_pk_bf16_f32 v177, v45, v49
	ds_write2_b32 v174, v144, v177 offset0:64 offset1:96
	s_waitcnt vmcnt(18)
	v_cvt_pk_bf16_f32 v144, v50, v54
	v_cvt_pk_bf16_f32 v177, v51, v55
	ds_write2_b32 v175, v144, v177 offset1:32
	v_cvt_pk_bf16_f32 v144, v52, v56
	v_cvt_pk_bf16_f32 v177, v53, v57
	ds_write2_b32 v175, v144, v177 offset0:64 offset1:96
	s_waitcnt vmcnt(16)
	v_cvt_pk_bf16_f32 v144, v58, v62
	v_cvt_pk_bf16_f32 v177, v59, v63
	ds_write2_b32 v176, v144, v177 offset1:32
	v_cvt_pk_bf16_f32 v144, v60, v64
	v_cvt_pk_bf16_f32 v177, v61, v65
	ds_write2_b32 v176, v144, v177 offset0:64 offset1:96
	s_branch .Lcvj_0

; #define LAS __attribute__((address_space(3)))
; #define LDS_WAIT() asm volatile("s_waitcnt lgkmcnt(0)" ::: "memory")
; __device__ __forceinline__ TrItem tr_decode(const Args& a, int it) {
;     ...
;     if (r < T_IN) { const int kb = r & 31, nb = r >> 5; t.N = INCOLS; t.src = a.in[I_WIN] + (size_t)(64 * kb) * INCOLS + 64 * nb; t.dst = (bf16*)(ws + WS_WIN) + (size_t)(64 * nb) * DM + 64 * kb; return t; } r -= T_IN;
;     if (r < T_OUT) { const int kb = r & 31, nb = r >> 5; t.N = DM; t.src = a.in[I_WOUT] + (size_t)(64 * kb) * DM + 64 * nb; t.dst = (bf16*)(ws + WS_WOUT) + (size_t)(64 * nb) * DM + 64 * kb; return t; } r -= T_OUT;
;     if (r < NEXP * T_GU1) { const int e = r / T_GU1, q = r % T_GU1, kb = q & 31, nb = q >> 5, n0 = 64 * nb;
;         const int drow0 = n0 < 2048 ? (n0 >> 7) * 256 + (n0 & 127) : ((n0 - 2048) >> 7) * 256 + 128 + ((n0 - 2048) & 127);
;         t.N = 4096; t.src = a.in[I_WGU] + (size_t)e * DM * 4096 + (size_t)(64 * kb) * 4096 + n0; t.dst = (bf16*)(ws + WS_WGU) + (size_t)e * 4096 * DM + (size_t)drow0 * DM + 64 * kb; return t; } r -= NEXP * T_GU1;
;     { const int e = r / T_DN1, q = r % T_DN1, kb = q & 31, nb = q >> 5;
;         t.N = DM; t.src = a.in[I_WDN] + (size_t)e * DM * DM + (size_t)(64 * kb) * DM + 64 * nb; t.dst = (bf16*)(ws + WS_WDN) + (size_t)e * DM * DM + (size_t)(64 * nb) * DM + 64 * kb; return t; }
; __device__ __forceinline__ void tr_store(const TrItem& t, const f32x4 (&ra)[8], const f32x4 (&rb)[8], LAS unsigned* scr, int lane) {
;     ...
;     LDS_WAIT(); asm volatile("" ::: "memory");
;     const int nr = lane >> 3, ch = lane & 7;
; #pragma unroll
;     for (int i = 0; i < 8; ++i) { const int n = nr + 8 * i; const v4u v = *(const LAS v4u*)(scr + n * 32 + ((ch ^ ((n >> 2) & 7)) << 2));
;         __builtin_nontemporal_store(v, (v4u*)(t.dst + (size_t)n * DM + 8 * ch)); }
;     LDS_WAIT(); asm volatile("" ::: "memory");
; }
; __device__ __forceinline__ void conv_items(const Args& a, LAS unsigned char* lds, int it0, int it1, int vcu, int G, int lane, int wave) {
;     ...
;         if (!has) break;
;         it = nx; nx = it + NGW; has = nx < it1;
;         cur = tr_decode(a, has ? nx : it);
.Lcvj_0:
	s_waitcnt lgkmcnt(0)
	ds_read_b128 v[178:181], v1
	ds_read_b128 v[182:185], v143
	v_lshlrev_b32_e32 v144, 1, v146
	v_lshl_add_u64 v[190:191], s[16:17], 0, v[144:145]
	v_lshl_add_u64 v[186:187], v[190:191], 0, v[148:149]
	s_waitcnt lgkmcnt(1)
	global_store_dwordx4 v[186:187], v[178:181], off nt
	ds_read_b128 v[178:181], v147
	v_lshl_add_u64 v[186:187], v[190:191], 0, v[150:151]
	s_waitcnt lgkmcnt(1)
	global_store_dwordx4 v[186:187], v[182:185], off nt
	ds_read_b128 v[182:185], v164
	v_lshl_add_u64 v[186:187], v[190:191], 0, v[152:153]
	s_waitcnt lgkmcnt(1)
	global_store_dwordx4 v[186:187], v[178:181], off nt
	ds_read_b128 v[178:181], v165
	v_lshl_add_u64 v[186:187], v[190:191], 0, v[154:155]
	s_waitcnt lgkmcnt(1)
	global_store_dwordx4 v[186:187], v[182:185], off nt
	v_lshl_add_u64 v[186:187], v[190:191], 0, v[156:157]
	ds_read_b128 v[182:185], v166
	s_waitcnt lgkmcnt(1)
	global_store_dwordx4 v[186:187], v[178:181], off nt
	ds_read_b128 v[178:181], v167
	ds_read_b128 v[186:189], v168
	v_lshl_add_u64 v[192:193], v[190:191], 0, v[158:159]
	s_waitcnt lgkmcnt(2)
	global_store_dwordx4 v[192:193], v[182:185], off nt
	s_and_b64 vcc, exec, s[0:1]
	s_mov_b64 s[0:1], -1
	v_lshl_add_u64 v[182:183], v[190:191], 0, v[160:161]
	s_waitcnt lgkmcnt(1)
	global_store_dwordx4 v[182:183], v[178:181], off nt
	s_nop 1
	v_lshl_add_u64 v[178:179], v[190:191], 0, v[162:163]
	s_waitcnt lgkmcnt(0)
	global_store_dwordx4 v[178:179], v[186:189], off nt
	s_waitcnt lgkmcnt(0)
	s_cbranch_vccnz .LBB0_72
	s_add_i32 s6, s33, s30
	s_cmpk_lt_i32 s6, 0x1000
	s_cselect_b64 s[26:27], -1, 0
	s_and_b64 s[0:1], s[26:27], exec
	s_cselect_b32 s53, s6, s52
	s_cmpk_gt_i32 s53, 0xbff
	s_mov_b64 s[34:35], -1
	s_cbranch_scc0 .LBB0_107
	s_cmpk_gt_u32 s53, 0xfff
	s_cbranch_scc0 .LBB0_101
	s_cmp_gt_u32 s53, 0x10fff
	s_mov_b64 s[30:31], -1
	s_cbranch_scc0 .LBB0_94
	s_add_i32 s0, s53, 0xfffef000
	s_lshr_b32 s6, s0, 10
	s_lshl_b64 s[0:1], s[6:7], 24
	v_readlane_b32 s56, v246, 0
	v_readlane_b32 s57, v246, 1
	s_add_u32 s0, s56, s0
	s_addc_u32 s1, s57, s1
	s_lshl_b32 s8, s53, 6
	s_and_b32 s16, s8, 0x7c0
	s_lshl_b32 s8, s16, 13
	s_add_u32 s8, s0, s8
	s_addc_u32 s9, s1, 0
	s_lshl_b32 s0, s53, 1
	s_and_b32 s0, s0, 0x7c0
	s_lshl_b32 s14, s0, 2
	s_add_u32 s28, s8, s14
	s_addc_u32 s29, s9, 0
	s_lshl_b64 s[8:9], s[6:7], 23
	s_add_u32 s24, s3, s8
	v_readlane_b32 s58, v246, 2
	v_readlane_b32 s59, v246, 3
	v_readlane_b32 s60, v246, 4
	v_readlane_b32 s61, v246, 5
	v_readlane_b32 s62, v246, 6
	v_readlane_b32 s63, v246, 7
	s_mov_b32 s17, s7
	s_mov_b32 s1, s7
	s_addc_u32 s25, s5, s9
	s_mov_b64 s[30:31], 0

; __device__ __forceinline__ void tr_load(const TrItem& t, f32x4 (&ra)[8], f32x4 (&rb)[8], int lane) {
;     const int q = lane >> 4, n4 = lane & 15;
;     const float* p = t.src + (size_t)(2 * q) * t.N + 4 * n4;
; #pragma unroll
;     for (int i = 0; i < 8; ++i) { ra[i] = __builtin_nontemporal_load((const f32x4*)(p + (size_t)(8 * i) * t.N)); rb[i] = __builtin_nontemporal_load((const f32x4*)(p + (size_t)(8 * i + 1) * t.N)); }
; }
; __device__ __forceinline__ void conv_items(const Args& a, LAS unsigned char* lds, int it0, int it1, int vcu, int G, int lane, int wave) {
;     ...
;         it = nx; nx = it + NGW; has = nx < it1;
;         cur = tr_decode(a, has ? nx : it);
;         if (has) tr_load(cur, ra, rb, lane);
;         tr_store(nxt, na, nb_, scr, lane);
.LBB0_109:
	v_mul_u32_u24_e32 v2, s30, v131
	v_lshlrev_b32_e32 v2, 2, v2
	v_mov_b32_e32 v3, v145
	v_lshl_add_u64 v[2:3], s[28:29], 0, v[2:3]
	v_lshlrev_b32_e32 v4, 2, v142
	v_mov_b32_e32 v5, v145
	v_lshl_add_u64 v[2:3], v[2:3], 0, v[4:5]
	s_lshl_b64 s[8:9], s[30:31], 2
	v_lshl_add_u64 v[10:11], v[2:3], 0, s[8:9]
	s_mul_i32 s6, s30, 28
	global_load_dwordx4 v[2:5], v[2:3], off nt
	s_nop 0
	global_load_dwordx4 v[6:9], v[10:11], off nt
	v_lshl_add_u64 v[10:11], v[10:11], 0, s[6:7]
	v_lshl_add_u64 v[18:19], v[10:11], 0, s[8:9]
	global_load_dwordx4 v[10:13], v[10:11], off nt
	s_nop 0
	global_load_dwordx4 v[14:17], v[18:19], off nt
	v_lshl_add_u64 v[18:19], v[18:19], 0, s[6:7]
	v_lshl_add_u64 v[26:27], v[18:19], 0, s[8:9]
	global_load_dwordx4 v[18:21], v[18:19], off nt
	s_nop 0
	global_load_dwordx4 v[22:25], v[26:27], off nt
	v_lshl_add_u64 v[26:27], v[26:27], 0, s[6:7]
	v_lshl_add_u64 v[34:35], v[26:27], 0, s[8:9]
	v_lshl_add_u64 v[38:39], v[34:35], 0, s[6:7]
	v_lshl_add_u64 v[42:43], v[38:39], 0, s[8:9]
	v_lshl_add_u64 v[46:47], v[42:43], 0, s[6:7]
	v_lshl_add_u64 v[50:51], v[46:47], 0, s[8:9]
	v_lshl_add_u64 v[54:55], v[50:51], 0, s[6:7]
	v_lshl_add_u64 v[58:59], v[54:55], 0, s[8:9]
	v_lshl_add_u64 v[62:63], v[58:59], 0, s[6:7]
	global_load_dwordx4 v[26:29], v[26:27], off nt
	s_nop 0
	global_load_dwordx4 v[30:33], v[34:35], off nt
	s_nop 0
	global_load_dwordx4 v[34:37], v[38:39], off nt
	s_nop 0
	global_load_dwordx4 v[38:41], v[42:43], off nt
	s_nop 0
	global_load_dwordx4 v[42:45], v[46:47], off nt
	s_nop 0
	global_load_dwordx4 v[46:49], v[50:51], off nt
	s_nop 0
	global_load_dwordx4 v[50:53], v[54:55], off nt
	s_nop 0
	global_load_dwordx4 v[54:57], v[58:59], off nt
	s_nop 0
	global_load_dwordx4 v[58:61], v[62:63], off nt
	v_lshl_add_u64 v[62:63], v[62:63], 0, s[8:9]
	global_load_dwordx4 v[62:65], v[62:63], off nt
	s_waitcnt vmcnt(24)
	s_branch .LBB0_71

; #define LAS __attribute__((address_space(3)))
; __device__ __forceinline__ TrItem tr_decode(const Args& a, int it) {
;     unsigned char* ws = a.ws;
;     constexpr int T_IN = 32 * (INCOLS / 64), T_OUT = 32 * (DM / 64), T_GU1 = 32 * (4096 / 64), T_DN1 = 32 * (DM / 64);
;     TrItem t; int r = it;
;     if (r < T_IN) { const int kb = r & 31, nb = r >> 5; t.N = INCOLS; t.src = a.in[I_WIN] + (size_t)(64 * kb) * INCOLS + 64 * nb; t.dst = (bf16*)(ws + WS_WIN) + (size_t)(64 * nb) * DM + 64 * kb; return t; } r -= T_IN;
;     if (r < T_OUT) { const int kb = r & 31, nb = r >> 5; t.N = DM; t.src = a.in[I_WOUT] + (size_t)(64 * kb) * DM + 64 * nb; t.dst = (bf16*)(ws + WS_WOUT) + (size_t)(64 * nb) * DM + 64 * kb; return t; } r -= T_OUT;
;     if (r < NEXP * T_GU1) { const int e = r / T_GU1, q = r % T_GU1, kb = q & 31, nb = q >> 5, n0 = 64 * nb;
;         const int drow0 = n0 < 2048 ? (n0 >> 7) * 256 + (n0 & 127) : ((n0 - 2048) >> 7) * 256 + 128 + ((n0 - 2048) & 127);
;         t.N = 4096; t.src = a.in[I_WGU] + (size_t)e * DM * 4096 + (size_t)(64 * kb) * 4096 + n0; t.dst = (bf16*)(ws + WS_WGU) + (size_t)e * 4096 * DM + (size_t)drow0 * DM + 64 * kb; return t; } r -= NEXP * T_GU1;
;     { const int e = r / T_DN1, q = r % T_DN1, kb = q & 31, nb = q >> 5;
;         t.N = DM; t.src = a.in[I_WDN] + (size_t)e * DM * DM + (size_t)(64 * kb) * DM + 64 * nb; t.dst = (bf16*)(ws + WS_WDN) + (size_t)e * DM * DM + (size_t)(64 * nb) * DM + 64 * kb; return t; }
; }
; __device__ __forceinline__ void tr_load(const TrItem& t, f32x4 (&ra)[8], f32x4 (&rb)[8], int lane) {
;     const int q = lane >> 4, n4 = lane & 15;
;     const float* p = t.src + (size_t)(2 * q) * t.N + 4 * n4;
; #pragma unroll
;     for (int i = 0; i < 8; ++i) { ra[i] = __builtin_nontemporal_load((const f32x4*)(p + (size_t)(8 * i) * t.N)); rb[i] = __builtin_nontemporal_load((const f32x4*)(p + (size_t)(8 * i + 1) * t.N)); }
; }
; __device__ __forceinline__ void conv_items(const Args& a, LAS unsigned char* lds, int it0, int it1, int vcu, int G, int lane, int wave) {
;     LAS unsigned* scr = (LAS unsigned*)(lds + wave * 16384);
;     const int gw = vcu * NWAVES + wave, NGW = G * NWAVES;
;     f32x4 ra[8], rb[8], na[8], nb_[8];
;     int it = it0 + gw;
;     if (it >= it1) return;
;     TrItem cur = tr_decode(a, it);
;     tr_load(cur, ra, rb, lane);
.LBB0_181:
	v_readlane_b32 s2, v246, 33
	s_lshl_b32 s2, s2, 14
	v_readlane_b32 s9, v246, 11
	v_lshrrev_b32_e32 v66, 3, v194
	s_add_i32 s8, s2, 0
	s_lshl_b32 s17, s9, 3
	s_lshl_b64 s[4:5], s[4:5], 12
	v_and_b32_e32 v1, 6, v66
	s_add_u32 s2, s12, s4
	s_waitcnt vmcnt(23) lgkmcnt(0)
	v_mul_u32_u24_e32 v2, s20, v1
	v_lshlrev_b32_e32 v67, 2, v194
	s_addc_u32 s4, s13, s5
	s_lshl_b64 s[0:1], s[0:1], 1
	v_lshlrev_b32_e32 v130, 2, v2
	v_mov_b32_e32 v131, 0
	v_and_b32_e32 v132, 60, v67
	s_add_u32 s12, s2, s0
	v_lshl_add_u64 v[2:3], s[18:19], 0, v[130:131]
	v_lshlrev_b32_e32 v130, 2, v132
	s_addc_u32 s13, s4, s1
	v_lshl_add_u64 v[2:3], v[2:3], 0, v[130:131]
	s_lshl_b64 s[0:1], s[20:21], 2
	s_mov_b32 s3, 0
	s_waitcnt vmcnt(21)
	v_lshl_add_u64 v[10:11], v[2:3], 0, s[0:1]
	s_mul_i32 s2, s20, 28
	global_load_dwordx4 v[2:5], v[2:3], off nt
	s_nop 0
	global_load_dwordx4 v[6:9], v[10:11], off nt
	v_lshl_add_u64 v[10:11], v[10:11], 0, s[2:3]
	s_waitcnt vmcnt(21)
	v_lshl_add_u64 v[18:19], v[10:11], 0, s[0:1]
	global_load_dwordx4 v[10:13], v[10:11], off nt
	s_nop 0
	global_load_dwordx4 v[14:17], v[18:19], off nt
	v_lshl_add_u64 v[18:19], v[18:19], 0, s[2:3]
	s_waitcnt vmcnt(21)
	v_lshl_add_u64 v[26:27], v[18:19], 0, s[0:1]
	global_load_dwordx4 v[18:21], v[18:19], off nt
	s_nop 0
	global_load_dwordx4 v[22:25], v[26:27], off nt
	v_lshl_add_u64 v[26:27], v[26:27], 0, s[2:3]
	s_waitcnt vmcnt(21)
	v_lshl_add_u64 v[34:35], v[26:27], 0, s[0:1]
	s_waitcnt vmcnt(20)
	v_lshl_add_u64 v[38:39], v[34:35], 0, s[2:3]
	s_waitcnt vmcnt(19)
	v_lshl_add_u64 v[42:43], v[38:39], 0, s[0:1]
	s_waitcnt vmcnt(18)
	v_lshl_add_u64 v[46:47], v[42:43], 0, s[2:3]
	s_waitcnt vmcnt(17)
	v_lshl_add_u64 v[50:51], v[46:47], 0, s[0:1]
	s_waitcnt vmcnt(16)
	v_lshl_add_u64 v[54:55], v[50:51], 0, s[2:3]
	s_waitcnt vmcnt(15)
	v_lshl_add_u64 v[58:59], v[54:55], 0, s[0:1]
	s_waitcnt vmcnt(14)
	v_lshl_add_u64 v[62:63], v[58:59], 0, s[2:3]
	global_load_dwordx4 v[26:29], v[26:27], off nt
	s_nop 0
	global_load_dwordx4 v[30:33], v[34:35], off nt
	v_lshlrev_b32_e32 v77, 3, v0
	global_load_dwordx4 v[34:37], v[38:39], off nt
	v_bitop3_b32 v78, v66, 28, v67 bitop3:0x48
	global_load_dwordx4 v[38:41], v[42:43], off nt
	v_and_b32_e32 v134, 56, v77
	global_load_dwordx4 v[42:45], v[46:47], off nt
	v_lshlrev_b32_e32 v77, 7, v66
	global_load_dwordx4 v[46:49], v[50:51], off nt
	v_lshlrev_b32_e32 v78, 2, v78
	global_load_dwordx4 v[50:53], v[54:55], off nt
	v_add3_u32 v133, s8, v77, v78
	global_load_dwordx4 v[54:57], v[58:59], off nt
	v_or_b32_e32 v77, 8, v66
	global_load_dwordx4 v[58:61], v[62:63], off nt
	v_lshl_add_u64 v[62:63], v[62:63], 0, s[0:1]
	global_load_dwordx4 v[62:65], v[62:63], off nt
	v_bitop3_b32 v80, v77, 28, v67 bitop3:0x48
	v_lshlrev_b32_e32 v79, 7, v77
	v_lshlrev_b32_e32 v80, 2, v80
	v_lshlrev_b32_e32 v138, 12, v77
	v_or_b32_e32 v77, 16, v66
	v_add3_u32 v135, s8, v79, v80
	v_bitop3_b32 v80, v77, 28, v67 bitop3:0x48
	v_lshlrev_b32_e32 v79, 7, v77
	v_lshlrev_b32_e32 v80, 2, v80
	v_lshlrev_b32_e32 v140, 12, v77
	v_or_b32_e32 v77, 24, v66
	v_add3_u32 v152, s8, v79, v80
	v_bitop3_b32 v80, v77, 28, v67 bitop3:0x48
	v_lshlrev_b32_e32 v79, 7, v77
	v_lshlrev_b32_e32 v80, 2, v80
	v_lshlrev_b32_e32 v142, 12, v77
	v_or_b32_e32 v77, 32, v66
	v_lshlrev_b32_e32 v68, 9, v0
	v_lshrrev_b32_e32 v69, 2, v194
	v_add3_u32 v153, s8, v79, v80
	v_lshlrev_b32_e32 v79, 7, v77
	v_lshlrev_b32_e32 v144, 12, v77
	v_or_b32_e32 v77, 40, v66
	s_add_u32 s33, s92, 0x70800000
	v_and_b32_e32 v68, 0x1e00, v68
	v_and_b32_e32 v69, 12, v69
	v_add3_u32 v154, s8, v79, v78
	v_bitop3_b32 v79, v77, 28, v67 bitop3:0x48
	s_addc_u32 s44, s93, 0
	v_add3_u32 v68, s8, v68, v69
	v_lshlrev_b32_e32 v69, 4, v0
	v_mov_b32_e32 v71, 0x70
	s_movk_i32 s1, 0x50
	v_lshlrev_b32_e32 v136, 12, v66
	v_lshlrev_b32_e32 v78, 7, v77
	v_lshlrev_b32_e32 v79, 2, v79
	v_lshlrev_b32_e32 v146, 12, v77
	v_or_b32_e32 v77, 48, v66
	v_or_b32_e32 v66, 56, v66
	s_add_u32 s45, s92, 0x50800000
	s_movk_i32 s0, 0x70
	v_bitop3_b32 v76, v69, s1, v71 bitop3:0x6c
	s_movk_i32 s1, 0x60
	v_add3_u32 v155, s8, v78, v79
	v_bitop3_b32 v79, v77, 28, v67 bitop3:0x48
	v_bitop3_b32 v67, v66, 28, v67 bitop3:0x48
	s_addc_u32 s52, s93, 0
	v_and_b32_e32 v70, 0x70, v69
	v_bitop3_b32 v72, v69, 16, v71 bitop3:0x6c
	v_bitop3_b32 v73, v69, 32, v71 bitop3:0x6c
	v_bitop3_b32 v74, v69, 48, v71 bitop3:0x6c
	v_bitop3_b32 v75, v69, 64, v71 bitop3:0x6c
	v_bitop3_b32 v71, v69, s1, v71 bitop3:0x6c
	v_bitop3_b32 v69, v69, s0, v69 bitop3:0xc
	v_lshlrev_b32_e32 v78, 7, v77
	v_lshlrev_b32_e32 v79, 2, v79
	v_lshlrev_b32_e32 v148, 12, v77
	v_lshlrev_b32_e32 v77, 7, v66
	v_lshlrev_b32_e32 v67, 2, v67
	s_add_u32 s4, s92, 0x1a00000
	v_mov_b32_e32 v137, v131
	v_mov_b32_e32 v139, v131
	v_mov_b32_e32 v141, v131
	v_mov_b32_e32 v143, v131
	v_mov_b32_e32 v145, v131
	v_mov_b32_e32 v147, v131
	v_add3_u32 v156, s8, v78, v79
	v_mov_b32_e32 v149, v131
	v_add3_u32 v157, s8, v77, v67
	v_lshlrev_b32_e32 v150, 12, v66
	v_mov_b32_e32 v151, v131
	s_addc_u32 s5, s93, 0
	s_lshl_b32 s53, s9, 4
	v_add_u32_e32 v158, v68, v70
	v_add_u32_e32 v159, v68, v72
	v_add_u32_e32 v160, v68, v73
	v_add_u32_e32 v161, v68, v74
	v_add_u32_e32 v162, v68, v75
	v_add_u32_e32 v163, v68, v76
	v_add_u32_e32 v164, v68, v71
	v_add_u32_e32 v165, v68, v69
	s_branch .LBB0_184
; #define LAS __attribute__((address_space(3)))
; #define LDS_WAIT() asm volatile("s_waitcnt lgkmcnt(0)" ::: "memory")
; __device__ __forceinline__ unsigned cvt2bf(float lo, float hi) { const f32x2_t v = {lo, hi}; const bf16x2_t r = __builtin_convertvector(v, bf16x2_t); return __builtin_bit_cast(unsigned, r); }
; __device__ __forceinline__ void tr_store(const TrItem& t, const f32x4 (&ra)[8], const f32x4 (&rb)[8], LAS unsigned* scr, int lane) {
;     const int q = lane >> 4, n4 = lane & 15;
; #pragma unroll
;     for (int i = 0; i < 8; ++i)
; #pragma unroll
;         for (int j = 0; j < 4; ++j) scr[(4 * n4 + j) * 32 + ((i ^ (n4 & 7)) << 2) + q] = cvt2bf(ra[i][j], rb[i][j]);
;     LDS_WAIT(); asm volatile("" ::: "memory");
;     const int nr = lane >> 3, ch = lane & 7;
; #pragma unroll
;     for (int i = 0; i < 8; ++i) { const int n = nr + 8 * i; const v4u v = *(const LAS v4u*)(scr + n * 32 + ((ch ^ ((n >> 2) & 7)) << 2));
;         __builtin_nontemporal_store(v, (v4u*)(t.dst + (size_t)n * DM + 8 * ch)); }
;     LDS_WAIT(); asm volatile("" ::: "memory");
; }
; __device__ __forceinline__ void conv_items(const Args& a, LAS unsigned char* lds, int it0, int it1, int vcu, int G, int lane, int wave) {
;     ...
;         it = nx; nx = it + NGW; has = nx < it1;
.Lcvw_1:
	s_waitcnt vmcnt(8)
.LBB0_182:
	v_cvt_pk_bf16_f32 v166, v66, v74
	v_cvt_pk_bf16_f32 v167, v67, v75
	ds_write2_b32 v158, v166, v167 offset1:32
	v_cvt_pk_bf16_f32 v166, v68, v76
	v_cvt_pk_bf16_f32 v167, v69, v77
	ds_write2_b32 v158, v166, v167 offset0:64 offset1:96
	v_cvt_pk_bf16_f32 v166, v70, v86
	v_cvt_pk_bf16_f32 v167, v71, v87
	ds_write2_b32 v159, v166, v167 offset1:32
	v_cvt_pk_bf16_f32 v166, v72, v88
	v_cvt_pk_bf16_f32 v167, v73, v89
	ds_write2_b32 v159, v166, v167 offset0:64 offset1:96
	v_cvt_pk_bf16_f32 v166, v78, v98
	v_cvt_pk_bf16_f32 v167, v79, v99
	ds_write2_b32 v160, v166, v167 offset1:32
	v_cvt_pk_bf16_f32 v166, v80, v100
	v_cvt_pk_bf16_f32 v167, v81, v101
	ds_write2_b32 v160, v166, v167 offset0:64 offset1:96
	v_cvt_pk_bf16_f32 v166, v82, v106
	v_cvt_pk_bf16_f32 v167, v83, v107
	ds_write2_b32 v161, v166, v167 offset1:32
	v_cvt_pk_bf16_f32 v166, v84, v108
	v_cvt_pk_bf16_f32 v167, v85, v109
	ds_write2_b32 v161, v166, v167 offset0:64 offset1:96
	v_cvt_pk_bf16_f32 v166, v90, v114
	v_cvt_pk_bf16_f32 v167, v91, v115
	ds_write2_b32 v162, v166, v167 offset1:32
	v_cvt_pk_bf16_f32 v166, v92, v116
	v_cvt_pk_bf16_f32 v167, v93, v117
	ds_write2_b32 v162, v166, v167 offset0:64 offset1:96
	v_cvt_pk_bf16_f32 v166, v94, v118
	v_cvt_pk_bf16_f32 v167, v95, v119
	ds_write2_b32 v163, v166, v167 offset1:32
	v_cvt_pk_bf16_f32 v166, v96, v120
	v_cvt_pk_bf16_f32 v167, v97, v121
	ds_write2_b32 v163, v166, v167 offset0:64 offset1:96
	v_cvt_pk_bf16_f32 v166, v102, v122
	v_cvt_pk_bf16_f32 v167, v103, v123
	s_lshl_b64 s[0:1], s[0:1], 12
	ds_write2_b32 v164, v166, v167 offset1:32
	v_cvt_pk_bf16_f32 v166, v104, v124
	v_cvt_pk_bf16_f32 v167, v105, v125
	s_add_u32 s2, s24, s0
	ds_write2_b32 v164, v166, v167 offset0:64 offset1:96
	v_cvt_pk_bf16_f32 v166, v110, v126
	v_cvt_pk_bf16_f32 v167, v111, v127
	s_addc_u32 s8, s25, s1
	s_lshl_b64 s[0:1], s[12:13], 1
	ds_write2_b32 v165, v166, v167 offset1:32
	v_cvt_pk_bf16_f32 v166, v112, v128
	v_cvt_pk_bf16_f32 v167, v113, v129
	s_add_u32 s12, s2, s0
	ds_write2_b32 v165, v166, v167 offset0:64 offset1:96
	s_addc_u32 s13, s8, s1
	s_add_i32 s30, s54, s17
	s_lshl_b64 s[0:1], s[18:19], 12
	s_waitcnt lgkmcnt(0)
	s_add_u32 s2, s22, s0
	s_addc_u32 s8, s23, s1
	s_lshl_b64 s[0:1], s[20:21], 1
	ds_read_b128 v[166:169], v133
	ds_read_b128 v[170:173], v135
	s_add_u32 s0, s2, s0
	s_addc_u32 s1, s8, s1
	v_lshl_add_u64 v[178:179], s[0:1], 0, v[130:131]
	v_lshl_add_u64 v[174:175], v[178:179], 0, v[136:137]
	s_waitcnt lgkmcnt(1)
	global_store_dwordx4 v[174:175], v[166:169], off nt
	ds_read_b128 v[166:169], v152
	v_lshl_add_u64 v[174:175], v[178:179], 0, v[138:139]
	s_waitcnt lgkmcnt(1)
	global_store_dwordx4 v[174:175], v[170:173], off nt
	ds_read_b128 v[170:173], v153
	v_lshl_add_u64 v[174:175], v[178:179], 0, v[140:141]
	s_waitcnt lgkmcnt(1)
	global_store_dwordx4 v[174:175], v[166:169], off nt
	ds_read_b128 v[166:169], v154
	v_lshl_add_u64 v[174:175], v[178:179], 0, v[142:143]
	s_waitcnt lgkmcnt(1)
	global_store_dwordx4 v[174:175], v[170:173], off nt
	v_lshl_add_u64 v[174:175], v[178:179], 0, v[144:145]
	ds_read_b128 v[170:173], v155
	s_waitcnt lgkmcnt(1)
	global_store_dwordx4 v[174:175], v[166:169], off nt
	ds_read_b128 v[166:169], v156
	ds_read_b128 v[174:177], v157
	v_lshl_add_u64 v[180:181], v[178:179], 0, v[146:147]
	s_waitcnt lgkmcnt(2)
	global_store_dwordx4 v[180:181], v[170:173], off nt
	s_cmp_gt_i32 s30, 0x8332
	s_cselect_b64 s[0:1], -1, 0
	v_lshl_add_u64 v[170:171], v[178:179], 0, v[148:149]
	s_waitcnt lgkmcnt(1)
	global_store_dwordx4 v[170:171], v[166:169], off nt
	s_nop 1
	v_lshl_add_u64 v[166:167], v[178:179], 0, v[150:151]
	s_waitcnt lgkmcnt(0)
	global_store_dwordx4 v[166:167], v[174:177], off nt
	s_waitcnt lgkmcnt(0)

; #define LAS __attribute__((address_space(3)))
; __device__ __forceinline__ unsigned cvt2bf(float lo, float hi) { const f32x2_t v = {lo, hi}; const bf16x2_t r = __builtin_convertvector(v, bf16x2_t); return __builtin_bit_cast(unsigned, r); }
; __device__ __forceinline__ void tr_load(const TrItem& t, f32x4 (&ra)[8], f32x4 (&rb)[8], int lane) {
;     const int q = lane >> 4, n4 = lane & 15;
;     const float* p = t.src + (size_t)(2 * q) * t.N + 4 * n4;
; #pragma unroll
;     for (int i = 0; i < 8; ++i) { ra[i] = __builtin_nontemporal_load((const f32x4*)(p + (size_t)(8 * i) * t.N)); rb[i] = __builtin_nontemporal_load((const f32x4*)(p + (size_t)(8 * i + 1) * t.N)); }
; }
; __device__ __forceinline__ void tr_store(const TrItem& t, const f32x4 (&ra)[8], const f32x4 (&rb)[8], LAS unsigned* scr, int lane) {
;     const int q = lane >> 4, n4 = lane & 15;
; #pragma unroll
;     for (int i = 0; i < 8; ++i)
; #pragma unroll
;         for (int j = 0; j < 4; ++j) scr[(4 * n4 + j) * 32 + ((i ^ (n4 & 7)) << 2) + q] = cvt2bf(ra[i][j], rb[i][j]);
; __device__ __forceinline__ void conv_items(const Args& a, LAS unsigned char* lds, int it0, int it1, int vcu, int G, int lane, int wave) {
;     ...
;         int nx = it + NGW; bool has = nx < it1;
;         TrItem nxt = tr_decode(a, has ? nx : it);
;         if (has) tr_load(nxt, na, nb_, lane);
;         tr_store(cur, ra, rb, scr, lane);
.LBB0_199:
	v_mul_u32_u24_e32 v66, s28, v1
	v_lshlrev_b32_e32 v130, 2, v66
	v_lshl_add_u64 v[66:67], s[26:27], 0, v[130:131]
	v_lshlrev_b32_e32 v130, 2, v132
	v_lshl_add_u64 v[66:67], v[66:67], 0, v[130:131]
	s_lshl_b64 s[8:9], s[28:29], 2
	v_lshl_add_u64 v[70:71], v[66:67], 0, s[8:9]
	s_mul_i32 s2, s28, 28
	global_load_dwordx4 v[66:69], v[66:67], off nt
	s_nop 0
	global_load_dwordx4 v[74:77], v[70:71], off nt
	v_lshl_add_u64 v[70:71], v[70:71], 0, s[2:3]
	v_lshl_add_u64 v[78:79], v[70:71], 0, s[8:9]
	global_load_dwordx4 v[70:73], v[70:71], off nt
	s_nop 0
	global_load_dwordx4 v[86:89], v[78:79], off nt
	v_lshl_add_u64 v[78:79], v[78:79], 0, s[2:3]
	v_lshl_add_u64 v[82:83], v[78:79], 0, s[8:9]
	global_load_dwordx4 v[78:81], v[78:79], off nt
	s_nop 0
	global_load_dwordx4 v[98:101], v[82:83], off nt
	v_lshl_add_u64 v[82:83], v[82:83], 0, s[2:3]
	v_lshl_add_u64 v[90:91], v[82:83], 0, s[8:9]
	v_lshl_add_u64 v[94:95], v[90:91], 0, s[2:3]
	global_load_dwordx4 v[82:85], v[82:83], off nt
	s_nop 0
	global_load_dwordx4 v[106:109], v[90:91], off nt
	s_nop 0
	global_load_dwordx4 v[90:93], v[94:95], off nt
	v_lshl_add_u64 v[94:95], v[94:95], 0, s[8:9]
	v_lshl_add_u64 v[102:103], v[94:95], 0, s[2:3]
	global_load_dwordx4 v[114:117], v[94:95], off nt
	s_nop 0
	global_load_dwordx4 v[94:97], v[102:103], off nt
	v_lshl_add_u64 v[102:103], v[102:103], 0, s[8:9]
	v_lshl_add_u64 v[110:111], v[102:103], 0, s[2:3]
	global_load_dwordx4 v[118:121], v[102:103], off nt
	s_nop 0
	global_load_dwordx4 v[102:105], v[110:111], off nt
	v_lshl_add_u64 v[110:111], v[110:111], 0, s[8:9]
	v_lshl_add_u64 v[126:127], v[110:111], 0, s[2:3]
	global_load_dwordx4 v[122:125], v[110:111], off nt
	s_nop 0
	global_load_dwordx4 v[110:113], v[126:127], off nt
	v_lshl_add_u64 v[126:127], v[126:127], 0, s[8:9]
	global_load_dwordx4 v[126:129], v[126:127], off nt
	s_waitcnt vmcnt(30)
	v_cvt_pk_bf16_f32 v130, v2, v6
	v_cvt_pk_bf16_f32 v166, v3, v7
	ds_write2_b32 v158, v130, v166 offset1:32
	v_cvt_pk_bf16_f32 v130, v4, v8
	v_cvt_pk_bf16_f32 v166, v5, v9
	ds_write2_b32 v158, v130, v166 offset0:64 offset1:96
	s_waitcnt vmcnt(28)
	v_cvt_pk_bf16_f32 v130, v10, v14
	v_cvt_pk_bf16_f32 v166, v11, v15
	ds_write2_b32 v159, v130, v166 offset1:32
	v_cvt_pk_bf16_f32 v130, v12, v16
	v_cvt_pk_bf16_f32 v166, v13, v17
	ds_write2_b32 v159, v130, v166 offset0:64 offset1:96
	s_waitcnt vmcnt(26)
	v_cvt_pk_bf16_f32 v130, v18, v22
	v_cvt_pk_bf16_f32 v166, v19, v23
	ds_write2_b32 v160, v130, v166 offset1:32
	v_cvt_pk_bf16_f32 v130, v20, v24
	v_cvt_pk_bf16_f32 v166, v21, v25
	ds_write2_b32 v160, v130, v166 offset0:64 offset1:96
	s_waitcnt vmcnt(24)
	v_cvt_pk_bf16_f32 v130, v26, v30
	v_cvt_pk_bf16_f32 v166, v27, v31
	ds_write2_b32 v161, v130, v166 offset1:32
	v_cvt_pk_bf16_f32 v130, v28, v32
	v_cvt_pk_bf16_f32 v166, v29, v33
	ds_write2_b32 v161, v130, v166 offset0:64 offset1:96
	s_waitcnt vmcnt(22)
	v_cvt_pk_bf16_f32 v130, v34, v38
	v_cvt_pk_bf16_f32 v166, v35, v39
	ds_write2_b32 v162, v130, v166 offset1:32
	v_cvt_pk_bf16_f32 v130, v36, v40
	v_cvt_pk_bf16_f32 v166, v37, v41
	ds_write2_b32 v162, v130, v166 offset0:64 offset1:96
	s_waitcnt vmcnt(20)
	v_cvt_pk_bf16_f32 v130, v42, v46
	v_cvt_pk_bf16_f32 v166, v43, v47
	ds_write2_b32 v163, v130, v166 offset1:32
	v_cvt_pk_bf16_f32 v130, v44, v48
	v_cvt_pk_bf16_f32 v166, v45, v49
	ds_write2_b32 v163, v130, v166 offset0:64 offset1:96
	s_waitcnt vmcnt(18)
	v_cvt_pk_bf16_f32 v130, v50, v54
	v_cvt_pk_bf16_f32 v166, v51, v55
	ds_write2_b32 v164, v130, v166 offset1:32
	v_cvt_pk_bf16_f32 v130, v52, v56
	v_cvt_pk_bf16_f32 v166, v53, v57
	ds_write2_b32 v164, v130, v166 offset0:64 offset1:96
	s_waitcnt vmcnt(16)
	v_cvt_pk_bf16_f32 v130, v58, v62
	v_cvt_pk_bf16_f32 v166, v59, v63
	ds_write2_b32 v165, v130, v166 offset1:32
	v_cvt_pk_bf16_f32 v130, v60, v64
	v_cvt_pk_bf16_f32 v166, v61, v65
	ds_write2_b32 v165, v130, v166 offset0:64 offset1:96
	s_branch .Lcvj_1

; #define LAS __attribute__((address_space(3)))
; #define LDS_WAIT() asm volatile("s_waitcnt lgkmcnt(0)" ::: "memory")
; __device__ __forceinline__ TrItem tr_decode(const Args& a, int it) {
;     ...
;     if (r < T_IN) { const int kb = r & 31, nb = r >> 5; t.N = INCOLS; t.src = a.in[I_WIN] + (size_t)(64 * kb) * INCOLS + 64 * nb; t.dst = (bf16*)(ws + WS_WIN) + (size_t)(64 * nb) * DM + 64 * kb; return t; } r -= T_IN;
;     if (r < T_OUT) { const int kb = r & 31, nb = r >> 5; t.N = DM; t.src = a.in[I_WOUT] + (size_t)(64 * kb) * DM + 64 * nb; t.dst = (bf16*)(ws + WS_WOUT) + (size_t)(64 * nb) * DM + 64 * kb; return t; } r -= T_OUT;
;     if (r < NEXP * T_GU1) { const int e = r / T_GU1, q = r % T_GU1, kb = q & 31, nb = q >> 5, n0 = 64 * nb;
;         const int drow0 = n0 < 2048 ? (n0 >> 7) * 256 + (n0 & 127) : ((n0 - 2048) >> 7) * 256 + 128 + ((n0 - 2048) & 127);
;         t.N = 4096; t.src = a.in[I_WGU] + (size_t)e * DM * 4096 + (size_t)(64 * kb) * 4096 + n0; t.dst = (bf16*)(ws + WS_WGU) + (size_t)e * 4096 * DM + (size_t)drow0 * DM + 64 * kb; return t; } r -= NEXP * T_GU1;
;     { const int e = r / T_DN1, q = r % T_DN1, kb = q & 31, nb = q >> 5;
;         t.N = DM; t.src = a.in[I_WDN] + (size_t)e * DM * DM + (size_t)(64 * kb) * DM + 64 * nb; t.dst = (bf16*)(ws + WS_WDN) + (size_t)e * DM * DM + (size_t)(64 * nb) * DM + 64 * kb; return t; }
; __device__ __forceinline__ void tr_store(const TrItem& t, const f32x4 (&ra)[8], const f32x4 (&rb)[8], LAS unsigned* scr, int lane) {
;     ...
;     LDS_WAIT(); asm volatile("" ::: "memory");
;     const int nr = lane >> 3, ch = lane & 7;
; #pragma unroll
;     for (int i = 0; i < 8; ++i) { const int n = nr + 8 * i; const v4u v = *(const LAS v4u*)(scr + n * 32 + ((ch ^ ((n >> 2) & 7)) << 2));
;         __builtin_nontemporal_store(v, (v4u*)(t.dst + (size_t)n * DM + 8 * ch)); }
;     LDS_WAIT(); asm volatile("" ::: "memory");
; }
; __device__ __forceinline__ void conv_items(const Args& a, LAS unsigned char* lds, int it0, int it1, int vcu, int G, int lane, int wave) {
;     ...
;         if (!has) break;
;         it = nx; nx = it + NGW; has = nx < it1;
;         cur = tr_decode(a, has ? nx : it);
.Lcvj_1:
	s_waitcnt lgkmcnt(0)
	ds_read_b128 v[166:169], v133
	ds_read_b128 v[170:173], v135
	v_lshlrev_b32_e32 v130, 1, v134
	v_lshl_add_u64 v[178:179], s[12:13], 0, v[130:131]
	v_lshl_add_u64 v[174:175], v[178:179], 0, v[136:137]
	s_waitcnt lgkmcnt(1)
	global_store_dwordx4 v[174:175], v[166:169], off nt
	ds_read_b128 v[166:169], v152
	v_lshl_add_u64 v[174:175], v[178:179], 0, v[138:139]
	s_waitcnt lgkmcnt(1)
	global_store_dwordx4 v[174:175], v[170:173], off nt
	ds_read_b128 v[170:173], v153
	v_lshl_add_u64 v[174:175], v[178:179], 0, v[140:141]
	s_waitcnt lgkmcnt(1)
	global_store_dwordx4 v[174:175], v[166:169], off nt
	ds_read_b128 v[166:169], v154
	v_lshl_add_u64 v[174:175], v[178:179], 0, v[142:143]
	s_waitcnt lgkmcnt(1)
	global_store_dwordx4 v[174:175], v[170:173], off nt
	v_lshl_add_u64 v[174:175], v[178:179], 0, v[144:145]
	ds_read_b128 v[170:173], v155
	s_waitcnt lgkmcnt(1)
	global_store_dwordx4 v[174:175], v[166:169], off nt
	ds_read_b128 v[166:169], v156
	ds_read_b128 v[174:177], v157
	v_lshl_add_u64 v[180:181], v[178:179], 0, v[146:147]
	s_waitcnt lgkmcnt(2)
	global_store_dwordx4 v[180:181], v[170:173], off nt
	s_and_b64 vcc, exec, s[0:1]
	s_mov_b64 s[0:1], -1
	v_lshl_add_u64 v[170:171], v[178:179], 0, v[148:149]
	s_waitcnt lgkmcnt(1)
	global_store_dwordx4 v[170:171], v[166:169], off nt
	s_nop 1
	v_lshl_add_u64 v[166:167], v[178:179], 0, v[150:151]
	s_waitcnt lgkmcnt(0)
	global_store_dwordx4 v[166:167], v[174:177], off nt
	s_waitcnt lgkmcnt(0)
	s_cbranch_vccnz .LBB0_183
	s_add_i32 s2, s53, s30
	s_cmp_lt_i32 s2, 0x8333
	s_cselect_b64 s[26:27], -1, 0
	s_and_b64 s[0:1], s[26:27], exec
	s_cselect_b32 s55, s2, s54
	s_cmpk_gt_i32 s55, 0xbff
	s_mov_b64 s[34:35], -1
	s_cbranch_scc0 .LBB0_218
	s_cmpk_gt_u32 s55, 0xfff
	s_cbranch_scc0 .LBB0_212
	s_cmp_gt_u32 s55, 0x10fff
	s_mov_b64 s[30:31], -1
	s_cbranch_scc0 .LBB0_205
	s_add_i32 s0, s55, 0xfffef000
	s_lshr_b32 s2, s0, 10
	s_lshl_b64 s[0:1], s[2:3], 24
	v_readlane_b32 s56, v246, 0
	v_readlane_b32 s57, v246, 1
	s_add_u32 s0, s56, s0
	s_addc_u32 s1, s57, s1
	s_lshl_b32 s8, s55, 6
	s_and_b32 s12, s8, 0x7c0
	s_lshl_b32 s8, s12, 13
	s_add_u32 s8, s0, s8
	s_addc_u32 s9, s1, 0
	s_lshl_b32 s0, s55, 1
	s_and_b32 s0, s0, 0x7c0
	s_lshl_b32 s14, s0, 2
	s_add_u32 s28, s8, s14
	s_addc_u32 s29, s9, 0
	s_lshl_b64 s[8:9], s[2:3], 23
	s_add_u32 s24, s33, s8
	v_readlane_b32 s58, v246, 2
	v_readlane_b32 s59, v246, 3
	v_readlane_b32 s60, v246, 4
	v_readlane_b32 s61, v246, 5
	v_readlane_b32 s62, v246, 6
	v_readlane_b32 s63, v246, 7
	s_mov_b32 s13, s3
	s_mov_b32 s1, s3
	s_addc_u32 s25, s44, s9
	s_mov_b64 s[30:31], 0

; __device__ __forceinline__ void tr_load(const TrItem& t, f32x4 (&ra)[8], f32x4 (&rb)[8], int lane) {
;     const int q = lane >> 4, n4 = lane & 15;
;     const float* p = t.src + (size_t)(2 * q) * t.N + 4 * n4;
; #pragma unroll
;     for (int i = 0; i < 8; ++i) { ra[i] = __builtin_nontemporal_load((const f32x4*)(p + (size_t)(8 * i) * t.N)); rb[i] = __builtin_nontemporal_load((const f32x4*)(p + (size_t)(8 * i + 1) * t.N)); }
; }
; __device__ __forceinline__ void conv_items(const Args& a, LAS unsigned char* lds, int it0, int it1, int vcu, int G, int lane, int wave) {
;     ...
;         it = nx; nx = it + NGW; has = nx < it1;
;         cur = tr_decode(a, has ? nx : it);
;         if (has) tr_load(cur, ra, rb, lane);
;         tr_store(nxt, na, nb_, scr, lane);
.LBB0_220:
	v_mul_u32_u24_e32 v2, s30, v1
	v_lshlrev_b32_e32 v2, 2, v2
	v_mov_b32_e32 v3, v131
	v_lshl_add_u64 v[2:3], s[28:29], 0, v[2:3]
	v_lshlrev_b32_e32 v4, 2, v132
	v_mov_b32_e32 v5, v131
	v_lshl_add_u64 v[2:3], v[2:3], 0, v[4:5]
	s_lshl_b64 s[8:9], s[30:31], 2
	v_lshl_add_u64 v[10:11], v[2:3], 0, s[8:9]
	s_mul_i32 s2, s30, 28
	global_load_dwordx4 v[2:5], v[2:3], off nt
	s_nop 0
	global_load_dwordx4 v[6:9], v[10:11], off nt
	v_lshl_add_u64 v[10:11], v[10:11], 0, s[2:3]
	v_lshl_add_u64 v[18:19], v[10:11], 0, s[8:9]
	global_load_dwordx4 v[10:13], v[10:11], off nt
	s_nop 0
	global_load_dwordx4 v[14:17], v[18:19], off nt
	v_lshl_add_u64 v[18:19], v[18:19], 0, s[2:3]
	v_lshl_add_u64 v[26:27], v[18:19], 0, s[8:9]
	global_load_dwordx4 v[18:21], v[18:19], off nt
	s_nop 0
	global_load_dwordx4 v[22:25], v[26:27], off nt
	v_lshl_add_u64 v[26:27], v[26:27], 0, s[2:3]
	v_lshl_add_u64 v[34:35], v[26:27], 0, s[8:9]
	v_lshl_add_u64 v[38:39], v[34:35], 0, s[2:3]
	v_lshl_add_u64 v[42:43], v[38:39], 0, s[8:9]
	v_lshl_add_u64 v[46:47], v[42:43], 0, s[2:3]
	v_lshl_add_u64 v[50:51], v[46:47], 0, s[8:9]
	v_lshl_add_u64 v[54:55], v[50:51], 0, s[2:3]
	v_lshl_add_u64 v[58:59], v[54:55], 0, s[8:9]
	v_lshl_add_u64 v[62:63], v[58:59], 0, s[2:3]
	global_load_dwordx4 v[26:29], v[26:27], off nt
	s_nop 0
	global_load_dwordx4 v[30:33], v[34:35], off nt
	s_nop 0
	global_load_dwordx4 v[34:37], v[38:39], off nt
	s_nop 0
	global_load_dwordx4 v[38:41], v[42:43], off nt
	s_nop 0
	global_load_dwordx4 v[42:45], v[46:47], off nt
	s_nop 0
	global_load_dwordx4 v[46:49], v[50:51], off nt
	s_nop 0
	global_load_dwordx4 v[50:53], v[54:55], off nt
	s_nop 0
	global_load_dwordx4 v[54:57], v[58:59], off nt
	s_nop 0
	global_load_dwordx4 v[58:61], v[62:63], off nt
	v_lshl_add_u64 v[62:63], v[62:63], 0, s[8:9]
	global_load_dwordx4 v[62:65], v[62:63], off nt
	s_waitcnt vmcnt(24)
	s_branch .LBB0_182

; #define LAS __attribute__((address_space(3)))
; __device__ __forceinline__ TrItem tr_decode(const Args& a, int it) {
;     unsigned char* ws = a.ws;
;     constexpr int T_IN = 32 * (INCOLS / 64), T_OUT = 32 * (DM / 64), T_GU1 = 32 * (4096 / 64), T_DN1 = 32 * (DM / 64);
;     TrItem t; int r = it;
;     if (r < T_IN) { const int kb = r & 31, nb = r >> 5; t.N = INCOLS; t.src = a.in[I_WIN] + (size_t)(64 * kb) * INCOLS + 64 * nb; t.dst = (bf16*)(ws + WS_WIN) + (size_t)(64 * nb) * DM + 64 * kb; return t; } r -= T_IN;
;     if (r < T_OUT) { const int kb = r & 31, nb = r >> 5; t.N = DM; t.src = a.in[I_WOUT] + (size_t)(64 * kb) * DM + 64 * nb; t.dst = (bf16*)(ws + WS_WOUT) + (size_t)(64 * nb) * DM + 64 * kb; return t; } r -= T_OUT;
;     if (r < NEXP * T_GU1) { const int e = r / T_GU1, q = r % T_GU1, kb = q & 31, nb = q >> 5, n0 = 64 * nb;
;         const int drow0 = n0 < 2048 ? (n0 >> 7) * 256 + (n0 & 127) : ((n0 - 2048) >> 7) * 256 + 128 + ((n0 - 2048) & 127);
;         t.N = 4096; t.src = a.in[I_WGU] + (size_t)e * DM * 4096 + (size_t)(64 * kb) * 4096 + n0; t.dst = (bf16*)(ws + WS_WGU) + (size_t)e * 4096 * DM + (size_t)drow0 * DM + 64 * kb; return t; } r -= NEXP * T_GU1;
;     { const int e = r / T_DN1, q = r % T_DN1, kb = q & 31, nb = q >> 5;
;         t.N = DM; t.src = a.in[I_WDN] + (size_t)e * DM * DM + (size_t)(64 * kb) * DM + 64 * nb; t.dst = (bf16*)(ws + WS_WDN) + (size_t)e * DM * DM + (size_t)(64 * nb) * DM + 64 * kb; return t; }
; }
; __device__ __forceinline__ void tr_load(const TrItem& t, f32x4 (&ra)[8], f32x4 (&rb)[8], int lane) {
;     const int q = lane >> 4, n4 = lane & 15;
;     const float* p = t.src + (size_t)(2 * q) * t.N + 4 * n4;
; #pragma unroll
;     for (int i = 0; i < 8; ++i) { ra[i] = __builtin_nontemporal_load((const f32x4*)(p + (size_t)(8 * i) * t.N)); rb[i] = __builtin_nontemporal_load((const f32x4*)(p + (size_t)(8 * i + 1) * t.N)); }
; }
; __device__ __forceinline__ void conv_items(const Args& a, LAS unsigned char* lds, int it0, int it1, int vcu, int G, int lane, int wave) {
;     LAS unsigned* scr = (LAS unsigned*)(lds + wave * 16384);
;     const int gw = vcu * NWAVES + wave, NGW = G * NWAVES;
;     f32x4 ra[8], rb[8], na[8], nb_[8];
;     int it = it0 + gw;
;     if (it >= it1) return;
;     TrItem cur = tr_decode(a, it);
;     tr_load(cur, ra, rb, lane);
.LBB0_416:
	v_readlane_b32 s2, v246, 33
	s_lshl_b32 s2, s2, 14
	v_readlane_b32 s9, v246, 11
	s_waitcnt vmcnt(11)
	v_lshrrev_b32_e32 v66, 3, v194
	s_add_i32 s8, s2, 0
	s_lshl_b32 s30, s9, 3
	s_lshl_b64 s[4:5], s[4:5], 12
	s_waitcnt lgkmcnt(0)
	v_and_b32_e32 v133, 6, v66
	s_add_u32 s2, s10, s4
	v_mul_u32_u24_e32 v2, s16, v133
	v_lshlrev_b32_e32 v67, 2, v194
	s_addc_u32 s4, s11, s5
	s_lshl_b64 s[0:1], s[0:1], 1
	v_lshlrev_b32_e32 v130, 2, v2
	v_mov_b32_e32 v131, 0
	v_and_b32_e32 v132, 60, v67
	s_add_u32 s10, s2, s0
	v_lshl_add_u64 v[2:3], s[12:13], 0, v[130:131]
	v_lshlrev_b32_e32 v130, 2, v132
	s_addc_u32 s11, s4, s1
	v_lshl_add_u64 v[2:3], v[2:3], 0, v[130:131]
	s_lshl_b64 s[0:1], s[16:17], 2
	s_mov_b32 s3, 0
	v_lshl_add_u64 v[10:11], v[2:3], 0, s[0:1]
	s_mul_i32 s2, s16, 28
	global_load_dwordx4 v[2:5], v[2:3], off nt
	s_nop 0
	global_load_dwordx4 v[6:9], v[10:11], off nt
	v_lshl_add_u64 v[10:11], v[10:11], 0, s[2:3]
	v_lshl_add_u64 v[18:19], v[10:11], 0, s[0:1]
	global_load_dwordx4 v[10:13], v[10:11], off nt
	s_nop 0
	global_load_dwordx4 v[14:17], v[18:19], off nt
	v_lshl_add_u64 v[18:19], v[18:19], 0, s[2:3]
	v_lshl_add_u64 v[26:27], v[18:19], 0, s[0:1]
	global_load_dwordx4 v[18:21], v[18:19], off nt
	s_nop 0
	global_load_dwordx4 v[22:25], v[26:27], off nt
	v_lshl_add_u64 v[26:27], v[26:27], 0, s[2:3]
	v_lshl_add_u64 v[34:35], v[26:27], 0, s[0:1]
	v_lshl_add_u64 v[38:39], v[34:35], 0, s[2:3]
	v_lshl_add_u64 v[42:43], v[38:39], 0, s[0:1]
	v_lshl_add_u64 v[46:47], v[42:43], 0, s[2:3]
	s_waitcnt vmcnt(14)
	v_lshl_add_u64 v[50:51], v[46:47], 0, s[0:1]
	s_waitcnt vmcnt(12)
	v_lshl_add_u64 v[54:55], v[50:51], 0, s[2:3]
	v_lshl_add_u64 v[58:59], v[54:55], 0, s[0:1]
	v_lshl_add_u64 v[62:63], v[58:59], 0, s[2:3]
	global_load_dwordx4 v[26:29], v[26:27], off nt
	s_nop 0
	global_load_dwordx4 v[30:33], v[34:35], off nt
	v_or_b32_e32 v78, 8, v66
	global_load_dwordx4 v[34:37], v[38:39], off nt
	v_bitop3_b32 v80, v78, 28, v67 bitop3:0x48
	global_load_dwordx4 v[38:41], v[42:43], off nt
	v_lshlrev_b32_e32 v79, 7, v78
	global_load_dwordx4 v[42:45], v[46:47], off nt
	v_lshlrev_b32_e32 v80, 2, v80
	global_load_dwordx4 v[46:49], v[50:51], off nt
	v_lshlrev_b32_e32 v138, 12, v78
	global_load_dwordx4 v[50:53], v[54:55], off nt
	v_or_b32_e32 v78, 16, v66
	global_load_dwordx4 v[54:57], v[58:59], off nt
	v_add3_u32 v135, s8, v79, v80
	global_load_dwordx4 v[58:61], v[62:63], off nt
	v_lshl_add_u64 v[62:63], v[62:63], 0, s[0:1]
	global_load_dwordx4 v[62:65], v[62:63], off nt
	v_bitop3_b32 v80, v78, 28, v67 bitop3:0x48
	v_lshlrev_b32_e32 v68, 9, v0
	v_lshrrev_b32_e32 v69, 2, v194
	v_mov_b32_e32 v70, 0x70
	s_movk_i32 s1, 0x50
	v_lshlrev_b32_e32 v79, 7, v78
	v_lshlrev_b32_e32 v80, 2, v80
	v_lshlrev_b32_e32 v140, 12, v78
	v_or_b32_e32 v78, 24, v66
	v_and_b32_e32 v68, 0x1e00, v68
	v_and_b32_e32 v69, 12, v69
	s_movk_i32 s0, 0x70
	v_bitop3_b32 v75, v1, s1, v70 bitop3:0x6c
	s_movk_i32 s1, 0x60
	v_add3_u32 v152, s8, v79, v80
	v_bitop3_b32 v80, v78, 28, v67 bitop3:0x48
	v_add3_u32 v68, s8, v68, v69
	v_and_b32_e32 v69, 0x70, v1
	v_bitop3_b32 v71, v1, 16, v70 bitop3:0x6c
	v_bitop3_b32 v72, v1, 32, v70 bitop3:0x6c
	v_bitop3_b32 v73, v1, 48, v70 bitop3:0x6c
	v_bitop3_b32 v74, v1, 64, v70 bitop3:0x6c
	v_bitop3_b32 v70, v1, s1, v70 bitop3:0x6c
	v_bitop3_b32 v76, v1, s0, v1 bitop3:0xc
	v_lshlrev_b32_e32 v1, 3, v0
	v_bitop3_b32 v77, v66, 28, v67 bitop3:0x48
	v_lshlrev_b32_e32 v79, 7, v78
	v_lshlrev_b32_e32 v80, 2, v80
	v_lshlrev_b32_e32 v142, 12, v78
	v_or_b32_e32 v78, 32, v66
	v_and_b32_e32 v134, 56, v1
	v_lshlrev_b32_e32 v1, 7, v66
	v_lshlrev_b32_e32 v77, 2, v77
	v_add3_u32 v153, s8, v79, v80
	v_lshlrev_b32_e32 v79, 7, v78
	v_add3_u32 v1, s8, v1, v77
	v_add3_u32 v154, s8, v79, v77
	v_or_b32_e32 v77, 40, v66
	s_add_u32 s31, s92, 0x70800000
	v_bitop3_b32 v79, v77, 28, v67 bitop3:0x48
	s_addc_u32 s33, s93, 0
	v_lshlrev_b32_e32 v136, 12, v66
	v_lshlrev_b32_e32 v144, 12, v78
	v_lshlrev_b32_e32 v78, 7, v77
	v_lshlrev_b32_e32 v79, 2, v79
	v_lshlrev_b32_e32 v146, 12, v77
	v_or_b32_e32 v77, 48, v66
	v_or_b32_e32 v66, 56, v66
	s_add_u32 s34, s92, 0x50800000
	v_add3_u32 v155, s8, v78, v79
	v_bitop3_b32 v79, v77, 28, v67 bitop3:0x48
	v_bitop3_b32 v67, v66, 28, v67 bitop3:0x48
	s_addc_u32 s35, s93, 0
	v_lshlrev_b32_e32 v78, 7, v77
	v_lshlrev_b32_e32 v79, 2, v79
	v_lshlrev_b32_e32 v148, 12, v77
	v_lshlrev_b32_e32 v77, 7, v66
	v_lshlrev_b32_e32 v67, 2, v67
	s_add_u32 s4, s92, 0x1a00000
	v_mov_b32_e32 v137, v131
	v_mov_b32_e32 v139, v131
	v_mov_b32_e32 v141, v131
	v_mov_b32_e32 v143, v131
	v_mov_b32_e32 v145, v131
	v_mov_b32_e32 v147, v131
	v_add3_u32 v156, s8, v78, v79
	v_mov_b32_e32 v149, v131
	v_add3_u32 v157, s8, v77, v67
	v_lshlrev_b32_e32 v150, 12, v66
	v_mov_b32_e32 v151, v131
	s_addc_u32 s5, s93, 0
	s_lshl_b32 s44, s9, 4
	v_add_u32_e32 v158, v68, v69
	v_add_u32_e32 v159, v68, v71
	v_add_u32_e32 v160, v68, v72
	v_add_u32_e32 v161, v68, v73
	v_add_u32_e32 v162, v68, v74
	v_add_u32_e32 v163, v68, v75
	v_add_u32_e32 v164, v68, v70
	v_add_u32_e32 v165, v68, v76
	s_branch .LBB0_419
; #define LAS __attribute__((address_space(3)))
; #define LDS_WAIT() asm volatile("s_waitcnt lgkmcnt(0)" ::: "memory")
; __device__ __forceinline__ unsigned cvt2bf(float lo, float hi) { const f32x2_t v = {lo, hi}; const bf16x2_t r = __builtin_convertvector(v, bf16x2_t); return __builtin_bit_cast(unsigned, r); }
; __device__ __forceinline__ void tr_store(const TrItem& t, const f32x4 (&ra)[8], const f32x4 (&rb)[8], LAS unsigned* scr, int lane) {
;     const int q = lane >> 4, n4 = lane & 15;
; #pragma unroll
;     for (int i = 0; i < 8; ++i)
; #pragma unroll
;         for (int j = 0; j < 4; ++j) scr[(4 * n4 + j) * 32 + ((i ^ (n4 & 7)) << 2) + q] = cvt2bf(ra[i][j], rb[i][j]);
;     LDS_WAIT(); asm volatile("" ::: "memory");
;     const int nr = lane >> 3, ch = lane & 7;
; #pragma unroll
;     for (int i = 0; i < 8; ++i) { const int n = nr + 8 * i; const v4u v = *(const LAS v4u*)(scr + n * 32 + ((ch ^ ((n >> 2) & 7)) << 2));
;         __builtin_nontemporal_store(v, (v4u*)(t.dst + (size_t)n * DM + 8 * ch)); }
;     LDS_WAIT(); asm volatile("" ::: "memory");
; }
; __device__ __forceinline__ void conv_items(const Args& a, LAS unsigned char* lds, int it0, int it1, int vcu, int G, int lane, int wave) {
;     ...
;         it = nx; nx = it + NGW; has = nx < it1;
.Lcvw_2:
	s_waitcnt vmcnt(8)
.LBB0_417:
	v_cvt_pk_bf16_f32 v166, v66, v74
	v_cvt_pk_bf16_f32 v167, v67, v75
	ds_write2_b32 v158, v166, v167 offset1:32
	v_cvt_pk_bf16_f32 v166, v68, v76
	v_cvt_pk_bf16_f32 v167, v69, v77
	ds_write2_b32 v158, v166, v167 offset0:64 offset1:96
	v_cvt_pk_bf16_f32 v166, v70, v86
	v_cvt_pk_bf16_f32 v167, v71, v87
	ds_write2_b32 v159, v166, v167 offset1:32
	v_cvt_pk_bf16_f32 v166, v72, v88
	v_cvt_pk_bf16_f32 v167, v73, v89
	ds_write2_b32 v159, v166, v167 offset0:64 offset1:96
	v_cvt_pk_bf16_f32 v166, v78, v98
	v_cvt_pk_bf16_f32 v167, v79, v99
	ds_write2_b32 v160, v166, v167 offset1:32
	v_cvt_pk_bf16_f32 v166, v80, v100
	v_cvt_pk_bf16_f32 v167, v81, v101
	ds_write2_b32 v160, v166, v167 offset0:64 offset1:96
	v_cvt_pk_bf16_f32 v166, v82, v106
	v_cvt_pk_bf16_f32 v167, v83, v107
	ds_write2_b32 v161, v166, v167 offset1:32
	v_cvt_pk_bf16_f32 v166, v84, v108
	v_cvt_pk_bf16_f32 v167, v85, v109
	ds_write2_b32 v161, v166, v167 offset0:64 offset1:96
	v_cvt_pk_bf16_f32 v166, v90, v114
	v_cvt_pk_bf16_f32 v167, v91, v115
	ds_write2_b32 v162, v166, v167 offset1:32
	v_cvt_pk_bf16_f32 v166, v92, v116
	v_cvt_pk_bf16_f32 v167, v93, v117
	ds_write2_b32 v162, v166, v167 offset0:64 offset1:96
	v_cvt_pk_bf16_f32 v166, v94, v118
	v_cvt_pk_bf16_f32 v167, v95, v119
	ds_write2_b32 v163, v166, v167 offset1:32
	v_cvt_pk_bf16_f32 v166, v96, v120
	v_cvt_pk_bf16_f32 v167, v97, v121
	ds_write2_b32 v163, v166, v167 offset0:64 offset1:96
	v_cvt_pk_bf16_f32 v166, v102, v122
	v_cvt_pk_bf16_f32 v167, v103, v123
	s_lshl_b64 s[0:1], s[0:1], 12
	ds_write2_b32 v164, v166, v167 offset1:32
	v_cvt_pk_bf16_f32 v166, v104, v124
	v_cvt_pk_bf16_f32 v167, v105, v125
	s_add_u32 s2, s20, s0
	ds_write2_b32 v164, v166, v167 offset0:64 offset1:96
	v_cvt_pk_bf16_f32 v166, v110, v126
	v_cvt_pk_bf16_f32 v167, v111, v127
	s_addc_u32 s8, s21, s1
	s_lshl_b64 s[0:1], s[10:11], 1
	ds_write2_b32 v165, v166, v167 offset1:32
	v_cvt_pk_bf16_f32 v166, v112, v128
	v_cvt_pk_bf16_f32 v167, v113, v129
	s_add_u32 s10, s2, s0
	ds_write2_b32 v165, v166, v167 offset0:64 offset1:96
	s_addc_u32 s11, s8, s1
	s_add_i32 s26, s45, s30
	s_lshl_b64 s[0:1], s[12:13], 12
	s_waitcnt lgkmcnt(0)
	s_add_u32 s2, s18, s0
	s_addc_u32 s8, s19, s1
	s_lshl_b64 s[0:1], s[16:17], 1
	ds_read_b128 v[166:169], v1
	ds_read_b128 v[170:173], v135
	s_add_u32 s0, s2, s0
	s_addc_u32 s1, s8, s1
	v_lshl_add_u64 v[178:179], s[0:1], 0, v[130:131]
	v_lshl_add_u64 v[174:175], v[178:179], 0, v[136:137]
	s_waitcnt lgkmcnt(1)
	global_store_dwordx4 v[174:175], v[166:169], off nt
	ds_read_b128 v[166:169], v152
	v_lshl_add_u64 v[174:175], v[178:179], 0, v[138:139]
	s_waitcnt lgkmcnt(1)
	global_store_dwordx4 v[174:175], v[170:173], off nt
	ds_read_b128 v[170:173], v153
	v_lshl_add_u64 v[174:175], v[178:179], 0, v[140:141]
	s_waitcnt lgkmcnt(1)
	global_store_dwordx4 v[174:175], v[166:169], off nt
	ds_read_b128 v[166:169], v154
	v_lshl_add_u64 v[174:175], v[178:179], 0, v[142:143]
	s_waitcnt lgkmcnt(1)
	global_store_dwordx4 v[174:175], v[170:173], off nt
	v_lshl_add_u64 v[174:175], v[178:179], 0, v[144:145]
	ds_read_b128 v[170:173], v155
	s_waitcnt lgkmcnt(1)
	global_store_dwordx4 v[174:175], v[166:169], off nt
	ds_read_b128 v[166:169], v156
	ds_read_b128 v[174:177], v157
	v_lshl_add_u64 v[180:181], v[178:179], 0, v[146:147]
	s_waitcnt lgkmcnt(2)
	global_store_dwordx4 v[180:181], v[170:173], off nt
	s_cmp_gt_i32 s26, 0x8332
	s_cselect_b64 s[0:1], -1, 0
	v_lshl_add_u64 v[170:171], v[178:179], 0, v[148:149]
	s_waitcnt lgkmcnt(1)
	global_store_dwordx4 v[170:171], v[166:169], off nt
	s_nop 1
	v_lshl_add_u64 v[166:167], v[178:179], 0, v[150:151]
	s_waitcnt lgkmcnt(0)
	global_store_dwordx4 v[166:167], v[174:177], off nt
	s_waitcnt lgkmcnt(0)

; #define LAS __attribute__((address_space(3)))
; __device__ __forceinline__ unsigned cvt2bf(float lo, float hi) { const f32x2_t v = {lo, hi}; const bf16x2_t r = __builtin_convertvector(v, bf16x2_t); return __builtin_bit_cast(unsigned, r); }
; __device__ __forceinline__ void tr_load(const TrItem& t, f32x4 (&ra)[8], f32x4 (&rb)[8], int lane) {
;     const int q = lane >> 4, n4 = lane & 15;
;     const float* p = t.src + (size_t)(2 * q) * t.N + 4 * n4;
; #pragma unroll
;     for (int i = 0; i < 8; ++i) { ra[i] = __builtin_nontemporal_load((const f32x4*)(p + (size_t)(8 * i) * t.N)); rb[i] = __builtin_nontemporal_load((const f32x4*)(p + (size_t)(8 * i + 1) * t.N)); }
; }
; __device__ __forceinline__ void tr_store(const TrItem& t, const f32x4 (&ra)[8], const f32x4 (&rb)[8], LAS unsigned* scr, int lane) {
;     const int q = lane >> 4, n4 = lane & 15;
; #pragma unroll
;     for (int i = 0; i < 8; ++i)
; #pragma unroll
;         for (int j = 0; j < 4; ++j) scr[(4 * n4 + j) * 32 + ((i ^ (n4 & 7)) << 2) + q] = cvt2bf(ra[i][j], rb[i][j]);
; __device__ __forceinline__ void conv_items(const Args& a, LAS unsigned char* lds, int it0, int it1, int vcu, int G, int lane, int wave) {
;     ...
;         int nx = it + NGW; bool has = nx < it1;
;         TrItem nxt = tr_decode(a, has ? nx : it);
;         if (has) tr_load(nxt, na, nb_, lane);
;         tr_store(cur, ra, rb, scr, lane);
.LBB0_434:
	v_mul_u32_u24_e32 v66, s24, v133
	v_lshlrev_b32_e32 v130, 2, v66
	v_lshl_add_u64 v[66:67], s[22:23], 0, v[130:131]
	v_lshlrev_b32_e32 v130, 2, v132
	v_lshl_add_u64 v[66:67], v[66:67], 0, v[130:131]
	s_lshl_b64 s[8:9], s[24:25], 2
	v_lshl_add_u64 v[70:71], v[66:67], 0, s[8:9]
	s_mul_i32 s2, s24, 28
	global_load_dwordx4 v[66:69], v[66:67], off nt
	s_nop 0
	global_load_dwordx4 v[74:77], v[70:71], off nt
	v_lshl_add_u64 v[70:71], v[70:71], 0, s[2:3]
	v_lshl_add_u64 v[78:79], v[70:71], 0, s[8:9]
	global_load_dwordx4 v[70:73], v[70:71], off nt
	s_nop 0
	global_load_dwordx4 v[86:89], v[78:79], off nt
	v_lshl_add_u64 v[78:79], v[78:79], 0, s[2:3]
	v_lshl_add_u64 v[82:83], v[78:79], 0, s[8:9]
	global_load_dwordx4 v[78:81], v[78:79], off nt
	s_nop 0
	global_load_dwordx4 v[98:101], v[82:83], off nt
	v_lshl_add_u64 v[82:83], v[82:83], 0, s[2:3]
	v_lshl_add_u64 v[90:91], v[82:83], 0, s[8:9]
	v_lshl_add_u64 v[94:95], v[90:91], 0, s[2:3]
	global_load_dwordx4 v[82:85], v[82:83], off nt
	s_nop 0
	global_load_dwordx4 v[106:109], v[90:91], off nt
	s_nop 0
	global_load_dwordx4 v[90:93], v[94:95], off nt
	v_lshl_add_u64 v[94:95], v[94:95], 0, s[8:9]
	v_lshl_add_u64 v[102:103], v[94:95], 0, s[2:3]
	global_load_dwordx4 v[114:117], v[94:95], off nt
	s_nop 0
	global_load_dwordx4 v[94:97], v[102:103], off nt
	v_lshl_add_u64 v[102:103], v[102:103], 0, s[8:9]
	v_lshl_add_u64 v[110:111], v[102:103], 0, s[2:3]
	global_load_dwordx4 v[118:121], v[102:103], off nt
	s_nop 0
	global_load_dwordx4 v[102:105], v[110:111], off nt
	v_lshl_add_u64 v[110:111], v[110:111], 0, s[8:9]
	v_lshl_add_u64 v[126:127], v[110:111], 0, s[2:3]
	global_load_dwordx4 v[122:125], v[110:111], off nt
	s_nop 0
	global_load_dwordx4 v[110:113], v[126:127], off nt
	v_lshl_add_u64 v[126:127], v[126:127], 0, s[8:9]
	global_load_dwordx4 v[126:129], v[126:127], off nt
	s_waitcnt vmcnt(30)
	v_cvt_pk_bf16_f32 v130, v2, v6
	v_cvt_pk_bf16_f32 v166, v3, v7
	ds_write2_b32 v158, v130, v166 offset1:32
	v_cvt_pk_bf16_f32 v130, v4, v8
	v_cvt_pk_bf16_f32 v166, v5, v9
	ds_write2_b32 v158, v130, v166 offset0:64 offset1:96
	s_waitcnt vmcnt(28)
	v_cvt_pk_bf16_f32 v130, v10, v14
	v_cvt_pk_bf16_f32 v166, v11, v15
	ds_write2_b32 v159, v130, v166 offset1:32
	v_cvt_pk_bf16_f32 v130, v12, v16
	v_cvt_pk_bf16_f32 v166, v13, v17
	ds_write2_b32 v159, v130, v166 offset0:64 offset1:96
	s_waitcnt vmcnt(26)
	v_cvt_pk_bf16_f32 v130, v18, v22
	v_cvt_pk_bf16_f32 v166, v19, v23
	ds_write2_b32 v160, v130, v166 offset1:32
	v_cvt_pk_bf16_f32 v130, v20, v24
	v_cvt_pk_bf16_f32 v166, v21, v25
	ds_write2_b32 v160, v130, v166 offset0:64 offset1:96
	s_waitcnt vmcnt(24)
	v_cvt_pk_bf16_f32 v130, v26, v30
	v_cvt_pk_bf16_f32 v166, v27, v31
	ds_write2_b32 v161, v130, v166 offset1:32
	v_cvt_pk_bf16_f32 v130, v28, v32
	v_cvt_pk_bf16_f32 v166, v29, v33
	ds_write2_b32 v161, v130, v166 offset0:64 offset1:96
	s_waitcnt vmcnt(22)
	v_cvt_pk_bf16_f32 v130, v34, v38
	v_cvt_pk_bf16_f32 v166, v35, v39
	ds_write2_b32 v162, v130, v166 offset1:32
	v_cvt_pk_bf16_f32 v130, v36, v40
	v_cvt_pk_bf16_f32 v166, v37, v41
	ds_write2_b32 v162, v130, v166 offset0:64 offset1:96
	s_waitcnt vmcnt(20)
	v_cvt_pk_bf16_f32 v130, v42, v46
	v_cvt_pk_bf16_f32 v166, v43, v47
	ds_write2_b32 v163, v130, v166 offset1:32
	v_cvt_pk_bf16_f32 v130, v44, v48
	v_cvt_pk_bf16_f32 v166, v45, v49
	ds_write2_b32 v163, v130, v166 offset0:64 offset1:96
	s_waitcnt vmcnt(18)
	v_cvt_pk_bf16_f32 v130, v50, v54
	v_cvt_pk_bf16_f32 v166, v51, v55
	ds_write2_b32 v164, v130, v166 offset1:32
	v_cvt_pk_bf16_f32 v130, v52, v56
	v_cvt_pk_bf16_f32 v166, v53, v57
	ds_write2_b32 v164, v130, v166 offset0:64 offset1:96
	s_waitcnt vmcnt(16)
	v_cvt_pk_bf16_f32 v130, v58, v62
	v_cvt_pk_bf16_f32 v166, v59, v63
	ds_write2_b32 v165, v130, v166 offset1:32
	v_cvt_pk_bf16_f32 v130, v60, v64
	v_cvt_pk_bf16_f32 v166, v61, v65
	ds_write2_b32 v165, v130, v166 offset0:64 offset1:96
	s_branch .Lcvj_2

; #define LAS __attribute__((address_space(3)))
; #define LDS_WAIT() asm volatile("s_waitcnt lgkmcnt(0)" ::: "memory")
; __device__ __forceinline__ TrItem tr_decode(const Args& a, int it) {
;     ...
;     if (r < T_IN) { const int kb = r & 31, nb = r >> 5; t.N = INCOLS; t.src = a.in[I_WIN] + (size_t)(64 * kb) * INCOLS + 64 * nb; t.dst = (bf16*)(ws + WS_WIN) + (size_t)(64 * nb) * DM + 64 * kb; return t; } r -= T_IN;
;     if (r < T_OUT) { const int kb = r & 31, nb = r >> 5; t.N = DM; t.src = a.in[I_WOUT] + (size_t)(64 * kb) * DM + 64 * nb; t.dst = (bf16*)(ws + WS_WOUT) + (size_t)(64 * nb) * DM + 64 * kb; return t; } r -= T_OUT;
;     if (r < NEXP * T_GU1) { const int e = r / T_GU1, q = r % T_GU1, kb = q & 31, nb = q >> 5, n0 = 64 * nb;
;         const int drow0 = n0 < 2048 ? (n0 >> 7) * 256 + (n0 & 127) : ((n0 - 2048) >> 7) * 256 + 128 + ((n0 - 2048) & 127);
;         t.N = 4096; t.src = a.in[I_WGU] + (size_t)e * DM * 4096 + (size_t)(64 * kb) * 4096 + n0; t.dst = (bf16*)(ws + WS_WGU) + (size_t)e * 4096 * DM + (size_t)drow0 * DM + 64 * kb; return t; } r -= NEXP * T_GU1;
;     { const int e = r / T_DN1, q = r % T_DN1, kb = q & 31, nb = q >> 5;
;         t.N = DM; t.src = a.in[I_WDN] + (size_t)e * DM * DM + (size_t)(64 * kb) * DM + 64 * nb; t.dst = (bf16*)(ws + WS_WDN) + (size_t)e * DM * DM + (size_t)(64 * nb) * DM + 64 * kb; return t; }
; __device__ __forceinline__ void tr_store(const TrItem& t, const f32x4 (&ra)[8], const f32x4 (&rb)[8], LAS unsigned* scr, int lane) {
;     ...
;     LDS_WAIT(); asm volatile("" ::: "memory");
;     const int nr = lane >> 3, ch = lane & 7;
; #pragma unroll
;     for (int i = 0; i < 8; ++i) { const int n = nr + 8 * i; const v4u v = *(const LAS v4u*)(scr + n * 32 + ((ch ^ ((n >> 2) & 7)) << 2));
;         __builtin_nontemporal_store(v, (v4u*)(t.dst + (size_t)n * DM + 8 * ch)); }
;     LDS_WAIT(); asm volatile("" ::: "memory");
; }
; __device__ __forceinline__ void conv_items(const Args& a, LAS unsigned char* lds, int it0, int it1, int vcu, int G, int lane, int wave) {
;     ...
;         if (!has) break;
;         it = nx; nx = it + NGW; has = nx < it1;
;         cur = tr_decode(a, has ? nx : it);
.Lcvj_2:
	s_waitcnt lgkmcnt(0)
	ds_read_b128 v[166:169], v1
	ds_read_b128 v[170:173], v135
	v_lshlrev_b32_e32 v130, 1, v134
	v_lshl_add_u64 v[178:179], s[10:11], 0, v[130:131]
	v_lshl_add_u64 v[174:175], v[178:179], 0, v[136:137]
	s_waitcnt lgkmcnt(1)
	global_store_dwordx4 v[174:175], v[166:169], off nt
	ds_read_b128 v[166:169], v152
	v_lshl_add_u64 v[174:175], v[178:179], 0, v[138:139]
	s_waitcnt lgkmcnt(1)
	global_store_dwordx4 v[174:175], v[170:173], off nt
	ds_read_b128 v[170:173], v153
	v_lshl_add_u64 v[174:175], v[178:179], 0, v[140:141]
	s_waitcnt lgkmcnt(1)
	global_store_dwordx4 v[174:175], v[166:169], off nt
	ds_read_b128 v[166:169], v154
	v_lshl_add_u64 v[174:175], v[178:179], 0, v[142:143]
	s_waitcnt lgkmcnt(1)
	global_store_dwordx4 v[174:175], v[170:173], off nt
	v_lshl_add_u64 v[174:175], v[178:179], 0, v[144:145]
	ds_read_b128 v[170:173], v155
	s_waitcnt lgkmcnt(1)
	global_store_dwordx4 v[174:175], v[166:169], off nt
	ds_read_b128 v[166:169], v156
	ds_read_b128 v[174:177], v157
	v_lshl_add_u64 v[180:181], v[178:179], 0, v[146:147]
	s_waitcnt lgkmcnt(2)
	global_store_dwordx4 v[180:181], v[170:173], off nt
	s_and_b64 vcc, exec, s[0:1]
	s_mov_b64 s[0:1], -1
	v_lshl_add_u64 v[170:171], v[178:179], 0, v[148:149]
	s_waitcnt lgkmcnt(1)
	global_store_dwordx4 v[170:171], v[166:169], off nt
	s_nop 1
	v_lshl_add_u64 v[166:167], v[178:179], 0, v[150:151]
	s_waitcnt lgkmcnt(0)
	global_store_dwordx4 v[166:167], v[174:177], off nt
	s_waitcnt lgkmcnt(0)
	s_cbranch_vccnz .LBB0_418
	s_add_i32 s2, s44, s26
	s_cmp_lt_i32 s2, 0x8333
	s_cselect_b64 s[22:23], -1, 0
	s_and_b64 s[0:1], s[22:23], exec
	s_cselect_b32 s52, s2, s45
	s_cmpk_gt_i32 s52, 0xbff
	s_mov_b64 s[28:29], -1
	s_cbranch_scc0 .LBB0_453
	s_cmpk_gt_u32 s52, 0xfff
	s_cbranch_scc0 .LBB0_447
	s_cmp_gt_u32 s52, 0x10fff
	s_mov_b64 s[26:27], -1
	s_cbranch_scc0 .LBB0_440
	s_add_i32 s0, s52, 0xfffef000
	s_lshr_b32 s2, s0, 10
	s_lshl_b64 s[0:1], s[2:3], 24
	v_readlane_b32 s56, v246, 0
	v_readlane_b32 s57, v246, 1
	s_add_u32 s0, s56, s0
	s_addc_u32 s1, s57, s1
	s_lshl_b32 s8, s52, 6
	s_and_b32 s10, s8, 0x7c0
	s_lshl_b32 s8, s10, 13
	s_add_u32 s8, s0, s8
	s_addc_u32 s9, s1, 0
	s_lshl_b32 s0, s52, 1
	s_and_b32 s0, s0, 0x7c0
	s_lshl_b32 s14, s0, 2
	s_add_u32 s24, s8, s14
	s_addc_u32 s25, s9, 0
	s_lshl_b64 s[8:9], s[2:3], 23
	s_add_u32 s20, s31, s8
	v_readlane_b32 s58, v246, 2
	v_readlane_b32 s59, v246, 3
	v_readlane_b32 s60, v246, 4
	v_readlane_b32 s61, v246, 5
	v_readlane_b32 s62, v246, 6
	v_readlane_b32 s63, v246, 7
	s_mov_b32 s11, s3
	s_mov_b32 s1, s3
	s_addc_u32 s21, s33, s9
	s_mov_b64 s[26:27], 0

; __device__ __forceinline__ void tr_load(const TrItem& t, f32x4 (&ra)[8], f32x4 (&rb)[8], int lane) {
;     const int q = lane >> 4, n4 = lane & 15;
;     const float* p = t.src + (size_t)(2 * q) * t.N + 4 * n4;
; #pragma unroll
;     for (int i = 0; i < 8; ++i) { ra[i] = __builtin_nontemporal_load((const f32x4*)(p + (size_t)(8 * i) * t.N)); rb[i] = __builtin_nontemporal_load((const f32x4*)(p + (size_t)(8 * i + 1) * t.N)); }
; }
; __device__ __forceinline__ void conv_items(const Args& a, LAS unsigned char* lds, int it0, int it1, int vcu, int G, int lane, int wave) {
;     ...
;         it = nx; nx = it + NGW; has = nx < it1;
;         cur = tr_decode(a, has ? nx : it);
;         if (has) tr_load(cur, ra, rb, lane);
;         tr_store(nxt, na, nb_, scr, lane);
.LBB0_455:
	v_mul_u32_u24_e32 v2, s26, v133
	v_lshlrev_b32_e32 v2, 2, v2
	v_mov_b32_e32 v3, v131
	v_lshl_add_u64 v[2:3], s[24:25], 0, v[2:3]
	v_lshlrev_b32_e32 v4, 2, v132
	v_mov_b32_e32 v5, v131
	v_lshl_add_u64 v[2:3], v[2:3], 0, v[4:5]
	s_lshl_b64 s[8:9], s[26:27], 2
	v_lshl_add_u64 v[10:11], v[2:3], 0, s[8:9]
	s_mul_i32 s2, s26, 28
	global_load_dwordx4 v[2:5], v[2:3], off nt
	s_nop 0
	global_load_dwordx4 v[6:9], v[10:11], off nt
	v_lshl_add_u64 v[10:11], v[10:11], 0, s[2:3]
	v_lshl_add_u64 v[18:19], v[10:11], 0, s[8:9]
	global_load_dwordx4 v[10:13], v[10:11], off nt
	s_nop 0
	global_load_dwordx4 v[14:17], v[18:19], off nt
	v_lshl_add_u64 v[18:19], v[18:19], 0, s[2:3]
	v_lshl_add_u64 v[26:27], v[18:19], 0, s[8:9]
	global_load_dwordx4 v[18:21], v[18:19], off nt
	s_nop 0
	global_load_dwordx4 v[22:25], v[26:27], off nt
	v_lshl_add_u64 v[26:27], v[26:27], 0, s[2:3]
	v_lshl_add_u64 v[34:35], v[26:27], 0, s[8:9]
	v_lshl_add_u64 v[38:39], v[34:35], 0, s[2:3]
	v_lshl_add_u64 v[42:43], v[38:39], 0, s[8:9]
	v_lshl_add_u64 v[46:47], v[42:43], 0, s[2:3]
	v_lshl_add_u64 v[50:51], v[46:47], 0, s[8:9]
	v_lshl_add_u64 v[54:55], v[50:51], 0, s[2:3]
	v_lshl_add_u64 v[58:59], v[54:55], 0, s[8:9]
	v_lshl_add_u64 v[62:63], v[58:59], 0, s[2:3]
	global_load_dwordx4 v[26:29], v[26:27], off nt
	s_nop 0
	global_load_dwordx4 v[30:33], v[34:35], off nt
	s_nop 0
	global_load_dwordx4 v[34:37], v[38:39], off nt
	s_nop 0
	global_load_dwordx4 v[38:41], v[42:43], off nt
	s_nop 0
	global_load_dwordx4 v[42:45], v[46:47], off nt
	s_nop 0
	global_load_dwordx4 v[46:49], v[50:51], off nt
	s_nop 0
	global_load_dwordx4 v[50:53], v[54:55], off nt
	s_nop 0
	global_load_dwordx4 v[54:57], v[58:59], off nt
	s_nop 0
	global_load_dwordx4 v[58:61], v[62:63], off nt
	v_lshl_add_u64 v[62:63], v[62:63], 0, s[8:9]
	global_load_dwordx4 v[62:65], v[62:63], off nt
	s_waitcnt vmcnt(24)
	s_branch .LBB0_417

; #define LAS __attribute__((address_space(3)))
; __device__ __forceinline__ TrItem tr_decode(const Args& a, int it) {
;     unsigned char* ws = a.ws;
;     constexpr int T_IN = 32 * (INCOLS / 64), T_OUT = 32 * (DM / 64), T_GU1 = 32 * (4096 / 64), T_DN1 = 32 * (DM / 64);
;     TrItem t; int r = it;
;     if (r < T_IN) { const int kb = r & 31, nb = r >> 5; t.N = INCOLS; t.src = a.in[I_WIN] + (size_t)(64 * kb) * INCOLS + 64 * nb; t.dst = (bf16*)(ws + WS_WIN) + (size_t)(64 * nb) * DM + 64 * kb; return t; } r -= T_IN;
;     if (r < T_OUT) { const int kb = r & 31, nb = r >> 5; t.N = DM; t.src = a.in[I_WOUT] + (size_t)(64 * kb) * DM + 64 * nb; t.dst = (bf16*)(ws + WS_WOUT) + (size_t)(64 * nb) * DM + 64 * kb; return t; } r -= T_OUT;
;     if (r < NEXP * T_GU1) { const int e = r / T_GU1, q = r % T_GU1, kb = q & 31, nb = q >> 5, n0 = 64 * nb;
;         const int drow0 = n0 < 2048 ? (n0 >> 7) * 256 + (n0 & 127) : ((n0 - 2048) >> 7) * 256 + 128 + ((n0 - 2048) & 127);
;         t.N = 4096; t.src = a.in[I_WGU] + (size_t)e * DM * 4096 + (size_t)(64 * kb) * 4096 + n0; t.dst = (bf16*)(ws + WS_WGU) + (size_t)e * 4096 * DM + (size_t)drow0 * DM + 64 * kb; return t; } r -= NEXP * T_GU1;
;     { const int e = r / T_DN1, q = r % T_DN1, kb = q & 31, nb = q >> 5;
;         t.N = DM; t.src = a.in[I_WDN] + (size_t)e * DM * DM + (size_t)(64 * kb) * DM + 64 * nb; t.dst = (bf16*)(ws + WS_WDN) + (size_t)e * DM * DM + (size_t)(64 * nb) * DM + 64 * kb; return t; }
; }
; __device__ __forceinline__ void tr_load(const TrItem& t, f32x4 (&ra)[8], f32x4 (&rb)[8], int lane) {
;     const int q = lane >> 4, n4 = lane & 15;
;     const float* p = t.src + (size_t)(2 * q) * t.N + 4 * n4;
; #pragma unroll
;     for (int i = 0; i < 8; ++i) { ra[i] = __builtin_nontemporal_load((const f32x4*)(p + (size_t)(8 * i) * t.N)); rb[i] = __builtin_nontemporal_load((const f32x4*)(p + (size_t)(8 * i + 1) * t.N)); }
; }
; __device__ __forceinline__ void conv_items(const Args& a, LAS unsigned char* lds, int it0, int it1, int vcu, int G, int lane, int wave) {
;     LAS unsigned* scr = (LAS unsigned*)(lds + wave * 16384);
;     const int gw = vcu * NWAVES + wave, NGW = G * NWAVES;
;     f32x4 ra[8], rb[8], na[8], nb_[8];
;     int it = it0 + gw;
;     if (it >= it1) return;
;     TrItem cur = tr_decode(a, it);
;     tr_load(cur, ra, rb, lane);
.LBB0_523:
	v_readlane_b32 s9, v246, 11
	s_waitcnt vmcnt(11)
	v_lshrrev_b32_e32 v66, 3, v194
	s_add_i32 s8, s52, 0
	s_lshl_b32 s33, s9, 3
	s_lshl_b64 s[4:5], s[4:5], 12
	v_and_b32_e32 v1, 6, v66
	s_add_u32 s2, s12, s4
	s_waitcnt lgkmcnt(0)
	v_mul_u32_u24_e32 v2, s16, v1
	v_lshlrev_b32_e32 v67, 2, v194
	s_addc_u32 s4, s13, s5
	s_lshl_b64 s[0:1], s[0:1], 1
	v_lshlrev_b32_e32 v130, 2, v2
	v_mov_b32_e32 v131, 0
	v_and_b32_e32 v132, 60, v67
	s_add_u32 s12, s2, s0
	v_lshl_add_u64 v[2:3], s[6:7], 0, v[130:131]
	v_lshlrev_b32_e32 v130, 2, v132
	s_addc_u32 s13, s4, s1
	v_lshl_add_u64 v[2:3], v[2:3], 0, v[130:131]
	s_lshl_b64 s[0:1], s[16:17], 2
	s_mov_b32 s3, 0
	v_lshl_add_u64 v[10:11], v[2:3], 0, s[0:1]
	s_mul_i32 s2, s16, 28
	global_load_dwordx4 v[2:5], v[2:3], off nt
	s_nop 0
	global_load_dwordx4 v[6:9], v[10:11], off nt
	v_lshl_add_u64 v[10:11], v[10:11], 0, s[2:3]
	v_lshl_add_u64 v[18:19], v[10:11], 0, s[0:1]
	global_load_dwordx4 v[10:13], v[10:11], off nt
	s_nop 0
	global_load_dwordx4 v[14:17], v[18:19], off nt
	v_lshl_add_u64 v[18:19], v[18:19], 0, s[2:3]
	v_lshl_add_u64 v[26:27], v[18:19], 0, s[0:1]
	global_load_dwordx4 v[18:21], v[18:19], off nt
	s_nop 0
	global_load_dwordx4 v[22:25], v[26:27], off nt
	v_lshl_add_u64 v[26:27], v[26:27], 0, s[2:3]
	v_lshl_add_u64 v[34:35], v[26:27], 0, s[0:1]
	v_lshl_add_u64 v[38:39], v[34:35], 0, s[2:3]
	v_lshl_add_u64 v[42:43], v[38:39], 0, s[0:1]
	v_lshl_add_u64 v[46:47], v[42:43], 0, s[2:3]
	s_waitcnt vmcnt(14)
	v_lshl_add_u64 v[50:51], v[46:47], 0, s[0:1]
	s_waitcnt vmcnt(12)
	v_lshl_add_u64 v[54:55], v[50:51], 0, s[2:3]
	v_lshl_add_u64 v[58:59], v[54:55], 0, s[0:1]
	v_lshl_add_u64 v[62:63], v[58:59], 0, s[2:3]
	global_load_dwordx4 v[26:29], v[26:27], off nt
	s_nop 0
	global_load_dwordx4 v[30:33], v[34:35], off nt
	v_lshlrev_b32_e32 v77, 3, v0
	global_load_dwordx4 v[34:37], v[38:39], off nt
	v_bitop3_b32 v78, v66, 28, v67 bitop3:0x48
	global_load_dwordx4 v[38:41], v[42:43], off nt
	v_and_b32_e32 v134, 56, v77
	global_load_dwordx4 v[42:45], v[46:47], off nt
	v_lshlrev_b32_e32 v77, 7, v66
	global_load_dwordx4 v[46:49], v[50:51], off nt
	v_lshlrev_b32_e32 v78, 2, v78
	global_load_dwordx4 v[50:53], v[54:55], off nt
	v_add3_u32 v133, s8, v77, v78
	global_load_dwordx4 v[54:57], v[58:59], off nt
	v_or_b32_e32 v77, 8, v66
	global_load_dwordx4 v[58:61], v[62:63], off nt
	v_lshl_add_u64 v[62:63], v[62:63], 0, s[0:1]
	global_load_dwordx4 v[62:65], v[62:63], off nt
	v_bitop3_b32 v80, v77, 28, v67 bitop3:0x48
	v_lshlrev_b32_e32 v79, 7, v77
	v_lshlrev_b32_e32 v80, 2, v80
	v_lshlrev_b32_e32 v138, 12, v77
	v_or_b32_e32 v77, 16, v66
	v_add3_u32 v135, s8, v79, v80
	v_bitop3_b32 v80, v77, 28, v67 bitop3:0x48
	v_lshlrev_b32_e32 v79, 7, v77
	v_lshlrev_b32_e32 v80, 2, v80
	v_lshlrev_b32_e32 v140, 12, v77
	v_or_b32_e32 v77, 24, v66
	v_add3_u32 v152, s8, v79, v80
	v_bitop3_b32 v80, v77, 28, v67 bitop3:0x48
	s_add_u32 s34, s92, 0x70800000
	v_lshlrev_b32_e32 v79, 7, v77
	v_lshlrev_b32_e32 v80, 2, v80
	v_lshlrev_b32_e32 v142, 12, v77
	v_or_b32_e32 v77, 32, v66
	s_addc_u32 s35, s93, 0
	v_lshlrev_b32_e32 v68, 9, v0
	v_lshrrev_b32_e32 v69, 2, v194
	v_add3_u32 v153, s8, v79, v80
	v_lshlrev_b32_e32 v79, 7, v77
	v_lshlrev_b32_e32 v144, 12, v77
	v_or_b32_e32 v77, 40, v66
	s_add_u32 s44, s92, 0x50800000
	v_and_b32_e32 v68, 0x1e00, v68
	v_and_b32_e32 v69, 12, v69
	v_add3_u32 v154, s8, v79, v78
	v_bitop3_b32 v79, v77, 28, v67 bitop3:0x48
	s_addc_u32 s45, s93, 0
	v_add3_u32 v68, s8, v68, v69
	v_lshlrev_b32_e32 v69, 4, v0
	v_mov_b32_e32 v71, 0x70
	s_movk_i32 s1, 0x50
	v_lshlrev_b32_e32 v136, 12, v66
	v_lshlrev_b32_e32 v78, 7, v77
	v_lshlrev_b32_e32 v79, 2, v79
	v_lshlrev_b32_e32 v146, 12, v77
	v_or_b32_e32 v77, 48, v66
	v_or_b32_e32 v66, 56, v66
	s_add_u32 s4, s92, 0x1a00000
	s_movk_i32 s0, 0x70
	v_bitop3_b32 v76, v69, s1, v71 bitop3:0x6c
	s_movk_i32 s1, 0x60
	v_add3_u32 v155, s8, v78, v79
	v_bitop3_b32 v79, v77, 28, v67 bitop3:0x48
	v_bitop3_b32 v67, v66, 28, v67 bitop3:0x48
	s_addc_u32 s5, s93, 0
	v_and_b32_e32 v70, 0x70, v69
	v_bitop3_b32 v72, v69, 16, v71 bitop3:0x6c
	v_bitop3_b32 v73, v69, 32, v71 bitop3:0x6c
	v_bitop3_b32 v74, v69, 48, v71 bitop3:0x6c
	v_bitop3_b32 v75, v69, 64, v71 bitop3:0x6c
	v_bitop3_b32 v71, v69, s1, v71 bitop3:0x6c
	v_bitop3_b32 v69, v69, s0, v69 bitop3:0xc
	v_lshlrev_b32_e32 v78, 7, v77
	v_lshlrev_b32_e32 v79, 2, v79
	v_lshlrev_b32_e32 v148, 12, v77
	v_lshlrev_b32_e32 v77, 7, v66
	v_lshlrev_b32_e32 v67, 2, v67
	s_add_u32 s6, s92, 0x200000
	v_mov_b32_e32 v137, v131
	v_mov_b32_e32 v139, v131
	v_mov_b32_e32 v141, v131
	v_mov_b32_e32 v143, v131
	v_mov_b32_e32 v145, v131
	v_mov_b32_e32 v147, v131
	v_add3_u32 v156, s8, v78, v79
	v_mov_b32_e32 v149, v131
	v_add3_u32 v157, s8, v77, v67
	v_lshlrev_b32_e32 v150, 12, v66
	v_mov_b32_e32 v151, v131
	s_addc_u32 s7, s93, 0
	s_lshl_b32 s53, s9, 4
	v_add_u32_e32 v158, v68, v70
	v_add_u32_e32 v159, v68, v72
	v_add_u32_e32 v160, v68, v73
	v_add_u32_e32 v161, v68, v74
	v_add_u32_e32 v162, v68, v75
	v_add_u32_e32 v163, v68, v76
	v_add_u32_e32 v164, v68, v71
	v_add_u32_e32 v165, v68, v69
	s_branch .LBB0_526
; #define LAS __attribute__((address_space(3)))
; #define LDS_WAIT() asm volatile("s_waitcnt lgkmcnt(0)" ::: "memory")
; __device__ __forceinline__ unsigned cvt2bf(float lo, float hi) { const f32x2_t v = {lo, hi}; const bf16x2_t r = __builtin_convertvector(v, bf16x2_t); return __builtin_bit_cast(unsigned, r); }
; __device__ __forceinline__ void tr_store(const TrItem& t, const f32x4 (&ra)[8], const f32x4 (&rb)[8], LAS unsigned* scr, int lane) {
;     const int q = lane >> 4, n4 = lane & 15;
; #pragma unroll
;     for (int i = 0; i < 8; ++i)
; #pragma unroll
;         for (int j = 0; j < 4; ++j) scr[(4 * n4 + j) * 32 + ((i ^ (n4 & 7)) << 2) + q] = cvt2bf(ra[i][j], rb[i][j]);
;     LDS_WAIT(); asm volatile("" ::: "memory");
;     const int nr = lane >> 3, ch = lane & 7;
; #pragma unroll
;     for (int i = 0; i < 8; ++i) { const int n = nr + 8 * i; const v4u v = *(const LAS v4u*)(scr + n * 32 + ((ch ^ ((n >> 2) & 7)) << 2));
;         __builtin_nontemporal_store(v, (v4u*)(t.dst + (size_t)n * DM + 8 * ch)); }
;     LDS_WAIT(); asm volatile("" ::: "memory");
; }
; __device__ __forceinline__ void conv_items(const Args& a, LAS unsigned char* lds, int it0, int it1, int vcu, int G, int lane, int wave) {
;     ...
;         it = nx; nx = it + NGW; has = nx < it1;
.Lcvw_3:
	s_waitcnt vmcnt(8)
.LBB0_524:
	v_cvt_pk_bf16_f32 v166, v66, v74
	v_cvt_pk_bf16_f32 v167, v67, v75
	ds_write2_b32 v158, v166, v167 offset1:32
	v_cvt_pk_bf16_f32 v166, v68, v76
	v_cvt_pk_bf16_f32 v167, v69, v77
	ds_write2_b32 v158, v166, v167 offset0:64 offset1:96
	v_cvt_pk_bf16_f32 v166, v70, v86
	v_cvt_pk_bf16_f32 v167, v71, v87
	ds_write2_b32 v159, v166, v167 offset1:32
	v_cvt_pk_bf16_f32 v166, v72, v88
	v_cvt_pk_bf16_f32 v167, v73, v89
	ds_write2_b32 v159, v166, v167 offset0:64 offset1:96
	v_cvt_pk_bf16_f32 v166, v78, v98
	v_cvt_pk_bf16_f32 v167, v79, v99
	ds_write2_b32 v160, v166, v167 offset1:32
	v_cvt_pk_bf16_f32 v166, v80, v100
	v_cvt_pk_bf16_f32 v167, v81, v101
	ds_write2_b32 v160, v166, v167 offset0:64 offset1:96
	v_cvt_pk_bf16_f32 v166, v82, v106
	v_cvt_pk_bf16_f32 v167, v83, v107
	ds_write2_b32 v161, v166, v167 offset1:32
	v_cvt_pk_bf16_f32 v166, v84, v108
	v_cvt_pk_bf16_f32 v167, v85, v109
	ds_write2_b32 v161, v166, v167 offset0:64 offset1:96
	v_cvt_pk_bf16_f32 v166, v90, v114
	v_cvt_pk_bf16_f32 v167, v91, v115
	ds_write2_b32 v162, v166, v167 offset1:32
	v_cvt_pk_bf16_f32 v166, v92, v116
	v_cvt_pk_bf16_f32 v167, v93, v117
	ds_write2_b32 v162, v166, v167 offset0:64 offset1:96
	v_cvt_pk_bf16_f32 v166, v94, v118
	v_cvt_pk_bf16_f32 v167, v95, v119
	ds_write2_b32 v163, v166, v167 offset1:32
	v_cvt_pk_bf16_f32 v166, v96, v120
	v_cvt_pk_bf16_f32 v167, v97, v121
	ds_write2_b32 v163, v166, v167 offset0:64 offset1:96
	v_cvt_pk_bf16_f32 v166, v102, v122
	v_cvt_pk_bf16_f32 v167, v103, v123
	s_lshl_b64 s[0:1], s[0:1], 12
	ds_write2_b32 v164, v166, v167 offset1:32
	v_cvt_pk_bf16_f32 v166, v104, v124
	v_cvt_pk_bf16_f32 v167, v105, v125
	s_add_u32 s2, s22, s0
	ds_write2_b32 v164, v166, v167 offset0:64 offset1:96
	v_cvt_pk_bf16_f32 v166, v110, v126
	v_cvt_pk_bf16_f32 v167, v111, v127
	s_addc_u32 s8, s23, s1
	s_lshl_b64 s[0:1], s[12:13], 1
	ds_write2_b32 v165, v166, v167 offset1:32
	v_cvt_pk_bf16_f32 v166, v112, v128
	v_cvt_pk_bf16_f32 v167, v113, v129
	s_add_u32 s12, s2, s0
	ds_write2_b32 v165, v166, v167 offset0:64 offset1:96
	s_addc_u32 s13, s8, s1
	s_add_i32 s28, s54, s33
	s_lshl_b64 s[0:1], s[16:17], 12
	s_waitcnt lgkmcnt(0)
	s_add_u32 s2, s20, s0
	s_addc_u32 s8, s21, s1
	s_lshl_b64 s[0:1], s[18:19], 1
	ds_read_b128 v[166:169], v133
	ds_read_b128 v[170:173], v135
	s_add_u32 s0, s2, s0
	s_addc_u32 s1, s8, s1
	v_lshl_add_u64 v[178:179], s[0:1], 0, v[130:131]
	v_lshl_add_u64 v[174:175], v[178:179], 0, v[136:137]
	s_waitcnt lgkmcnt(1)
	global_store_dwordx4 v[174:175], v[166:169], off nt
	ds_read_b128 v[166:169], v152
	v_lshl_add_u64 v[174:175], v[178:179], 0, v[138:139]
	s_waitcnt lgkmcnt(1)
	global_store_dwordx4 v[174:175], v[170:173], off nt
	ds_read_b128 v[170:173], v153
	v_lshl_add_u64 v[174:175], v[178:179], 0, v[140:141]
	s_waitcnt lgkmcnt(1)
	global_store_dwordx4 v[174:175], v[166:169], off nt
	ds_read_b128 v[166:169], v154
	v_lshl_add_u64 v[174:175], v[178:179], 0, v[142:143]
	s_waitcnt lgkmcnt(1)
	global_store_dwordx4 v[174:175], v[170:173], off nt
	v_lshl_add_u64 v[174:175], v[178:179], 0, v[144:145]
	ds_read_b128 v[170:173], v155
	s_waitcnt lgkmcnt(1)
	global_store_dwordx4 v[174:175], v[166:169], off nt
	ds_read_b128 v[166:169], v156
	ds_read_b128 v[174:177], v157
	v_lshl_add_u64 v[180:181], v[178:179], 0, v[146:147]
	s_waitcnt lgkmcnt(2)
	global_store_dwordx4 v[180:181], v[170:173], off nt
	s_cmp_gt_i32 s28, 0xe998
	s_cselect_b64 s[0:1], -1, 0
	v_lshl_add_u64 v[170:171], v[178:179], 0, v[148:149]
	s_waitcnt lgkmcnt(1)
	global_store_dwordx4 v[170:171], v[166:169], off nt
	s_nop 1
	v_lshl_add_u64 v[166:167], v[178:179], 0, v[150:151]
	s_waitcnt lgkmcnt(0)
	global_store_dwordx4 v[166:167], v[174:177], off nt
	s_waitcnt lgkmcnt(0)

; #define LAS __attribute__((address_space(3)))
; __device__ __forceinline__ unsigned cvt2bf(float lo, float hi) { const f32x2_t v = {lo, hi}; const bf16x2_t r = __builtin_convertvector(v, bf16x2_t); return __builtin_bit_cast(unsigned, r); }
; __device__ __forceinline__ void tr_load(const TrItem& t, f32x4 (&ra)[8], f32x4 (&rb)[8], int lane) {
;     const int q = lane >> 4, n4 = lane & 15;
;     const float* p = t.src + (size_t)(2 * q) * t.N + 4 * n4;
; #pragma unroll
;     for (int i = 0; i < 8; ++i) { ra[i] = __builtin_nontemporal_load((const f32x4*)(p + (size_t)(8 * i) * t.N)); rb[i] = __builtin_nontemporal_load((const f32x4*)(p + (size_t)(8 * i + 1) * t.N)); }
; }
; __device__ __forceinline__ void tr_store(const TrItem& t, const f32x4 (&ra)[8], const f32x4 (&rb)[8], LAS unsigned* scr, int lane) {
;     const int q = lane >> 4, n4 = lane & 15;
; #pragma unroll
;     for (int i = 0; i < 8; ++i)
; #pragma unroll
;         for (int j = 0; j < 4; ++j) scr[(4 * n4 + j) * 32 + ((i ^ (n4 & 7)) << 2) + q] = cvt2bf(ra[i][j], rb[i][j]);
; __device__ __forceinline__ void conv_items(const Args& a, LAS unsigned char* lds, int it0, int it1, int vcu, int G, int lane, int wave) {
;     ...
;         int nx = it + NGW; bool has = nx < it1;
;         TrItem nxt = tr_decode(a, has ? nx : it);
;         if (has) tr_load(nxt, na, nb_, lane);
;         tr_store(cur, ra, rb, scr, lane);
.LBB0_541:
	v_mul_u32_u24_e32 v66, s26, v1
	v_lshlrev_b32_e32 v130, 2, v66
	v_lshl_add_u64 v[66:67], s[24:25], 0, v[130:131]
	v_lshlrev_b32_e32 v130, 2, v132
	v_lshl_add_u64 v[66:67], v[66:67], 0, v[130:131]
	s_lshl_b64 s[8:9], s[26:27], 2
	v_lshl_add_u64 v[70:71], v[66:67], 0, s[8:9]
	s_mul_i32 s2, s26, 28
	global_load_dwordx4 v[66:69], v[66:67], off nt
	s_nop 0
	global_load_dwordx4 v[74:77], v[70:71], off nt
	v_lshl_add_u64 v[70:71], v[70:71], 0, s[2:3]
	v_lshl_add_u64 v[78:79], v[70:71], 0, s[8:9]
	global_load_dwordx4 v[70:73], v[70:71], off nt
	s_nop 0
	global_load_dwordx4 v[86:89], v[78:79], off nt
	v_lshl_add_u64 v[78:79], v[78:79], 0, s[2:3]
	v_lshl_add_u64 v[82:83], v[78:79], 0, s[8:9]
	global_load_dwordx4 v[78:81], v[78:79], off nt
	s_nop 0
	global_load_dwordx4 v[98:101], v[82:83], off nt
	v_lshl_add_u64 v[82:83], v[82:83], 0, s[2:3]
	v_lshl_add_u64 v[90:91], v[82:83], 0, s[8:9]
	v_lshl_add_u64 v[94:95], v[90:91], 0, s[2:3]
	global_load_dwordx4 v[82:85], v[82:83], off nt
	s_nop 0
	global_load_dwordx4 v[106:109], v[90:91], off nt
	s_nop 0
	global_load_dwordx4 v[90:93], v[94:95], off nt
	v_lshl_add_u64 v[94:95], v[94:95], 0, s[8:9]
	v_lshl_add_u64 v[102:103], v[94:95], 0, s[2:3]
	global_load_dwordx4 v[114:117], v[94:95], off nt
	s_nop 0
	global_load_dwordx4 v[94:97], v[102:103], off nt
	v_lshl_add_u64 v[102:103], v[102:103], 0, s[8:9]
	v_lshl_add_u64 v[110:111], v[102:103], 0, s[2:3]
	global_load_dwordx4 v[118:121], v[102:103], off nt
	s_nop 0
	global_load_dwordx4 v[102:105], v[110:111], off nt
	v_lshl_add_u64 v[110:111], v[110:111], 0, s[8:9]
	v_lshl_add_u64 v[126:127], v[110:111], 0, s[2:3]
	global_load_dwordx4 v[122:125], v[110:111], off nt
	s_nop 0
	global_load_dwordx4 v[110:113], v[126:127], off nt
	v_lshl_add_u64 v[126:127], v[126:127], 0, s[8:9]
	global_load_dwordx4 v[126:129], v[126:127], off nt
	s_waitcnt vmcnt(30)
	v_cvt_pk_bf16_f32 v130, v2, v6
	v_cvt_pk_bf16_f32 v166, v3, v7
	ds_write2_b32 v158, v130, v166 offset1:32
	v_cvt_pk_bf16_f32 v130, v4, v8
	v_cvt_pk_bf16_f32 v166, v5, v9
	ds_write2_b32 v158, v130, v166 offset0:64 offset1:96
	s_waitcnt vmcnt(28)
	v_cvt_pk_bf16_f32 v130, v10, v14
	v_cvt_pk_bf16_f32 v166, v11, v15
	ds_write2_b32 v159, v130, v166 offset1:32
	v_cvt_pk_bf16_f32 v130, v12, v16
	v_cvt_pk_bf16_f32 v166, v13, v17
	ds_write2_b32 v159, v130, v166 offset0:64 offset1:96
	s_waitcnt vmcnt(26)
	v_cvt_pk_bf16_f32 v130, v18, v22
	v_cvt_pk_bf16_f32 v166, v19, v23
	ds_write2_b32 v160, v130, v166 offset1:32
	v_cvt_pk_bf16_f32 v130, v20, v24
	v_cvt_pk_bf16_f32 v166, v21, v25
	ds_write2_b32 v160, v130, v166 offset0:64 offset1:96
	s_waitcnt vmcnt(24)
	v_cvt_pk_bf16_f32 v130, v26, v30
	v_cvt_pk_bf16_f32 v166, v27, v31
	ds_write2_b32 v161, v130, v166 offset1:32
	v_cvt_pk_bf16_f32 v130, v28, v32
	v_cvt_pk_bf16_f32 v166, v29, v33
	ds_write2_b32 v161, v130, v166 offset0:64 offset1:96
	s_waitcnt vmcnt(22)
	v_cvt_pk_bf16_f32 v130, v34, v38
	v_cvt_pk_bf16_f32 v166, v35, v39
	ds_write2_b32 v162, v130, v166 offset1:32
	v_cvt_pk_bf16_f32 v130, v36, v40
	v_cvt_pk_bf16_f32 v166, v37, v41
	ds_write2_b32 v162, v130, v166 offset0:64 offset1:96
	s_waitcnt vmcnt(20)
	v_cvt_pk_bf16_f32 v130, v42, v46
	v_cvt_pk_bf16_f32 v166, v43, v47
	ds_write2_b32 v163, v130, v166 offset1:32
	v_cvt_pk_bf16_f32 v130, v44, v48
	v_cvt_pk_bf16_f32 v166, v45, v49
	ds_write2_b32 v163, v130, v166 offset0:64 offset1:96
	s_waitcnt vmcnt(18)
	v_cvt_pk_bf16_f32 v130, v50, v54
	v_cvt_pk_bf16_f32 v166, v51, v55
	ds_write2_b32 v164, v130, v166 offset1:32
	v_cvt_pk_bf16_f32 v130, v52, v56
	v_cvt_pk_bf16_f32 v166, v53, v57
	ds_write2_b32 v164, v130, v166 offset0:64 offset1:96
	s_waitcnt vmcnt(16)
	v_cvt_pk_bf16_f32 v130, v58, v62
	v_cvt_pk_bf16_f32 v166, v59, v63
	ds_write2_b32 v165, v130, v166 offset1:32
	v_cvt_pk_bf16_f32 v130, v60, v64
	v_cvt_pk_bf16_f32 v166, v61, v65
	ds_write2_b32 v165, v130, v166 offset0:64 offset1:96
	s_branch .Lcvj_3

; #define LAS __attribute__((address_space(3)))
; #define LDS_WAIT() asm volatile("s_waitcnt lgkmcnt(0)" ::: "memory")
; __device__ __forceinline__ TrItem tr_decode(const Args& a, int it) {
;     ...
;     if (r < T_IN) { const int kb = r & 31, nb = r >> 5; t.N = INCOLS; t.src = a.in[I_WIN] + (size_t)(64 * kb) * INCOLS + 64 * nb; t.dst = (bf16*)(ws + WS_WIN) + (size_t)(64 * nb) * DM + 64 * kb; return t; } r -= T_IN;
;     if (r < T_OUT) { const int kb = r & 31, nb = r >> 5; t.N = DM; t.src = a.in[I_WOUT] + (size_t)(64 * kb) * DM + 64 * nb; t.dst = (bf16*)(ws + WS_WOUT) + (size_t)(64 * nb) * DM + 64 * kb; return t; } r -= T_OUT;
;     if (r < NEXP * T_GU1) { const int e = r / T_GU1, q = r % T_GU1, kb = q & 31, nb = q >> 5, n0 = 64 * nb;
;         const int drow0 = n0 < 2048 ? (n0 >> 7) * 256 + (n0 & 127) : ((n0 - 2048) >> 7) * 256 + 128 + ((n0 - 2048) & 127);
;         t.N = 4096; t.src = a.in[I_WGU] + (size_t)e * DM * 4096 + (size_t)(64 * kb) * 4096 + n0; t.dst = (bf16*)(ws + WS_WGU) + (size_t)e * 4096 * DM + (size_t)drow0 * DM + 64 * kb; return t; } r -= NEXP * T_GU1;
;     { const int e = r / T_DN1, q = r % T_DN1, kb = q & 31, nb = q >> 5;
;         t.N = DM; t.src = a.in[I_WDN] + (size_t)e * DM * DM + (size_t)(64 * kb) * DM + 64 * nb; t.dst = (bf16*)(ws + WS_WDN) + (size_t)e * DM * DM + (size_t)(64 * nb) * DM + 64 * kb; return t; }
; __device__ __forceinline__ void tr_store(const TrItem& t, const f32x4 (&ra)[8], const f32x4 (&rb)[8], LAS unsigned* scr, int lane) {
;     ...
;     LDS_WAIT(); asm volatile("" ::: "memory");
;     const int nr = lane >> 3, ch = lane & 7;
; #pragma unroll
;     for (int i = 0; i < 8; ++i) { const int n = nr + 8 * i; const v4u v = *(const LAS v4u*)(scr + n * 32 + ((ch ^ ((n >> 2) & 7)) << 2));
;         __builtin_nontemporal_store(v, (v4u*)(t.dst + (size_t)n * DM + 8 * ch)); }
;     LDS_WAIT(); asm volatile("" ::: "memory");
; }
; __device__ __forceinline__ void conv_items(const Args& a, LAS unsigned char* lds, int it0, int it1, int vcu, int G, int lane, int wave) {
;     ...
;         if (!has) break;
;         it = nx; nx = it + NGW; has = nx < it1;
;         cur = tr_decode(a, has ? nx : it);
.Lcvj_3:
	s_waitcnt lgkmcnt(0)
	ds_read_b128 v[166:169], v133
	ds_read_b128 v[170:173], v135
	v_lshlrev_b32_e32 v130, 1, v134
	v_lshl_add_u64 v[178:179], s[12:13], 0, v[130:131]
	v_lshl_add_u64 v[174:175], v[178:179], 0, v[136:137]
	s_waitcnt lgkmcnt(1)
	global_store_dwordx4 v[174:175], v[166:169], off nt
	ds_read_b128 v[166:169], v152
	v_lshl_add_u64 v[174:175], v[178:179], 0, v[138:139]
	s_waitcnt lgkmcnt(1)
	global_store_dwordx4 v[174:175], v[170:173], off nt
	ds_read_b128 v[170:173], v153
	v_lshl_add_u64 v[174:175], v[178:179], 0, v[140:141]
	s_waitcnt lgkmcnt(1)
	global_store_dwordx4 v[174:175], v[166:169], off nt
	ds_read_b128 v[166:169], v154
	v_lshl_add_u64 v[174:175], v[178:179], 0, v[142:143]
	s_waitcnt lgkmcnt(1)
	global_store_dwordx4 v[174:175], v[170:173], off nt
	v_lshl_add_u64 v[174:175], v[178:179], 0, v[144:145]
	ds_read_b128 v[170:173], v155
	s_waitcnt lgkmcnt(1)
	global_store_dwordx4 v[174:175], v[166:169], off nt
	ds_read_b128 v[166:169], v156
	ds_read_b128 v[174:177], v157
	v_lshl_add_u64 v[180:181], v[178:179], 0, v[146:147]
	s_waitcnt lgkmcnt(2)
	global_store_dwordx4 v[180:181], v[170:173], off nt
	s_and_b64 vcc, exec, s[0:1]
	s_mov_b64 s[0:1], -1
	v_lshl_add_u64 v[170:171], v[178:179], 0, v[148:149]
	s_waitcnt lgkmcnt(1)
	global_store_dwordx4 v[170:171], v[166:169], off nt
	s_nop 1
	v_lshl_add_u64 v[166:167], v[178:179], 0, v[150:151]
	s_waitcnt lgkmcnt(0)
	global_store_dwordx4 v[166:167], v[174:177], off nt
	s_waitcnt lgkmcnt(0)
	s_cbranch_vccnz .LBB0_525
	s_add_i32 s2, s53, s28
	s_cmp_lt_i32 s2, 0xe999
	s_cselect_b64 s[24:25], -1, 0
	s_and_b64 s[0:1], s[24:25], exec
	s_cselect_b32 s55, s2, s54
	s_cmpk_gt_i32 s55, 0xbff
	s_mov_b64 s[30:31], -1
	s_cbranch_scc0 .LBB0_560
	s_cmpk_gt_u32 s55, 0xfff
	s_cbranch_scc0 .LBB0_554
	s_cmp_gt_u32 s55, 0x10fff
	s_mov_b64 s[28:29], -1
	s_cbranch_scc0 .LBB0_547
	s_add_i32 s0, s55, 0xfffef000
	s_lshr_b32 s2, s0, 10
	s_lshl_b64 s[0:1], s[2:3], 24
	v_readlane_b32 s56, v246, 0
	v_readlane_b32 s57, v246, 1
	s_add_u32 s0, s56, s0
	s_addc_u32 s1, s57, s1
	s_lshl_b32 s8, s55, 6
	s_and_b32 s12, s8, 0x7c0
	s_lshl_b32 s8, s12, 13
	s_add_u32 s8, s0, s8
	s_addc_u32 s9, s1, 0
	s_lshl_b32 s0, s55, 1
	s_and_b32 s0, s0, 0x7c0
	s_lshl_b32 s14, s0, 2
	s_add_u32 s26, s8, s14
	s_addc_u32 s27, s9, 0
	s_lshl_b64 s[8:9], s[2:3], 23
	s_add_u32 s22, s34, s8
	v_readlane_b32 s58, v246, 2
	v_readlane_b32 s59, v246, 3
	v_readlane_b32 s60, v246, 4
	v_readlane_b32 s61, v246, 5
	v_readlane_b32 s62, v246, 6
	v_readlane_b32 s63, v246, 7
	s_mov_b32 s13, s3
	s_mov_b32 s1, s3
	s_addc_u32 s23, s35, s9
	s_mov_b64 s[28:29], 0

; __device__ __forceinline__ void tr_load(const TrItem& t, f32x4 (&ra)[8], f32x4 (&rb)[8], int lane) {
;     const int q = lane >> 4, n4 = lane & 15;
;     const float* p = t.src + (size_t)(2 * q) * t.N + 4 * n4;
; #pragma unroll
;     for (int i = 0; i < 8; ++i) { ra[i] = __builtin_nontemporal_load((const f32x4*)(p + (size_t)(8 * i) * t.N)); rb[i] = __builtin_nontemporal_load((const f32x4*)(p + (size_t)(8 * i + 1) * t.N)); }
; }
; __device__ __forceinline__ void conv_items(const Args& a, LAS unsigned char* lds, int it0, int it1, int vcu, int G, int lane, int wave) {
;     ...
;         it = nx; nx = it + NGW; has = nx < it1;
;         cur = tr_decode(a, has ? nx : it);
;         if (has) tr_load(cur, ra, rb, lane);
;         tr_store(nxt, na, nb_, scr, lane);
.LBB0_562:
	v_mul_u32_u24_e32 v2, s28, v1
	v_lshlrev_b32_e32 v2, 2, v2
	v_mov_b32_e32 v3, v131
	v_lshl_add_u64 v[2:3], s[26:27], 0, v[2:3]
	v_lshlrev_b32_e32 v4, 2, v132
	v_mov_b32_e32 v5, v131
	v_lshl_add_u64 v[2:3], v[2:3], 0, v[4:5]
	s_lshl_b64 s[8:9], s[28:29], 2
	v_lshl_add_u64 v[10:11], v[2:3], 0, s[8:9]
	s_mul_i32 s2, s28, 28
	global_load_dwordx4 v[2:5], v[2:3], off nt
	s_nop 0
	global_load_dwordx4 v[6:9], v[10:11], off nt
	v_lshl_add_u64 v[10:11], v[10:11], 0, s[2:3]
	v_lshl_add_u64 v[18:19], v[10:11], 0, s[8:9]
	global_load_dwordx4 v[10:13], v[10:11], off nt
	s_nop 0
	global_load_dwordx4 v[14:17], v[18:19], off nt
	v_lshl_add_u64 v[18:19], v[18:19], 0, s[2:3]
	v_lshl_add_u64 v[26:27], v[18:19], 0, s[8:9]
	global_load_dwordx4 v[18:21], v[18:19], off nt
	s_nop 0
	global_load_dwordx4 v[22:25], v[26:27], off nt
	v_lshl_add_u64 v[26:27], v[26:27], 0, s[2:3]
	v_lshl_add_u64 v[34:35], v[26:27], 0, s[8:9]
	v_lshl_add_u64 v[38:39], v[34:35], 0, s[2:3]
	v_lshl_add_u64 v[42:43], v[38:39], 0, s[8:9]
	v_lshl_add_u64 v[46:47], v[42:43], 0, s[2:3]
	v_lshl_add_u64 v[50:51], v[46:47], 0, s[8:9]
	v_lshl_add_u64 v[54:55], v[50:51], 0, s[2:3]
	v_lshl_add_u64 v[58:59], v[54:55], 0, s[8:9]
	v_lshl_add_u64 v[62:63], v[58:59], 0, s[2:3]
	global_load_dwordx4 v[26:29], v[26:27], off nt
	s_nop 0
	global_load_dwordx4 v[30:33], v[34:35], off nt
	s_nop 0
	global_load_dwordx4 v[34:37], v[38:39], off nt
	s_nop 0
	global_load_dwordx4 v[38:41], v[42:43], off nt
	s_nop 0
	global_load_dwordx4 v[42:45], v[46:47], off nt
	s_nop 0
	global_load_dwordx4 v[46:49], v[50:51], off nt
	s_nop 0
	global_load_dwordx4 v[50:53], v[54:55], off nt
	s_nop 0
	global_load_dwordx4 v[54:57], v[58:59], off nt
	s_nop 0
	global_load_dwordx4 v[58:61], v[62:63], off nt
	v_lshl_add_u64 v[62:63], v[62:63], 0, s[8:9]
	global_load_dwordx4 v[62:65], v[62:63], off nt
	s_waitcnt vmcnt(24)
	s_branch .LBB0_524

; #define LAS __attribute__((address_space(3)))
; __device__ __forceinline__ TrItem tr_decode(const Args& a, int it) {
;     unsigned char* ws = a.ws;
;     constexpr int T_IN = 32 * (INCOLS / 64), T_OUT = 32 * (DM / 64), T_GU1 = 32 * (4096 / 64), T_DN1 = 32 * (DM / 64);
;     TrItem t; int r = it;
;     if (r < T_IN) { const int kb = r & 31, nb = r >> 5; t.N = INCOLS; t.src = a.in[I_WIN] + (size_t)(64 * kb) * INCOLS + 64 * nb; t.dst = (bf16*)(ws + WS_WIN) + (size_t)(64 * nb) * DM + 64 * kb; return t; } r -= T_IN;
;     if (r < T_OUT) { const int kb = r & 31, nb = r >> 5; t.N = DM; t.src = a.in[I_WOUT] + (size_t)(64 * kb) * DM + 64 * nb; t.dst = (bf16*)(ws + WS_WOUT) + (size_t)(64 * nb) * DM + 64 * kb; return t; } r -= T_OUT;
;     if (r < NEXP * T_GU1) { const int e = r / T_GU1, q = r % T_GU1, kb = q & 31, nb = q >> 5, n0 = 64 * nb;
;         const int drow0 = n0 < 2048 ? (n0 >> 7) * 256 + (n0 & 127) : ((n0 - 2048) >> 7) * 256 + 128 + ((n0 - 2048) & 127);
;         t.N = 4096; t.src = a.in[I_WGU] + (size_t)e * DM * 4096 + (size_t)(64 * kb) * 4096 + n0; t.dst = (bf16*)(ws + WS_WGU) + (size_t)e * 4096 * DM + (size_t)drow0 * DM + 64 * kb; return t; } r -= NEXP * T_GU1;
;     { const int e = r / T_DN1, q = r % T_DN1, kb = q & 31, nb = q >> 5;
;         t.N = DM; t.src = a.in[I_WDN] + (size_t)e * DM * DM + (size_t)(64 * kb) * DM + 64 * nb; t.dst = (bf16*)(ws + WS_WDN) + (size_t)e * DM * DM + (size_t)(64 * nb) * DM + 64 * kb; return t; }
; }
; __device__ __forceinline__ void tr_load(const TrItem& t, f32x4 (&ra)[8], f32x4 (&rb)[8], int lane) {
;     const int q = lane >> 4, n4 = lane & 15;
;     const float* p = t.src + (size_t)(2 * q) * t.N + 4 * n4;
; #pragma unroll
;     for (int i = 0; i < 8; ++i) { ra[i] = __builtin_nontemporal_load((const f32x4*)(p + (size_t)(8 * i) * t.N)); rb[i] = __builtin_nontemporal_load((const f32x4*)(p + (size_t)(8 * i + 1) * t.N)); }
; }
; __device__ __forceinline__ void conv_items(const Args& a, LAS unsigned char* lds, int it0, int it1, int vcu, int G, int lane, int wave) {
;     LAS unsigned* scr = (LAS unsigned*)(lds + wave * 16384);
;     const int gw = vcu * NWAVES + wave, NGW = G * NWAVES;
;     f32x4 ra[8], rb[8], na[8], nb_[8];
;     int it = it0 + gw;
;     if (it >= it1) return;
;     TrItem cur = tr_decode(a, it);
;     tr_load(cur, ra, rb, lane);
.LBB0_643:
	v_readlane_b32 s9, v246, 11
	s_waitcnt vmcnt(11)
	v_lshrrev_b32_e32 v66, 3, v194
	s_add_i32 s8, s52, 0
	s_lshl_b32 s30, s9, 3
	s_lshl_b64 s[4:5], s[4:5], 12
	v_and_b32_e32 v135, 6, v66
	s_add_u32 s2, s10, s4
	v_mul_u32_u24_e32 v2, s12, v135
	v_lshlrev_b32_e32 v67, 2, v194
	s_addc_u32 s4, s11, s5
	s_lshl_b64 s[0:1], s[0:1], 1
	v_lshlrev_b32_e32 v130, 2, v2
	v_mov_b32_e32 v131, 0
	v_and_b32_e32 v132, 60, v67
	s_add_u32 s10, s2, s0
	v_lshl_add_u64 v[2:3], s[6:7], 0, v[130:131]
	v_lshlrev_b32_e32 v130, 2, v132
	s_addc_u32 s11, s4, s1
	v_lshl_add_u64 v[10:11], v[2:3], 0, v[130:131]
	s_lshl_b64 s[0:1], s[12:13], 2
	s_mov_b32 s3, 0
	v_lshl_add_u64 v[12:13], v[10:11], 0, s[0:1]
	s_mul_i32 s2, s12, 28
	v_lshl_add_u64 v[18:19], v[12:13], 0, s[2:3]
	v_lshl_add_u64 v[20:21], v[18:19], 0, s[0:1]
	v_lshl_add_u64 v[26:27], v[20:21], 0, s[2:3]
	v_lshl_add_u64 v[28:29], v[26:27], 0, s[0:1]
	v_lshl_add_u64 v[34:35], v[28:29], 0, s[2:3]
	v_lshl_add_u64 v[36:37], v[34:35], 0, s[0:1]
	v_lshl_add_u64 v[38:39], v[36:37], 0, s[2:3]
	v_lshl_add_u64 v[42:43], v[38:39], 0, s[0:1]
	v_lshl_add_u64 v[46:47], v[42:43], 0, s[2:3]
	s_waitcnt vmcnt(8)
	v_lshl_add_u64 v[50:51], v[46:47], 0, s[0:1]
	s_waitcnt vmcnt(6)
	v_lshl_add_u64 v[54:55], v[50:51], 0, s[2:3]
	v_lshl_add_u64 v[58:59], v[54:55], 0, s[0:1]
	v_lshl_add_u64 v[62:63], v[58:59], 0, s[2:3]
	global_load_dwordx4 v[2:5], v[10:11], off nt
	global_load_dwordx4 v[6:9], v[12:13], off nt
	s_nop 0
	global_load_dwordx4 v[10:13], v[18:19], off nt
	global_load_dwordx4 v[14:17], v[20:21], off nt
	s_nop 0
	global_load_dwordx4 v[18:21], v[26:27], off nt
	global_load_dwordx4 v[22:25], v[28:29], off nt
	s_nop 0
	global_load_dwordx4 v[26:29], v[34:35], off nt
	global_load_dwordx4 v[30:33], v[36:37], off nt
	v_or_b32_e32 v78, 8, v66
	global_load_dwordx4 v[34:37], v[38:39], off nt
	v_bitop3_b32 v80, v78, 28, v67 bitop3:0x48
	global_load_dwordx4 v[38:41], v[42:43], off nt
	v_lshlrev_b32_e32 v79, 7, v78
	global_load_dwordx4 v[42:45], v[46:47], off nt
	v_lshlrev_b32_e32 v80, 2, v80
	global_load_dwordx4 v[46:49], v[50:51], off nt
	v_lshlrev_b32_e32 v138, 12, v78
	global_load_dwordx4 v[50:53], v[54:55], off nt
	v_or_b32_e32 v78, 16, v66
	global_load_dwordx4 v[54:57], v[58:59], off nt
	v_lshlrev_b32_e32 v69, 2, v133
	global_load_dwordx4 v[58:61], v[62:63], off nt
	v_lshl_add_u64 v[62:63], v[62:63], 0, s[0:1]
	global_load_dwordx4 v[62:65], v[62:63], off nt
	v_add3_u32 v133, s8, v79, v80
	v_bitop3_b32 v80, v78, 28, v67 bitop3:0x48
	v_lshlrev_b32_e32 v79, 7, v78
	v_lshlrev_b32_e32 v80, 2, v80
	v_lshlrev_b32_e32 v140, 12, v78
	v_or_b32_e32 v78, 24, v66
	v_add3_u32 v152, s8, v79, v80
	v_bitop3_b32 v80, v78, 28, v67 bitop3:0x48
	v_bitop3_b32 v77, v66, 28, v67 bitop3:0x48
	v_lshlrev_b32_e32 v79, 7, v78
	v_lshlrev_b32_e32 v80, 2, v80
	v_lshlrev_b32_e32 v142, 12, v78
	v_or_b32_e32 v78, 32, v66
	s_add_u32 s31, s92, 0x70800000
	v_and_b32_e32 v134, 56, v1
	v_lshlrev_b32_e32 v1, 7, v66
	v_lshlrev_b32_e32 v77, 2, v77
	v_add3_u32 v153, s8, v79, v80
	v_lshlrev_b32_e32 v79, 7, v78
	s_addc_u32 s33, s93, 0
	v_lshlrev_b32_e32 v68, 9, v0
	v_add3_u32 v1, s8, v1, v77
	v_add3_u32 v154, s8, v79, v77
	v_or_b32_e32 v77, 40, v66
	s_add_u32 s34, s92, 0x50800000
	v_and_b32_e32 v68, 0x1e00, v68
	v_bitop3_b32 v79, v77, 28, v67 bitop3:0x48
	s_addc_u32 s35, s93, 0
	v_add3_u32 v68, s8, v68, v69
	v_lshlrev_b32_e32 v69, 4, v0
	v_mov_b32_e32 v71, 0x70
	s_movk_i32 s1, 0x50
	v_lshlrev_b32_e32 v136, 12, v66
	v_lshlrev_b32_e32 v144, 12, v78
	v_lshlrev_b32_e32 v78, 7, v77
	v_lshlrev_b32_e32 v79, 2, v79
	v_lshlrev_b32_e32 v146, 12, v77
	v_or_b32_e32 v77, 48, v66
	v_or_b32_e32 v66, 56, v66
	s_add_u32 s4, s92, 0x1a00000
	s_movk_i32 s0, 0x70
	v_bitop3_b32 v76, v69, s1, v71 bitop3:0x6c
	s_movk_i32 s1, 0x60
	v_add3_u32 v155, s8, v78, v79
	v_bitop3_b32 v79, v77, 28, v67 bitop3:0x48
	v_bitop3_b32 v67, v66, 28, v67 bitop3:0x48
	s_addc_u32 s5, s93, 0
	v_and_b32_e32 v70, 0x70, v69
	v_bitop3_b32 v72, v69, 16, v71 bitop3:0x6c
	v_bitop3_b32 v73, v69, 32, v71 bitop3:0x6c
	v_bitop3_b32 v74, v69, 48, v71 bitop3:0x6c
	v_bitop3_b32 v75, v69, 64, v71 bitop3:0x6c
	v_bitop3_b32 v71, v69, s1, v71 bitop3:0x6c
	v_bitop3_b32 v69, v69, s0, v69 bitop3:0xc
	v_lshlrev_b32_e32 v78, 7, v77
	v_lshlrev_b32_e32 v79, 2, v79
	v_lshlrev_b32_e32 v148, 12, v77
	v_lshlrev_b32_e32 v77, 7, v66
	v_lshlrev_b32_e32 v67, 2, v67
	s_add_u32 s6, s92, 0x200000
	v_mov_b32_e32 v137, v131
	v_mov_b32_e32 v139, v131
	v_mov_b32_e32 v141, v131
	v_mov_b32_e32 v143, v131
	v_mov_b32_e32 v145, v131
	v_mov_b32_e32 v147, v131
	v_add3_u32 v156, s8, v78, v79
	v_mov_b32_e32 v149, v131
	v_add3_u32 v157, s8, v77, v67
	v_lshlrev_b32_e32 v150, 12, v66
	v_mov_b32_e32 v151, v131
	s_addc_u32 s7, s93, 0
	s_lshl_b32 s36, s9, 4
	v_add_u32_e32 v158, v68, v70
	v_add_u32_e32 v159, v68, v72
	v_add_u32_e32 v160, v68, v73
	v_add_u32_e32 v161, v68, v74
	v_add_u32_e32 v162, v68, v75
	v_add_u32_e32 v163, v68, v76
	v_add_u32_e32 v164, v68, v71
	v_add_u32_e32 v165, v68, v69
	s_branch .LBB0_646
; #define LAS __attribute__((address_space(3)))
; #define LDS_WAIT() asm volatile("s_waitcnt lgkmcnt(0)" ::: "memory")
; __device__ __forceinline__ unsigned cvt2bf(float lo, float hi) { const f32x2_t v = {lo, hi}; const bf16x2_t r = __builtin_convertvector(v, bf16x2_t); return __builtin_bit_cast(unsigned, r); }
; __device__ __forceinline__ void tr_store(const TrItem& t, const f32x4 (&ra)[8], const f32x4 (&rb)[8], LAS unsigned* scr, int lane) {
;     const int q = lane >> 4, n4 = lane & 15;
; #pragma unroll
;     for (int i = 0; i < 8; ++i)
; #pragma unroll
;         for (int j = 0; j < 4; ++j) scr[(4 * n4 + j) * 32 + ((i ^ (n4 & 7)) << 2) + q] = cvt2bf(ra[i][j], rb[i][j]);
;     LDS_WAIT(); asm volatile("" ::: "memory");
;     const int nr = lane >> 3, ch = lane & 7;
; #pragma unroll
;     for (int i = 0; i < 8; ++i) { const int n = nr + 8 * i; const v4u v = *(const LAS v4u*)(scr + n * 32 + ((ch ^ ((n >> 2) & 7)) << 2));
;         __builtin_nontemporal_store(v, (v4u*)(t.dst + (size_t)n * DM + 8 * ch)); }
;     LDS_WAIT(); asm volatile("" ::: "memory");
; }
; __device__ __forceinline__ void conv_items(const Args& a, LAS unsigned char* lds, int it0, int it1, int vcu, int G, int lane, int wave) {
;     ...
;         it = nx; nx = it + NGW; has = nx < it1;
.Lcvw_4:
	s_waitcnt vmcnt(8)
.LBB0_644:
	v_cvt_pk_bf16_f32 v166, v66, v74
	v_cvt_pk_bf16_f32 v167, v67, v75
	ds_write2_b32 v158, v166, v167 offset1:32
	v_cvt_pk_bf16_f32 v166, v68, v76
	v_cvt_pk_bf16_f32 v167, v69, v77
	ds_write2_b32 v158, v166, v167 offset0:64 offset1:96
	v_cvt_pk_bf16_f32 v166, v70, v86
	v_cvt_pk_bf16_f32 v167, v71, v87
	ds_write2_b32 v159, v166, v167 offset1:32
	v_cvt_pk_bf16_f32 v166, v72, v88
	v_cvt_pk_bf16_f32 v167, v73, v89
	ds_write2_b32 v159, v166, v167 offset0:64 offset1:96
	v_cvt_pk_bf16_f32 v166, v78, v98
	v_cvt_pk_bf16_f32 v167, v79, v99
	ds_write2_b32 v160, v166, v167 offset1:32
	v_cvt_pk_bf16_f32 v166, v80, v100
	v_cvt_pk_bf16_f32 v167, v81, v101
	ds_write2_b32 v160, v166, v167 offset0:64 offset1:96
	v_cvt_pk_bf16_f32 v166, v82, v106
	v_cvt_pk_bf16_f32 v167, v83, v107
	ds_write2_b32 v161, v166, v167 offset1:32
	v_cvt_pk_bf16_f32 v166, v84, v108
	v_cvt_pk_bf16_f32 v167, v85, v109
	ds_write2_b32 v161, v166, v167 offset0:64 offset1:96
	v_cvt_pk_bf16_f32 v166, v90, v114
	v_cvt_pk_bf16_f32 v167, v91, v115
	ds_write2_b32 v162, v166, v167 offset1:32
	v_cvt_pk_bf16_f32 v166, v92, v116
	v_cvt_pk_bf16_f32 v167, v93, v117
	ds_write2_b32 v162, v166, v167 offset0:64 offset1:96
	v_cvt_pk_bf16_f32 v166, v94, v118
	v_cvt_pk_bf16_f32 v167, v95, v119
	ds_write2_b32 v163, v166, v167 offset1:32
	v_cvt_pk_bf16_f32 v166, v96, v120
	v_cvt_pk_bf16_f32 v167, v97, v121
	ds_write2_b32 v163, v166, v167 offset0:64 offset1:96
	v_cvt_pk_bf16_f32 v166, v102, v122
	v_cvt_pk_bf16_f32 v167, v103, v123
	s_lshl_b64 s[0:1], s[0:1], 12
	ds_write2_b32 v164, v166, v167 offset1:32
	v_cvt_pk_bf16_f32 v166, v104, v124
	v_cvt_pk_bf16_f32 v167, v105, v125
	s_add_u32 s2, s20, s0
	ds_write2_b32 v164, v166, v167 offset0:64 offset1:96
	v_cvt_pk_bf16_f32 v166, v110, v126
	v_cvt_pk_bf16_f32 v167, v111, v127
	s_addc_u32 s8, s21, s1
	s_lshl_b64 s[0:1], s[10:11], 1
	ds_write2_b32 v165, v166, v167 offset1:32
	v_cvt_pk_bf16_f32 v166, v112, v128
	v_cvt_pk_bf16_f32 v167, v113, v129
	s_add_u32 s10, s2, s0
	ds_write2_b32 v165, v166, v167 offset0:64 offset1:96
	s_addc_u32 s11, s8, s1
	s_add_i32 s26, s37, s30
	s_lshl_b64 s[0:1], s[12:13], 12
	s_waitcnt lgkmcnt(0)
	s_add_u32 s2, s18, s0
	s_addc_u32 s8, s19, s1
	s_lshl_b64 s[0:1], s[16:17], 1
	ds_read_b128 v[166:169], v1
	ds_read_b128 v[170:173], v133
	s_add_u32 s0, s2, s0
	s_addc_u32 s1, s8, s1
	v_lshl_add_u64 v[178:179], s[0:1], 0, v[130:131]
	v_lshl_add_u64 v[174:175], v[178:179], 0, v[136:137]
	s_waitcnt lgkmcnt(1)
	global_store_dwordx4 v[174:175], v[166:169], off nt
	ds_read_b128 v[166:169], v152
	v_lshl_add_u64 v[174:175], v[178:179], 0, v[138:139]
	s_waitcnt lgkmcnt(1)
	global_store_dwordx4 v[174:175], v[170:173], off nt
	ds_read_b128 v[170:173], v153
	v_lshl_add_u64 v[174:175], v[178:179], 0, v[140:141]
	s_waitcnt lgkmcnt(1)
	global_store_dwordx4 v[174:175], v[166:169], off nt
	ds_read_b128 v[166:169], v154
	v_lshl_add_u64 v[174:175], v[178:179], 0, v[142:143]
	s_waitcnt lgkmcnt(1)
	global_store_dwordx4 v[174:175], v[170:173], off nt
	v_lshl_add_u64 v[174:175], v[178:179], 0, v[144:145]
	ds_read_b128 v[170:173], v155
	s_waitcnt lgkmcnt(1)
	global_store_dwordx4 v[174:175], v[166:169], off nt
	ds_read_b128 v[166:169], v156
	ds_read_b128 v[174:177], v157
	v_lshl_add_u64 v[180:181], v[178:179], 0, v[146:147]
	s_waitcnt lgkmcnt(2)
	global_store_dwordx4 v[180:181], v[170:173], off nt
	s_cmp_gt_i32 s26, 0xe998
	s_cselect_b64 s[0:1], -1, 0
	v_lshl_add_u64 v[170:171], v[178:179], 0, v[148:149]
	s_waitcnt lgkmcnt(1)
	global_store_dwordx4 v[170:171], v[166:169], off nt
	s_nop 1
	v_lshl_add_u64 v[166:167], v[178:179], 0, v[150:151]
	s_waitcnt lgkmcnt(0)
	global_store_dwordx4 v[166:167], v[174:177], off nt
	s_waitcnt lgkmcnt(0)

; #define LAS __attribute__((address_space(3)))
; __device__ __forceinline__ unsigned cvt2bf(float lo, float hi) { const f32x2_t v = {lo, hi}; const bf16x2_t r = __builtin_convertvector(v, bf16x2_t); return __builtin_bit_cast(unsigned, r); }
; __device__ __forceinline__ void tr_load(const TrItem& t, f32x4 (&ra)[8], f32x4 (&rb)[8], int lane) {
;     const int q = lane >> 4, n4 = lane & 15;
;     const float* p = t.src + (size_t)(2 * q) * t.N + 4 * n4;
; #pragma unroll
;     for (int i = 0; i < 8; ++i) { ra[i] = __builtin_nontemporal_load((const f32x4*)(p + (size_t)(8 * i) * t.N)); rb[i] = __builtin_nontemporal_load((const f32x4*)(p + (size_t)(8 * i + 1) * t.N)); }
; }
; __device__ __forceinline__ void tr_store(const TrItem& t, const f32x4 (&ra)[8], const f32x4 (&rb)[8], LAS unsigned* scr, int lane) {
;     const int q = lane >> 4, n4 = lane & 15;
; #pragma unroll
;     for (int i = 0; i < 8; ++i)
; #pragma unroll
;         for (int j = 0; j < 4; ++j) scr[(4 * n4 + j) * 32 + ((i ^ (n4 & 7)) << 2) + q] = cvt2bf(ra[i][j], rb[i][j]);
; __device__ __forceinline__ void conv_items(const Args& a, LAS unsigned char* lds, int it0, int it1, int vcu, int G, int lane, int wave) {
;     ...
;         int nx = it + NGW; bool has = nx < it1;
;         TrItem nxt = tr_decode(a, has ? nx : it);
;         if (has) tr_load(nxt, na, nb_, lane);
;         tr_store(cur, ra, rb, scr, lane);
.LBB0_661:
	v_mul_u32_u24_e32 v66, s24, v135
	v_lshlrev_b32_e32 v130, 2, v66
	v_lshl_add_u64 v[66:67], s[22:23], 0, v[130:131]
	v_lshlrev_b32_e32 v130, 2, v132
	v_lshl_add_u64 v[66:67], v[66:67], 0, v[130:131]
	s_lshl_b64 s[8:9], s[24:25], 2
	v_lshl_add_u64 v[70:71], v[66:67], 0, s[8:9]
	s_mul_i32 s2, s24, 28
	global_load_dwordx4 v[66:69], v[66:67], off nt
	s_nop 0
	global_load_dwordx4 v[74:77], v[70:71], off nt
	v_lshl_add_u64 v[70:71], v[70:71], 0, s[2:3]
	v_lshl_add_u64 v[78:79], v[70:71], 0, s[8:9]
	global_load_dwordx4 v[70:73], v[70:71], off nt
	s_nop 0
	global_load_dwordx4 v[86:89], v[78:79], off nt
	v_lshl_add_u64 v[78:79], v[78:79], 0, s[2:3]
	v_lshl_add_u64 v[82:83], v[78:79], 0, s[8:9]
	global_load_dwordx4 v[78:81], v[78:79], off nt
	s_nop 0
	global_load_dwordx4 v[98:101], v[82:83], off nt
	v_lshl_add_u64 v[82:83], v[82:83], 0, s[2:3]
	v_lshl_add_u64 v[90:91], v[82:83], 0, s[8:9]
	v_lshl_add_u64 v[94:95], v[90:91], 0, s[2:3]
	global_load_dwordx4 v[82:85], v[82:83], off nt
	s_nop 0
	global_load_dwordx4 v[106:109], v[90:91], off nt
	s_nop 0
	global_load_dwordx4 v[90:93], v[94:95], off nt
	v_lshl_add_u64 v[94:95], v[94:95], 0, s[8:9]
	v_lshl_add_u64 v[102:103], v[94:95], 0, s[2:3]
	global_load_dwordx4 v[114:117], v[94:95], off nt
	s_nop 0
	global_load_dwordx4 v[94:97], v[102:103], off nt
	v_lshl_add_u64 v[102:103], v[102:103], 0, s[8:9]
	v_lshl_add_u64 v[110:111], v[102:103], 0, s[2:3]
	global_load_dwordx4 v[118:121], v[102:103], off nt
	s_nop 0
	global_load_dwordx4 v[102:105], v[110:111], off nt
	v_lshl_add_u64 v[110:111], v[110:111], 0, s[8:9]
	v_lshl_add_u64 v[126:127], v[110:111], 0, s[2:3]
	global_load_dwordx4 v[122:125], v[110:111], off nt
	s_nop 0
	global_load_dwordx4 v[110:113], v[126:127], off nt
	v_lshl_add_u64 v[126:127], v[126:127], 0, s[8:9]
	global_load_dwordx4 v[126:129], v[126:127], off nt
	s_waitcnt vmcnt(30)
	v_cvt_pk_bf16_f32 v130, v2, v6
	v_cvt_pk_bf16_f32 v166, v3, v7
	ds_write2_b32 v158, v130, v166 offset1:32
	v_cvt_pk_bf16_f32 v130, v4, v8
	v_cvt_pk_bf16_f32 v166, v5, v9
	ds_write2_b32 v158, v130, v166 offset0:64 offset1:96
	s_waitcnt vmcnt(28)
	v_cvt_pk_bf16_f32 v130, v10, v14
	v_cvt_pk_bf16_f32 v166, v11, v15
	ds_write2_b32 v159, v130, v166 offset1:32
	v_cvt_pk_bf16_f32 v130, v12, v16
	v_cvt_pk_bf16_f32 v166, v13, v17
	ds_write2_b32 v159, v130, v166 offset0:64 offset1:96
	s_waitcnt vmcnt(26)
	v_cvt_pk_bf16_f32 v130, v18, v22
	v_cvt_pk_bf16_f32 v166, v19, v23
	ds_write2_b32 v160, v130, v166 offset1:32
	v_cvt_pk_bf16_f32 v130, v20, v24
	v_cvt_pk_bf16_f32 v166, v21, v25
	ds_write2_b32 v160, v130, v166 offset0:64 offset1:96
	s_waitcnt vmcnt(24)
	v_cvt_pk_bf16_f32 v130, v26, v30
	v_cvt_pk_bf16_f32 v166, v27, v31
	ds_write2_b32 v161, v130, v166 offset1:32
	v_cvt_pk_bf16_f32 v130, v28, v32
	v_cvt_pk_bf16_f32 v166, v29, v33
	ds_write2_b32 v161, v130, v166 offset0:64 offset1:96
	s_waitcnt vmcnt(22)
	v_cvt_pk_bf16_f32 v130, v34, v38
	v_cvt_pk_bf16_f32 v166, v35, v39
	ds_write2_b32 v162, v130, v166 offset1:32
	v_cvt_pk_bf16_f32 v130, v36, v40
	v_cvt_pk_bf16_f32 v166, v37, v41
	ds_write2_b32 v162, v130, v166 offset0:64 offset1:96
	s_waitcnt vmcnt(20)
	v_cvt_pk_bf16_f32 v130, v42, v46
	v_cvt_pk_bf16_f32 v166, v43, v47
	ds_write2_b32 v163, v130, v166 offset1:32
	v_cvt_pk_bf16_f32 v130, v44, v48
	v_cvt_pk_bf16_f32 v166, v45, v49
	ds_write2_b32 v163, v130, v166 offset0:64 offset1:96
	s_waitcnt vmcnt(18)
	v_cvt_pk_bf16_f32 v130, v50, v54
	v_cvt_pk_bf16_f32 v166, v51, v55
	ds_write2_b32 v164, v130, v166 offset1:32
	v_cvt_pk_bf16_f32 v130, v52, v56
	v_cvt_pk_bf16_f32 v166, v53, v57
	ds_write2_b32 v164, v130, v166 offset0:64 offset1:96
	s_waitcnt vmcnt(16)
	v_cvt_pk_bf16_f32 v130, v58, v62
	v_cvt_pk_bf16_f32 v166, v59, v63
	ds_write2_b32 v165, v130, v166 offset1:32
	v_cvt_pk_bf16_f32 v130, v60, v64
	v_cvt_pk_bf16_f32 v166, v61, v65
	ds_write2_b32 v165, v130, v166 offset0:64 offset1:96
	s_branch .Lcvj_4

; #define LAS __attribute__((address_space(3)))
; #define LDS_WAIT() asm volatile("s_waitcnt lgkmcnt(0)" ::: "memory")
; __device__ __forceinline__ TrItem tr_decode(const Args& a, int it) {
;     ...
;     if (r < T_IN) { const int kb = r & 31, nb = r >> 5; t.N = INCOLS; t.src = a.in[I_WIN] + (size_t)(64 * kb) * INCOLS + 64 * nb; t.dst = (bf16*)(ws + WS_WIN) + (size_t)(64 * nb) * DM + 64 * kb; return t; } r -= T_IN;
;     if (r < T_OUT) { const int kb = r & 31, nb = r >> 5; t.N = DM; t.src = a.in[I_WOUT] + (size_t)(64 * kb) * DM + 64 * nb; t.dst = (bf16*)(ws + WS_WOUT) + (size_t)(64 * nb) * DM + 64 * kb; return t; } r -= T_OUT;
;     if (r < NEXP * T_GU1) { const int e = r / T_GU1, q = r % T_GU1, kb = q & 31, nb = q >> 5, n0 = 64 * nb;
;         const int drow0 = n0 < 2048 ? (n0 >> 7) * 256 + (n0 & 127) : ((n0 - 2048) >> 7) * 256 + 128 + ((n0 - 2048) & 127);
;         t.N = 4096; t.src = a.in[I_WGU] + (size_t)e * DM * 4096 + (size_t)(64 * kb) * 4096 + n0; t.dst = (bf16*)(ws + WS_WGU) + (size_t)e * 4096 * DM + (size_t)drow0 * DM + 64 * kb; return t; } r -= NEXP * T_GU1;
;     { const int e = r / T_DN1, q = r % T_DN1, kb = q & 31, nb = q >> 5;
;         t.N = DM; t.src = a.in[I_WDN] + (size_t)e * DM * DM + (size_t)(64 * kb) * DM + 64 * nb; t.dst = (bf16*)(ws + WS_WDN) + (size_t)e * DM * DM + (size_t)(64 * nb) * DM + 64 * kb; return t; }
; __device__ __forceinline__ void tr_store(const TrItem& t, const f32x4 (&ra)[8], const f32x4 (&rb)[8], LAS unsigned* scr, int lane) {
;     ...
;     const int nr = lane >> 3, ch = lane & 7;
; #pragma unroll
;     for (int i = 0; i < 8; ++i) { const int n = nr + 8 * i; const v4u v = *(const LAS v4u*)(scr + n * 32 + ((ch ^ ((n >> 2) & 7)) << 2));
;         __builtin_nontemporal_store(v, (v4u*)(t.dst + (size_t)n * DM + 8 * ch)); }
;     LDS_WAIT(); asm volatile("" ::: "memory");
.Lcvj_4:
	s_waitcnt lgkmcnt(0)
	ds_read_b128 v[166:169], v1
	ds_read_b128 v[170:173], v133
	v_lshlrev_b32_e32 v130, 1, v134
	v_lshl_add_u64 v[178:179], s[10:11], 0, v[130:131]
	v_lshl_add_u64 v[174:175], v[178:179], 0, v[136:137]
	s_waitcnt lgkmcnt(1)
	global_store_dwordx4 v[174:175], v[166:169], off nt
	ds_read_b128 v[166:169], v152
	v_lshl_add_u64 v[174:175], v[178:179], 0, v[138:139]
	s_waitcnt lgkmcnt(1)
	global_store_dwordx4 v[174:175], v[170:173], off nt
	ds_read_b128 v[170:173], v153
	v_lshl_add_u64 v[174:175], v[178:179], 0, v[140:141]
	s_waitcnt lgkmcnt(1)
	global_store_dwordx4 v[174:175], v[166:169], off nt
	ds_read_b128 v[166:169], v154
	v_lshl_add_u64 v[174:175], v[178:179], 0, v[142:143]
	s_waitcnt lgkmcnt(1)
	global_store_dwordx4 v[174:175], v[170:173], off nt
	v_lshl_add_u64 v[174:175], v[178:179], 0, v[144:145]
	ds_read_b128 v[170:173], v155
	s_waitcnt lgkmcnt(1)
	global_store_dwordx4 v[174:175], v[166:169], off nt
	ds_read_b128 v[166:169], v156
	ds_read_b128 v[174:177], v157
	v_lshl_add_u64 v[180:181], v[178:179], 0, v[146:147]
	s_waitcnt lgkmcnt(2)
	global_store_dwordx4 v[180:181], v[170:173], off nt
	s_and_b64 vcc, exec, s[0:1]
	s_mov_b64 s[0:1], -1
	v_lshl_add_u64 v[170:171], v[178:179], 0, v[148:149]
	s_waitcnt lgkmcnt(1)
	global_store_dwordx4 v[170:171], v[166:169], off nt
	s_nop 1
	v_lshl_add_u64 v[166:167], v[178:179], 0, v[150:151]
	s_waitcnt lgkmcnt(0)
	global_store_dwordx4 v[166:167], v[174:177], off nt
	s_waitcnt lgkmcnt(0)
	s_cbranch_vccnz .LBB0_645
	s_add_i32 s2, s36, s26
	s_cmp_lt_i32 s2, 0xe999
	s_cselect_b64 s[22:23], -1, 0
	s_and_b64 s[0:1], s[22:23], exec
	s_cselect_b32 s38, s2, s37
	s_cmpk_gt_i32 s38, 0xbff
	s_mov_b64 s[28:29], -1
	s_cbranch_scc0 .LBB0_680
	s_cmpk_gt_u32 s38, 0xfff
	s_cbranch_scc0 .LBB0_674
	s_cmp_gt_u32 s38, 0x10fff
	s_mov_b64 s[26:27], -1
	s_cbranch_scc0 .LBB0_667
	s_add_i32 s0, s38, 0xfffef000
	s_lshr_b32 s2, s0, 10
	s_lshl_b64 s[0:1], s[2:3], 24
	v_readlane_b32 s52, v246, 0
	v_readlane_b32 s53, v246, 1
	s_add_u32 s0, s52, s0
	s_addc_u32 s1, s53, s1
	s_lshl_b32 s8, s38, 6
	s_and_b32 s10, s8, 0x7c0
	s_lshl_b32 s8, s10, 13
	s_add_u32 s8, s0, s8
	s_addc_u32 s9, s1, 0
	s_lshl_b32 s0, s38, 1
	s_and_b32 s0, s0, 0x7c0
	s_lshl_b32 s14, s0, 2
	s_add_u32 s24, s8, s14
	s_addc_u32 s25, s9, 0
	s_lshl_b64 s[8:9], s[2:3], 23
	s_add_u32 s20, s31, s8
	v_readlane_b32 s54, v246, 2
	v_readlane_b32 s55, v246, 3
	v_readlane_b32 s56, v246, 4
	v_readlane_b32 s57, v246, 5
	v_readlane_b32 s58, v246, 6
	v_readlane_b32 s59, v246, 7
	s_mov_b32 s11, s3
	s_mov_b32 s1, s3
	s_addc_u32 s21, s33, s9
	s_mov_b64 s[26:27], 0

; __device__ __forceinline__ void tr_load(const TrItem& t, f32x4 (&ra)[8], f32x4 (&rb)[8], int lane) {
;     const int q = lane >> 4, n4 = lane & 15;
;     const float* p = t.src + (size_t)(2 * q) * t.N + 4 * n4;
; #pragma unroll
;     for (int i = 0; i < 8; ++i) { ra[i] = __builtin_nontemporal_load((const f32x4*)(p + (size_t)(8 * i) * t.N)); rb[i] = __builtin_nontemporal_load((const f32x4*)(p + (size_t)(8 * i + 1) * t.N)); }
; }
; __device__ __forceinline__ void conv_items(const Args& a, LAS unsigned char* lds, int it0, int it1, int vcu, int G, int lane, int wave) {
;     ...
;         it = nx; nx = it + NGW; has = nx < it1;
;         cur = tr_decode(a, has ? nx : it);
;         if (has) tr_load(cur, ra, rb, lane);
;         tr_store(nxt, na, nb_, scr, lane);
.LBB0_682:
	v_mul_u32_u24_e32 v2, s26, v135
	v_lshlrev_b32_e32 v2, 2, v2
	v_mov_b32_e32 v3, v131
	v_lshl_add_u64 v[2:3], s[24:25], 0, v[2:3]
	v_lshlrev_b32_e32 v4, 2, v132
	v_mov_b32_e32 v5, v131
	v_lshl_add_u64 v[2:3], v[2:3], 0, v[4:5]
	s_lshl_b64 s[8:9], s[26:27], 2
	v_lshl_add_u64 v[10:11], v[2:3], 0, s[8:9]
	s_mul_i32 s2, s26, 28
	global_load_dwordx4 v[2:5], v[2:3], off nt
	s_nop 0
	global_load_dwordx4 v[6:9], v[10:11], off nt
	v_lshl_add_u64 v[10:11], v[10:11], 0, s[2:3]
	v_lshl_add_u64 v[18:19], v[10:11], 0, s[8:9]
	global_load_dwordx4 v[10:13], v[10:11], off nt
	s_nop 0
	global_load_dwordx4 v[14:17], v[18:19], off nt
	v_lshl_add_u64 v[18:19], v[18:19], 0, s[2:3]
	v_lshl_add_u64 v[26:27], v[18:19], 0, s[8:9]
	global_load_dwordx4 v[18:21], v[18:19], off nt
	s_nop 0
	global_load_dwordx4 v[22:25], v[26:27], off nt
	v_lshl_add_u64 v[26:27], v[26:27], 0, s[2:3]
	v_lshl_add_u64 v[34:35], v[26:27], 0, s[8:9]
	v_lshl_add_u64 v[38:39], v[34:35], 0, s[2:3]
	v_lshl_add_u64 v[42:43], v[38:39], 0, s[8:9]
	v_lshl_add_u64 v[46:47], v[42:43], 0, s[2:3]
	v_lshl_add_u64 v[50:51], v[46:47], 0, s[8:9]
	v_lshl_add_u64 v[54:55], v[50:51], 0, s[2:3]
	v_lshl_add_u64 v[58:59], v[54:55], 0, s[8:9]
	v_lshl_add_u64 v[62:63], v[58:59], 0, s[2:3]
	global_load_dwordx4 v[26:29], v[26:27], off nt
	s_nop 0
	global_load_dwordx4 v[30:33], v[34:35], off nt
	s_nop 0
	global_load_dwordx4 v[34:37], v[38:39], off nt
	s_nop 0
	global_load_dwordx4 v[38:41], v[42:43], off nt
	s_nop 0
	global_load_dwordx4 v[42:45], v[46:47], off nt
	s_nop 0
	global_load_dwordx4 v[46:49], v[50:51], off nt
	s_nop 0
	global_load_dwordx4 v[50:53], v[54:55], off nt
	s_nop 0
	global_load_dwordx4 v[54:57], v[58:59], off nt
	s_nop 0
	global_load_dwordx4 v[58:61], v[62:63], off nt
	v_lshl_add_u64 v[62:63], v[62:63], 0, s[8:9]
	global_load_dwordx4 v[62:65], v[62:63], off nt
	s_waitcnt vmcnt(24)
	s_branch .LBB0_644

; #define LAS __attribute__((address_space(3)))
; #define LDS_WAIT() asm volatile("s_waitcnt lgkmcnt(0)" ::: "memory")
; __device__ __forceinline__ unsigned cvt2bf(float lo, float hi) { const f32x2_t v = {lo, hi}; const bf16x2_t r = __builtin_convertvector(v, bf16x2_t); return __builtin_bit_cast(unsigned, r); }
; __device__ __forceinline__ void tr_load(const TrItem& t, f32x4 (&ra)[8], f32x4 (&rb)[8], int lane) {
;     const int q = lane >> 4, n4 = lane & 15;
;     const float* p = t.src + (size_t)(2 * q) * t.N + 4 * n4;
; #pragma unroll
;     for (int i = 0; i < 8; ++i) { ra[i] = __builtin_nontemporal_load((const f32x4*)(p + (size_t)(8 * i) * t.N)); rb[i] = __builtin_nontemporal_load((const f32x4*)(p + (size_t)(8 * i + 1) * t.N)); }
; }
; __device__ __forceinline__ void tr_store(const TrItem& t, const f32x4 (&ra)[8], const f32x4 (&rb)[8], LAS unsigned* scr, int lane) {
;     const int q = lane >> 4, n4 = lane & 15;
; #pragma unroll
;     for (int i = 0; i < 8; ++i)
; #pragma unroll
;         for (int j = 0; j < 4; ++j) scr[(4 * n4 + j) * 32 + ((i ^ (n4 & 7)) << 2) + q] = cvt2bf(ra[i][j], rb[i][j]);
;     LDS_WAIT(); asm volatile("" ::: "memory");
;     const int nr = lane >> 3, ch = lane & 7;
; #pragma unroll
;     for (int i = 0; i < 8; ++i) { const int n = nr + 8 * i; const v4u v = *(const LAS v4u*)(scr + n * 32 + ((ch ^ ((n >> 2) & 7)) << 2));
;         __builtin_nontemporal_store(v, (v4u*)(t.dst + (size_t)n * DM + 8 * ch)); }
;     LDS_WAIT(); asm volatile("" ::: "memory");
; }
; __device__ __forceinline__ void conv_items(const Args& a, LAS unsigned char* lds, int it0, int it1, int vcu, int G, int lane, int wave) {
;     LAS unsigned* scr = (LAS unsigned*)(lds + wave * 16384);
;     const int gw = vcu * NWAVES + wave, NGW = G * NWAVES;
;     f32x4 ra[8], rb[8], na[8], nb_[8];
;     int it = it0 + gw;
;     if (it >= it1) return;
;     TrItem cur = tr_decode(a, it);
;     tr_load(cur, ra, rb, lane);
.LBB0_751:
	v_readlane_b32 s5, v246, 33
	s_lshl_b32 s5, s5, 14
	v_readlane_b32 s15, v246, 11
	s_waitcnt vmcnt(11)
	v_lshrrev_b32_e32 v66, 3, v194
	s_add_i32 s14, s5, 0
	s_lshl_b32 s5, s15, 3
	s_lshl_b64 s[8:9], s[12:13], 12
	v_and_b32_e32 v1, 6, v66
	s_add_u32 s6, s16, s8
	s_waitcnt lgkmcnt(0)
	v_mul_u32_u24_e32 v2, s20, v1
	v_lshlrev_b32_e32 v67, 2, v194
	s_addc_u32 s8, s17, s9
	s_lshl_b64 s[0:1], s[0:1], 1
	v_lshlrev_b32_e32 v130, 2, v2
	v_mov_b32_e32 v131, 0
	v_and_b32_e32 v132, 60, v67
	s_add_u32 s16, s6, s0
	v_lshl_add_u64 v[2:3], s[18:19], 0, v[130:131]
	v_lshlrev_b32_e32 v130, 2, v132
	s_addc_u32 s17, s8, s1
	v_lshl_add_u64 v[2:3], v[2:3], 0, v[130:131]
	s_lshl_b64 s[0:1], s[20:21], 2
	s_mov_b32 s7, 0
	v_lshl_add_u64 v[10:11], v[2:3], 0, s[0:1]
	s_mul_i32 s6, s20, 28
	global_load_dwordx4 v[2:5], v[2:3], off nt
	s_nop 0
	global_load_dwordx4 v[6:9], v[10:11], off nt
	v_lshl_add_u64 v[10:11], v[10:11], 0, s[6:7]
	v_lshl_add_u64 v[18:19], v[10:11], 0, s[0:1]
	global_load_dwordx4 v[10:13], v[10:11], off nt
	s_nop 0
	global_load_dwordx4 v[14:17], v[18:19], off nt
	v_lshl_add_u64 v[18:19], v[18:19], 0, s[6:7]
	v_lshl_add_u64 v[26:27], v[18:19], 0, s[0:1]
	global_load_dwordx4 v[18:21], v[18:19], off nt
	s_nop 0
	global_load_dwordx4 v[22:25], v[26:27], off nt
	v_lshl_add_u64 v[26:27], v[26:27], 0, s[6:7]
	v_lshl_add_u64 v[34:35], v[26:27], 0, s[0:1]
	v_lshl_add_u64 v[38:39], v[34:35], 0, s[6:7]
	v_lshl_add_u64 v[42:43], v[38:39], 0, s[0:1]
	v_lshl_add_u64 v[46:47], v[42:43], 0, s[6:7]
	s_waitcnt vmcnt(14)
	v_lshl_add_u64 v[50:51], v[46:47], 0, s[0:1]
	s_waitcnt vmcnt(12)
	v_lshl_add_u64 v[54:55], v[50:51], 0, s[6:7]
	v_lshl_add_u64 v[58:59], v[54:55], 0, s[0:1]
	v_lshl_add_u64 v[62:63], v[58:59], 0, s[6:7]
	global_load_dwordx4 v[26:29], v[26:27], off nt
	s_nop 0
	global_load_dwordx4 v[30:33], v[34:35], off nt
	v_lshlrev_b32_e32 v77, 3, v0
	global_load_dwordx4 v[34:37], v[38:39], off nt
	v_bitop3_b32 v78, v66, 28, v67 bitop3:0x48
	global_load_dwordx4 v[38:41], v[42:43], off nt
	v_and_b32_e32 v134, 56, v77
	global_load_dwordx4 v[42:45], v[46:47], off nt
	v_lshlrev_b32_e32 v77, 7, v66
	global_load_dwordx4 v[46:49], v[50:51], off nt
	v_lshlrev_b32_e32 v78, 2, v78
	global_load_dwordx4 v[50:53], v[54:55], off nt
	v_add3_u32 v133, s14, v77, v78
	global_load_dwordx4 v[54:57], v[58:59], off nt
	v_or_b32_e32 v77, 8, v66
	global_load_dwordx4 v[58:61], v[62:63], off nt
	v_lshl_add_u64 v[62:63], v[62:63], 0, s[0:1]
	global_load_dwordx4 v[62:65], v[62:63], off nt
	v_bitop3_b32 v80, v77, 28, v67 bitop3:0x48
	v_lshlrev_b32_e32 v79, 7, v77
	v_lshlrev_b32_e32 v80, 2, v80
	v_lshlrev_b32_e32 v138, 12, v77
	v_or_b32_e32 v77, 16, v66
	v_add3_u32 v135, s14, v79, v80
	v_bitop3_b32 v80, v77, 28, v67 bitop3:0x48
	v_lshlrev_b32_e32 v79, 7, v77
	v_lshlrev_b32_e32 v80, 2, v80
	v_lshlrev_b32_e32 v140, 12, v77
	v_or_b32_e32 v77, 24, v66
	v_add3_u32 v152, s14, v79, v80
	v_bitop3_b32 v80, v77, 28, v67 bitop3:0x48
	v_lshlrev_b32_e32 v79, 7, v77
	v_lshlrev_b32_e32 v80, 2, v80
	v_lshlrev_b32_e32 v142, 12, v77
	v_or_b32_e32 v77, 32, v66
	v_lshlrev_b32_e32 v68, 9, v0
	v_lshrrev_b32_e32 v69, 2, v194
	v_add3_u32 v153, s14, v79, v80
	v_lshlrev_b32_e32 v79, 7, v77
	v_lshlrev_b32_e32 v144, 12, v77
	v_or_b32_e32 v77, 40, v66
	s_add_u32 s33, s92, 0x70800000
	v_and_b32_e32 v68, 0x1e00, v68
	v_and_b32_e32 v69, 12, v69
	v_add3_u32 v154, s14, v79, v78
	v_bitop3_b32 v79, v77, 28, v67 bitop3:0x48
	s_addc_u32 s36, s93, 0
	v_add3_u32 v68, s14, v68, v69
	v_lshlrev_b32_e32 v69, 4, v0
	v_mov_b32_e32 v71, 0x70
	s_movk_i32 s1, 0x50
	v_lshlrev_b32_e32 v136, 12, v66
	v_lshlrev_b32_e32 v78, 7, v77
	v_lshlrev_b32_e32 v79, 2, v79
	v_lshlrev_b32_e32 v146, 12, v77
	v_or_b32_e32 v77, 48, v66
	v_or_b32_e32 v66, 56, v66
	s_add_u32 s37, s92, 0x50800000
	s_movk_i32 s0, 0x70
	v_bitop3_b32 v76, v69, s1, v71 bitop3:0x6c
	s_movk_i32 s1, 0x60
	v_add3_u32 v155, s14, v78, v79
	v_bitop3_b32 v79, v77, 28, v67 bitop3:0x48
	v_bitop3_b32 v67, v66, 28, v67 bitop3:0x48
	s_addc_u32 s38, s93, 0
	v_and_b32_e32 v70, 0x70, v69
	v_bitop3_b32 v72, v69, 16, v71 bitop3:0x6c
	v_bitop3_b32 v73, v69, 32, v71 bitop3:0x6c
	v_bitop3_b32 v74, v69, 48, v71 bitop3:0x6c
	v_bitop3_b32 v75, v69, 64, v71 bitop3:0x6c
	v_bitop3_b32 v71, v69, s1, v71 bitop3:0x6c
	v_bitop3_b32 v69, v69, s0, v69 bitop3:0xc
	v_lshlrev_b32_e32 v78, 7, v77
	v_lshlrev_b32_e32 v79, 2, v79
	v_lshlrev_b32_e32 v148, 12, v77
	v_lshlrev_b32_e32 v77, 7, v66
	v_lshlrev_b32_e32 v67, 2, v67
	s_add_u32 s12, s92, 0x200000
	v_mov_b32_e32 v137, v131
	v_mov_b32_e32 v139, v131
	v_mov_b32_e32 v141, v131
	v_mov_b32_e32 v143, v131
	v_mov_b32_e32 v145, v131
	v_mov_b32_e32 v147, v131
	v_add3_u32 v156, s14, v78, v79
	v_mov_b32_e32 v149, v131
	v_add3_u32 v157, s14, v77, v67
	v_lshlrev_b32_e32 v150, 12, v66
	v_mov_b32_e32 v151, v131
	s_addc_u32 s13, s93, 0
	s_lshl_b32 s39, s15, 4
	v_add_u32_e32 v158, v68, v70
	v_add_u32_e32 v159, v68, v72
	v_add_u32_e32 v160, v68, v73
	v_add_u32_e32 v161, v68, v74
	v_add_u32_e32 v162, v68, v75
	v_add_u32_e32 v163, v68, v76
	v_add_u32_e32 v164, v68, v71
	v_add_u32_e32 v165, v68, v69
	s_branch .LBB0_754
; #define LAS __attribute__((address_space(3)))
; #define LDS_WAIT() asm volatile("s_waitcnt lgkmcnt(0)" ::: "memory")
; __device__ __forceinline__ unsigned cvt2bf(float lo, float hi) { const f32x2_t v = {lo, hi}; const bf16x2_t r = __builtin_convertvector(v, bf16x2_t); return __builtin_bit_cast(unsigned, r); }
; __device__ __forceinline__ void tr_store(const TrItem& t, const f32x4 (&ra)[8], const f32x4 (&rb)[8], LAS unsigned* scr, int lane) {
;     const int q = lane >> 4, n4 = lane & 15;
; #pragma unroll
;     for (int i = 0; i < 8; ++i)
; #pragma unroll
;         for (int j = 0; j < 4; ++j) scr[(4 * n4 + j) * 32 + ((i ^ (n4 & 7)) << 2) + q] = cvt2bf(ra[i][j], rb[i][j]);
;     LDS_WAIT(); asm volatile("" ::: "memory");
;     const int nr = lane >> 3, ch = lane & 7;
; #pragma unroll
;     for (int i = 0; i < 8; ++i) { const int n = nr + 8 * i; const v4u v = *(const LAS v4u*)(scr + n * 32 + ((ch ^ ((n >> 2) & 7)) << 2));
;         __builtin_nontemporal_store(v, (v4u*)(t.dst + (size_t)n * DM + 8 * ch)); }
;     LDS_WAIT(); asm volatile("" ::: "memory");
; }
; __device__ __forceinline__ void conv_items(const Args& a, LAS unsigned char* lds, int it0, int it1, int vcu, int G, int lane, int wave) {
;     ...
;         tr_store(nxt, na, nb_, scr, lane);
;         if (!has) break;
;         it = nx;
.Lcvw_5:
	s_waitcnt vmcnt(8)
.LBB0_752:
	v_cvt_pk_bf16_f32 v166, v66, v74
	v_cvt_pk_bf16_f32 v167, v67, v75
	ds_write2_b32 v158, v166, v167 offset1:32
	v_cvt_pk_bf16_f32 v166, v68, v76
	v_cvt_pk_bf16_f32 v167, v69, v77
	ds_write2_b32 v158, v166, v167 offset0:64 offset1:96
	v_cvt_pk_bf16_f32 v166, v70, v86
	v_cvt_pk_bf16_f32 v167, v71, v87
	ds_write2_b32 v159, v166, v167 offset1:32
	v_cvt_pk_bf16_f32 v166, v72, v88
	v_cvt_pk_bf16_f32 v167, v73, v89
	ds_write2_b32 v159, v166, v167 offset0:64 offset1:96
	v_cvt_pk_bf16_f32 v166, v78, v98
	v_cvt_pk_bf16_f32 v167, v79, v99
	ds_write2_b32 v160, v166, v167 offset1:32
	v_cvt_pk_bf16_f32 v166, v80, v100
	v_cvt_pk_bf16_f32 v167, v81, v101
	ds_write2_b32 v160, v166, v167 offset0:64 offset1:96
	v_cvt_pk_bf16_f32 v166, v82, v106
	v_cvt_pk_bf16_f32 v167, v83, v107
	ds_write2_b32 v161, v166, v167 offset1:32
	v_cvt_pk_bf16_f32 v166, v84, v108
	v_cvt_pk_bf16_f32 v167, v85, v109
	ds_write2_b32 v161, v166, v167 offset0:64 offset1:96
	v_cvt_pk_bf16_f32 v166, v90, v114
	v_cvt_pk_bf16_f32 v167, v91, v115
	ds_write2_b32 v162, v166, v167 offset1:32
	v_cvt_pk_bf16_f32 v166, v92, v116
	v_cvt_pk_bf16_f32 v167, v93, v117
	ds_write2_b32 v162, v166, v167 offset0:64 offset1:96
	v_cvt_pk_bf16_f32 v166, v94, v118
	v_cvt_pk_bf16_f32 v167, v95, v119
	ds_write2_b32 v163, v166, v167 offset1:32
	v_cvt_pk_bf16_f32 v166, v96, v120
	v_cvt_pk_bf16_f32 v167, v97, v121
	ds_write2_b32 v163, v166, v167 offset0:64 offset1:96
	v_cvt_pk_bf16_f32 v166, v102, v122
	v_cvt_pk_bf16_f32 v167, v103, v123
	s_lshl_b64 s[0:1], s[0:1], 12
	ds_write2_b32 v164, v166, v167 offset1:32
	v_cvt_pk_bf16_f32 v166, v104, v124
	v_cvt_pk_bf16_f32 v167, v105, v125
	s_add_u32 s6, s24, s0
	ds_write2_b32 v164, v166, v167 offset0:64 offset1:96
	v_cvt_pk_bf16_f32 v166, v110, v126
	v_cvt_pk_bf16_f32 v167, v111, v127
	s_addc_u32 s8, s25, s1
	s_lshl_b64 s[0:1], s[16:17], 1
	ds_write2_b32 v165, v166, v167 offset1:32
	v_cvt_pk_bf16_f32 v166, v112, v128
	v_cvt_pk_bf16_f32 v167, v113, v129
	s_add_u32 s16, s6, s0
	ds_write2_b32 v165, v166, v167 offset0:64 offset1:96
	s_addc_u32 s17, s8, s1
	s_add_i32 s30, s44, s5
	s_lshl_b64 s[0:1], s[18:19], 12
	s_waitcnt lgkmcnt(0)
	s_add_u32 s6, s22, s0
	s_addc_u32 s8, s23, s1
	s_lshl_b64 s[0:1], s[20:21], 1
	ds_read_b128 v[166:169], v133
	ds_read_b128 v[170:173], v135
	s_add_u32 s0, s6, s0
	s_addc_u32 s1, s8, s1
	v_lshl_add_u64 v[178:179], s[0:1], 0, v[130:131]
	v_lshl_add_u64 v[174:175], v[178:179], 0, v[136:137]
	s_waitcnt lgkmcnt(1)
	global_store_dwordx4 v[174:175], v[166:169], off nt
	ds_read_b128 v[166:169], v152
	v_lshl_add_u64 v[174:175], v[178:179], 0, v[138:139]
	s_waitcnt lgkmcnt(1)
	global_store_dwordx4 v[174:175], v[170:173], off nt
	ds_read_b128 v[170:173], v153
	v_lshl_add_u64 v[174:175], v[178:179], 0, v[140:141]
	s_waitcnt lgkmcnt(1)
	global_store_dwordx4 v[174:175], v[166:169], off nt
	ds_read_b128 v[166:169], v154
	v_lshl_add_u64 v[174:175], v[178:179], 0, v[142:143]
	s_waitcnt lgkmcnt(1)
	global_store_dwordx4 v[174:175], v[170:173], off nt
	v_lshl_add_u64 v[174:175], v[178:179], 0, v[144:145]
	ds_read_b128 v[170:173], v155
	s_waitcnt lgkmcnt(1)
	global_store_dwordx4 v[174:175], v[166:169], off nt
	ds_read_b128 v[166:169], v156
	ds_read_b128 v[174:177], v157
	v_lshl_add_u64 v[180:181], v[178:179], 0, v[146:147]
	s_waitcnt lgkmcnt(2)
	global_store_dwordx4 v[180:181], v[170:173], off nt
	s_cmp_gt_i32 s30, 0x10fff
	s_cselect_b64 s[0:1], -1, 0
	v_lshl_add_u64 v[170:171], v[178:179], 0, v[148:149]
	s_waitcnt lgkmcnt(1)
	global_store_dwordx4 v[170:171], v[166:169], off nt
	s_nop 1
	v_lshl_add_u64 v[166:167], v[178:179], 0, v[150:151]
	s_waitcnt lgkmcnt(0)
	global_store_dwordx4 v[166:167], v[174:177], off nt
	s_waitcnt lgkmcnt(0)

; #define LAS __attribute__((address_space(3)))
; __device__ __forceinline__ unsigned cvt2bf(float lo, float hi) { const f32x2_t v = {lo, hi}; const bf16x2_t r = __builtin_convertvector(v, bf16x2_t); return __builtin_bit_cast(unsigned, r); }
; __device__ __forceinline__ void tr_load(const TrItem& t, f32x4 (&ra)[8], f32x4 (&rb)[8], int lane) {
;     const int q = lane >> 4, n4 = lane & 15;
;     const float* p = t.src + (size_t)(2 * q) * t.N + 4 * n4;
; #pragma unroll
;     for (int i = 0; i < 8; ++i) { ra[i] = __builtin_nontemporal_load((const f32x4*)(p + (size_t)(8 * i) * t.N)); rb[i] = __builtin_nontemporal_load((const f32x4*)(p + (size_t)(8 * i + 1) * t.N)); }
; }
; __device__ __forceinline__ void tr_store(const TrItem& t, const f32x4 (&ra)[8], const f32x4 (&rb)[8], LAS unsigned* scr, int lane) {
;     const int q = lane >> 4, n4 = lane & 15;
; #pragma unroll
;     for (int i = 0; i < 8; ++i)
; #pragma unroll
;         for (int j = 0; j < 4; ++j) scr[(4 * n4 + j) * 32 + ((i ^ (n4 & 7)) << 2) + q] = cvt2bf(ra[i][j], rb[i][j]);
; __device__ __forceinline__ void conv_items(const Args& a, LAS unsigned char* lds, int it0, int it1, int vcu, int G, int lane, int wave) {
;     ...
;         TrItem nxt = tr_decode(a, has ? nx : it);
;         if (has) tr_load(nxt, na, nb_, lane);
;         tr_store(cur, ra, rb, scr, lane);
.LBB0_769:
	v_mul_u32_u24_e32 v66, s28, v1
	v_lshlrev_b32_e32 v130, 2, v66
	v_lshl_add_u64 v[66:67], s[26:27], 0, v[130:131]
	v_lshlrev_b32_e32 v130, 2, v132
	v_lshl_add_u64 v[66:67], v[66:67], 0, v[130:131]
	s_lshl_b64 s[8:9], s[28:29], 2
	v_lshl_add_u64 v[70:71], v[66:67], 0, s[8:9]
	s_mul_i32 s6, s28, 28
	global_load_dwordx4 v[66:69], v[66:67], off nt
	s_nop 0
	global_load_dwordx4 v[74:77], v[70:71], off nt
	v_lshl_add_u64 v[70:71], v[70:71], 0, s[6:7]
	v_lshl_add_u64 v[78:79], v[70:71], 0, s[8:9]
	global_load_dwordx4 v[70:73], v[70:71], off nt
	s_nop 0
	global_load_dwordx4 v[86:89], v[78:79], off nt
	v_lshl_add_u64 v[78:79], v[78:79], 0, s[6:7]
	v_lshl_add_u64 v[82:83], v[78:79], 0, s[8:9]
	global_load_dwordx4 v[78:81], v[78:79], off nt
	s_nop 0
	global_load_dwordx4 v[98:101], v[82:83], off nt
	v_lshl_add_u64 v[82:83], v[82:83], 0, s[6:7]
	v_lshl_add_u64 v[90:91], v[82:83], 0, s[8:9]
	v_lshl_add_u64 v[94:95], v[90:91], 0, s[6:7]
	global_load_dwordx4 v[82:85], v[82:83], off nt
	s_nop 0
	global_load_dwordx4 v[106:109], v[90:91], off nt
	s_nop 0
	global_load_dwordx4 v[90:93], v[94:95], off nt
	v_lshl_add_u64 v[94:95], v[94:95], 0, s[8:9]
	v_lshl_add_u64 v[102:103], v[94:95], 0, s[6:7]
	global_load_dwordx4 v[114:117], v[94:95], off nt
	s_nop 0
	global_load_dwordx4 v[94:97], v[102:103], off nt
	v_lshl_add_u64 v[102:103], v[102:103], 0, s[8:9]
	v_lshl_add_u64 v[110:111], v[102:103], 0, s[6:7]
	global_load_dwordx4 v[118:121], v[102:103], off nt
	s_nop 0
	global_load_dwordx4 v[102:105], v[110:111], off nt
	v_lshl_add_u64 v[110:111], v[110:111], 0, s[8:9]
	v_lshl_add_u64 v[126:127], v[110:111], 0, s[6:7]
	global_load_dwordx4 v[122:125], v[110:111], off nt
	s_nop 0
	global_load_dwordx4 v[110:113], v[126:127], off nt
	v_lshl_add_u64 v[126:127], v[126:127], 0, s[8:9]
	global_load_dwordx4 v[126:129], v[126:127], off nt
	s_waitcnt vmcnt(30)
	v_cvt_pk_bf16_f32 v130, v2, v6
	v_cvt_pk_bf16_f32 v166, v3, v7
	ds_write2_b32 v158, v130, v166 offset1:32
	v_cvt_pk_bf16_f32 v130, v4, v8
	v_cvt_pk_bf16_f32 v166, v5, v9
	ds_write2_b32 v158, v130, v166 offset0:64 offset1:96
	s_waitcnt vmcnt(28)
	v_cvt_pk_bf16_f32 v130, v10, v14
	v_cvt_pk_bf16_f32 v166, v11, v15
	ds_write2_b32 v159, v130, v166 offset1:32
	v_cvt_pk_bf16_f32 v130, v12, v16
	v_cvt_pk_bf16_f32 v166, v13, v17
	ds_write2_b32 v159, v130, v166 offset0:64 offset1:96
	s_waitcnt vmcnt(26)
	v_cvt_pk_bf16_f32 v130, v18, v22
	v_cvt_pk_bf16_f32 v166, v19, v23
	ds_write2_b32 v160, v130, v166 offset1:32
	v_cvt_pk_bf16_f32 v130, v20, v24
	v_cvt_pk_bf16_f32 v166, v21, v25
	ds_write2_b32 v160, v130, v166 offset0:64 offset1:96
	s_waitcnt vmcnt(24)
	v_cvt_pk_bf16_f32 v130, v26, v30
	v_cvt_pk_bf16_f32 v166, v27, v31
	ds_write2_b32 v161, v130, v166 offset1:32
	v_cvt_pk_bf16_f32 v130, v28, v32
	v_cvt_pk_bf16_f32 v166, v29, v33
	ds_write2_b32 v161, v130, v166 offset0:64 offset1:96
	s_waitcnt vmcnt(22)
	v_cvt_pk_bf16_f32 v130, v34, v38
	v_cvt_pk_bf16_f32 v166, v35, v39
	ds_write2_b32 v162, v130, v166 offset1:32
	v_cvt_pk_bf16_f32 v130, v36, v40
	v_cvt_pk_bf16_f32 v166, v37, v41
	ds_write2_b32 v162, v130, v166 offset0:64 offset1:96
	s_waitcnt vmcnt(20)
	v_cvt_pk_bf16_f32 v130, v42, v46
	v_cvt_pk_bf16_f32 v166, v43, v47
	ds_write2_b32 v163, v130, v166 offset1:32
	v_cvt_pk_bf16_f32 v130, v44, v48
	v_cvt_pk_bf16_f32 v166, v45, v49
	ds_write2_b32 v163, v130, v166 offset0:64 offset1:96
	s_waitcnt vmcnt(18)
	v_cvt_pk_bf16_f32 v130, v50, v54
	v_cvt_pk_bf16_f32 v166, v51, v55
	ds_write2_b32 v164, v130, v166 offset1:32
	v_cvt_pk_bf16_f32 v130, v52, v56
	v_cvt_pk_bf16_f32 v166, v53, v57
	ds_write2_b32 v164, v130, v166 offset0:64 offset1:96
	s_waitcnt vmcnt(16)
	v_cvt_pk_bf16_f32 v130, v58, v62
	v_cvt_pk_bf16_f32 v166, v59, v63
	ds_write2_b32 v165, v130, v166 offset1:32
	v_cvt_pk_bf16_f32 v130, v60, v64
	v_cvt_pk_bf16_f32 v166, v61, v65
	ds_write2_b32 v165, v130, v166 offset0:64 offset1:96
	s_branch .Lcvj_5

; #define LAS __attribute__((address_space(3)))
; #define LDS_WAIT() asm volatile("s_waitcnt lgkmcnt(0)" ::: "memory")
; __device__ __forceinline__ TrItem tr_decode(const Args& a, int it) {
;     ...
;     if (r < T_IN) { const int kb = r & 31, nb = r >> 5; t.N = INCOLS; t.src = a.in[I_WIN] + (size_t)(64 * kb) * INCOLS + 64 * nb; t.dst = (bf16*)(ws + WS_WIN) + (size_t)(64 * nb) * DM + 64 * kb; return t; } r -= T_IN;
;     if (r < T_OUT) { const int kb = r & 31, nb = r >> 5; t.N = DM; t.src = a.in[I_WOUT] + (size_t)(64 * kb) * DM + 64 * nb; t.dst = (bf16*)(ws + WS_WOUT) + (size_t)(64 * nb) * DM + 64 * kb; return t; } r -= T_OUT;
;     if (r < NEXP * T_GU1) { const int e = r / T_GU1, q = r % T_GU1, kb = q & 31, nb = q >> 5, n0 = 64 * nb;
;         const int drow0 = n0 < 2048 ? (n0 >> 7) * 256 + (n0 & 127) : ((n0 - 2048) >> 7) * 256 + 128 + ((n0 - 2048) & 127);
;         t.N = 4096; t.src = a.in[I_WGU] + (size_t)e * DM * 4096 + (size_t)(64 * kb) * 4096 + n0; t.dst = (bf16*)(ws + WS_WGU) + (size_t)e * 4096 * DM + (size_t)drow0 * DM + 64 * kb; return t; } r -= NEXP * T_GU1;
;     { const int e = r / T_DN1, q = r % T_DN1, kb = q & 31, nb = q >> 5;
;         t.N = DM; t.src = a.in[I_WDN] + (size_t)e * DM * DM + (size_t)(64 * kb) * DM + 64 * nb; t.dst = (bf16*)(ws + WS_WDN) + (size_t)e * DM * DM + (size_t)(64 * nb) * DM + 64 * kb; return t; }
; __device__ __forceinline__ void tr_store(const TrItem& t, const f32x4 (&ra)[8], const f32x4 (&rb)[8], LAS unsigned* scr, int lane) {
;     ...
;     const int nr = lane >> 3, ch = lane & 7;
; #pragma unroll
;     for (int i = 0; i < 8; ++i) { const int n = nr + 8 * i; const v4u v = *(const LAS v4u*)(scr + n * 32 + ((ch ^ ((n >> 2) & 7)) << 2));
;         __builtin_nontemporal_store(v, (v4u*)(t.dst + (size_t)n * DM + 8 * ch)); }
;     LDS_WAIT(); asm volatile("" ::: "memory");
.Lcvj_5:
	s_waitcnt lgkmcnt(0)
	ds_read_b128 v[166:169], v133
	ds_read_b128 v[170:173], v135
	v_lshlrev_b32_e32 v130, 1, v134
	v_lshl_add_u64 v[178:179], s[16:17], 0, v[130:131]
	v_lshl_add_u64 v[174:175], v[178:179], 0, v[136:137]
	s_waitcnt lgkmcnt(1)
	global_store_dwordx4 v[174:175], v[166:169], off nt
	ds_read_b128 v[166:169], v152
	v_lshl_add_u64 v[174:175], v[178:179], 0, v[138:139]
	s_waitcnt lgkmcnt(1)
	global_store_dwordx4 v[174:175], v[170:173], off nt
	ds_read_b128 v[170:173], v153
	v_lshl_add_u64 v[174:175], v[178:179], 0, v[140:141]
	s_waitcnt lgkmcnt(1)
	global_store_dwordx4 v[174:175], v[166:169], off nt
	ds_read_b128 v[166:169], v154
	v_lshl_add_u64 v[174:175], v[178:179], 0, v[142:143]
	s_waitcnt lgkmcnt(1)
	global_store_dwordx4 v[174:175], v[170:173], off nt
	v_lshl_add_u64 v[174:175], v[178:179], 0, v[144:145]
	ds_read_b128 v[170:173], v155
	s_waitcnt lgkmcnt(1)
	global_store_dwordx4 v[174:175], v[166:169], off nt
	ds_read_b128 v[166:169], v156
	ds_read_b128 v[174:177], v157
	v_lshl_add_u64 v[180:181], v[178:179], 0, v[146:147]
	s_waitcnt lgkmcnt(2)
	global_store_dwordx4 v[180:181], v[170:173], off nt
	s_and_b64 vcc, exec, s[0:1]
	s_mov_b64 s[0:1], -1
	v_lshl_add_u64 v[170:171], v[178:179], 0, v[148:149]
	s_waitcnt lgkmcnt(1)
	global_store_dwordx4 v[170:171], v[166:169], off nt
	s_nop 1
	v_lshl_add_u64 v[166:167], v[178:179], 0, v[150:151]
	s_waitcnt lgkmcnt(0)
	global_store_dwordx4 v[166:167], v[174:177], off nt
	s_waitcnt lgkmcnt(0)
	s_cbranch_vccnz .LBB0_753
	s_add_i32 s6, s39, s30
	s_cmp_lt_i32 s6, 0x11000
	s_cselect_b64 s[26:27], -1, 0
	s_and_b64 s[0:1], s[26:27], exec
	s_cselect_b32 s45, s6, s44
	s_cmpk_gt_i32 s45, 0xbff
	s_mov_b64 s[34:35], -1
	s_cbranch_scc0 .LBB0_788
	s_cmpk_gt_u32 s45, 0xfff
	s_cbranch_scc0 .LBB0_782
	s_cmp_gt_u32 s45, 0x10fff
	s_mov_b64 s[30:31], -1
	s_cbranch_scc0 .LBB0_775
	s_add_i32 s0, s45, 0xfffef000
	s_lshr_b32 s6, s0, 10
	s_lshl_b64 s[0:1], s[6:7], 24
	v_readlane_b32 s52, v246, 0
	v_readlane_b32 s53, v246, 1
	s_add_u32 s0, s52, s0
	s_addc_u32 s1, s53, s1
	s_lshl_b32 s8, s45, 6
	s_and_b32 s16, s8, 0x7c0
	s_lshl_b32 s8, s16, 13
	s_add_u32 s8, s0, s8
	s_addc_u32 s9, s1, 0
	s_lshl_b32 s0, s45, 1
	s_and_b32 s0, s0, 0x7c0
	s_lshl_b32 s14, s0, 2
	s_add_u32 s28, s8, s14
	s_addc_u32 s29, s9, 0
	s_lshl_b64 s[8:9], s[6:7], 23
	s_add_u32 s24, s33, s8
	v_readlane_b32 s54, v246, 2
	v_readlane_b32 s55, v246, 3
	v_readlane_b32 s56, v246, 4
	v_readlane_b32 s57, v246, 5
	v_readlane_b32 s58, v246, 6
	v_readlane_b32 s59, v246, 7
	s_mov_b32 s17, s7
	s_mov_b32 s1, s7
	s_addc_u32 s25, s36, s9
	s_mov_b64 s[30:31], 0

; __device__ __forceinline__ void tr_load(const TrItem& t, f32x4 (&ra)[8], f32x4 (&rb)[8], int lane) {
;     const int q = lane >> 4, n4 = lane & 15;
;     const float* p = t.src + (size_t)(2 * q) * t.N + 4 * n4;
; #pragma unroll
;     for (int i = 0; i < 8; ++i) { ra[i] = __builtin_nontemporal_load((const f32x4*)(p + (size_t)(8 * i) * t.N)); rb[i] = __builtin_nontemporal_load((const f32x4*)(p + (size_t)(8 * i + 1) * t.N)); }
; }
; __device__ __forceinline__ void conv_items(const Args& a, LAS unsigned char* lds, int it0, int it1, int vcu, int G, int lane, int wave) {
;     ...
;         it = nx; nx = it + NGW; has = nx < it1;
;         cur = tr_decode(a, has ? nx : it);
;         if (has) tr_load(cur, ra, rb, lane);
;         tr_store(nxt, na, nb_, scr, lane);
.LBB0_790:
	v_mul_u32_u24_e32 v2, s30, v1
	v_lshlrev_b32_e32 v2, 2, v2
	v_mov_b32_e32 v3, v131
	v_lshl_add_u64 v[2:3], s[28:29], 0, v[2:3]
	v_lshlrev_b32_e32 v4, 2, v132
	v_mov_b32_e32 v5, v131
	v_lshl_add_u64 v[2:3], v[2:3], 0, v[4:5]
	s_lshl_b64 s[8:9], s[30:31], 2
	v_lshl_add_u64 v[10:11], v[2:3], 0, s[8:9]
	s_mul_i32 s6, s30, 28
	global_load_dwordx4 v[2:5], v[2:3], off nt
	s_nop 0
	global_load_dwordx4 v[6:9], v[10:11], off nt
	v_lshl_add_u64 v[10:11], v[10:11], 0, s[6:7]
	v_lshl_add_u64 v[18:19], v[10:11], 0, s[8:9]
	global_load_dwordx4 v[10:13], v[10:11], off nt
	s_nop 0
	global_load_dwordx4 v[14:17], v[18:19], off nt
	v_lshl_add_u64 v[18:19], v[18:19], 0, s[6:7]
	v_lshl_add_u64 v[26:27], v[18:19], 0, s[8:9]
	global_load_dwordx4 v[18:21], v[18:19], off nt
	s_nop 0
	global_load_dwordx4 v[22:25], v[26:27], off nt
	v_lshl_add_u64 v[26:27], v[26:27], 0, s[6:7]
	v_lshl_add_u64 v[34:35], v[26:27], 0, s[8:9]
	v_lshl_add_u64 v[38:39], v[34:35], 0, s[6:7]
	v_lshl_add_u64 v[42:43], v[38:39], 0, s[8:9]
	v_lshl_add_u64 v[46:47], v[42:43], 0, s[6:7]
	v_lshl_add_u64 v[50:51], v[46:47], 0, s[8:9]
	v_lshl_add_u64 v[54:55], v[50:51], 0, s[6:7]
	v_lshl_add_u64 v[58:59], v[54:55], 0, s[8:9]
	v_lshl_add_u64 v[62:63], v[58:59], 0, s[6:7]
	global_load_dwordx4 v[26:29], v[26:27], off nt
	s_nop 0
	global_load_dwordx4 v[30:33], v[34:35], off nt
	s_nop 0
	global_load_dwordx4 v[34:37], v[38:39], off nt
	s_nop 0
	global_load_dwordx4 v[38:41], v[42:43], off nt
	s_nop 0
	global_load_dwordx4 v[42:45], v[46:47], off nt
	s_nop 0
	global_load_dwordx4 v[46:49], v[50:51], off nt
	s_nop 0
	global_load_dwordx4 v[50:53], v[54:55], off nt
	s_nop 0
	global_load_dwordx4 v[54:57], v[58:59], off nt
	s_nop 0
	global_load_dwordx4 v[58:61], v[62:63], off nt
	v_lshl_add_u64 v[62:63], v[62:63], 0, s[8:9]
	global_load_dwordx4 v[62:65], v[62:63], off nt
	s_waitcnt vmcnt(24)
	s_branch .LBB0_752

; #define LAS __attribute__((address_space(3)))
; #define LDS_WAIT() asm volatile("s_waitcnt lgkmcnt(0)" ::: "memory")
; __device__ __forceinline__ unsigned cvt2bf(float lo, float hi) { const f32x2_t v = {lo, hi}; const bf16x2_t r = __builtin_convertvector(v, bf16x2_t); return __builtin_bit_cast(unsigned, r); }
; __device__ __forceinline__ void tr_load(const TrItem& t, f32x4 (&ra)[8], f32x4 (&rb)[8], int lane) {
;     const int q = lane >> 4, n4 = lane & 15;
;     const float* p = t.src + (size_t)(2 * q) * t.N + 4 * n4;
; #pragma unroll
;     for (int i = 0; i < 8; ++i) { ra[i] = __builtin_nontemporal_load((const f32x4*)(p + (size_t)(8 * i) * t.N)); rb[i] = __builtin_nontemporal_load((const f32x4*)(p + (size_t)(8 * i + 1) * t.N)); }
; }
; __device__ __forceinline__ void tr_store(const TrItem& t, const f32x4 (&ra)[8], const f32x4 (&rb)[8], LAS unsigned* scr, int lane) {
;     const int q = lane >> 4, n4 = lane & 15;
; #pragma unroll
;     for (int i = 0; i < 8; ++i)
; #pragma unroll
;         for (int j = 0; j < 4; ++j) scr[(4 * n4 + j) * 32 + ((i ^ (n4 & 7)) << 2) + q] = cvt2bf(ra[i][j], rb[i][j]);
;     LDS_WAIT(); asm volatile("" ::: "memory");
;     const int nr = lane >> 3, ch = lane & 7;
; #pragma unroll
;     for (int i = 0; i < 8; ++i) { const int n = nr + 8 * i; const v4u v = *(const LAS v4u*)(scr + n * 32 + ((ch ^ ((n >> 2) & 7)) << 2));
;         __builtin_nontemporal_store(v, (v4u*)(t.dst + (size_t)n * DM + 8 * ch)); }
;     LDS_WAIT(); asm volatile("" ::: "memory");
; }
; __device__ __forceinline__ void conv_items(const Args& a, LAS unsigned char* lds, int it0, int it1, int vcu, int G, int lane, int wave) {
;     LAS unsigned* scr = (LAS unsigned*)(lds + wave * 16384);
;     const int gw = vcu * NWAVES + wave, NGW = G * NWAVES;
;     f32x4 ra[8], rb[8], na[8], nb_[8];
;     int it = it0 + gw;
;     if (it >= it1) return;
;     TrItem cur = tr_decode(a, it);
;     tr_load(cur, ra, rb, lane);
.LBB0_834:
	v_readlane_b32 s2, v246, 33
	s_lshl_b32 s2, s2, 14
	v_readlane_b32 s15, v246, 11
	s_waitcnt vmcnt(11)
	v_lshrrev_b32_e32 v66, 3, v194
	s_add_i32 s14, s2, 0
	s_lshl_b32 s28, s15, 3
	s_lshl_b64 s[4:5], s[4:5], 12
	s_waitcnt lgkmcnt(0)
	v_and_b32_e32 v133, 6, v66
	s_add_u32 s2, s6, s4
	v_mul_u32_u24_e32 v2, s12, v133
	v_lshlrev_b32_e32 v67, 2, v194
	s_addc_u32 s4, s7, s5
	s_lshl_b64 s[0:1], s[0:1], 1
	v_lshlrev_b32_e32 v130, 2, v2
	v_mov_b32_e32 v131, 0
	v_and_b32_e32 v132, 60, v67
	s_add_u32 s6, s2, s0
	v_lshl_add_u64 v[2:3], s[8:9], 0, v[130:131]
	v_lshlrev_b32_e32 v130, 2, v132
	s_addc_u32 s7, s4, s1
	v_lshl_add_u64 v[10:11], v[2:3], 0, v[130:131]
	s_lshl_b64 s[0:1], s[12:13], 2
	s_mov_b32 s3, 0
	v_lshl_add_u64 v[12:13], v[10:11], 0, s[0:1]
	s_mul_i32 s2, s12, 28
	v_lshl_add_u64 v[18:19], v[12:13], 0, s[2:3]
	v_lshl_add_u64 v[20:21], v[18:19], 0, s[0:1]
	v_lshl_add_u64 v[26:27], v[20:21], 0, s[2:3]
	v_lshl_add_u64 v[28:29], v[26:27], 0, s[0:1]
	v_lshl_add_u64 v[34:35], v[28:29], 0, s[2:3]
	v_lshl_add_u64 v[36:37], v[34:35], 0, s[0:1]
	v_lshl_add_u64 v[38:39], v[36:37], 0, s[2:3]
	v_lshl_add_u64 v[42:43], v[38:39], 0, s[0:1]
	v_lshl_add_u64 v[46:47], v[42:43], 0, s[2:3]
	s_waitcnt vmcnt(8)
	v_lshl_add_u64 v[50:51], v[46:47], 0, s[0:1]
	s_waitcnt vmcnt(6)
	v_lshl_add_u64 v[54:55], v[50:51], 0, s[2:3]
	v_lshl_add_u64 v[58:59], v[54:55], 0, s[0:1]
	v_lshl_add_u64 v[62:63], v[58:59], 0, s[2:3]
	global_load_dwordx4 v[2:5], v[10:11], off nt
	global_load_dwordx4 v[6:9], v[12:13], off nt
	s_nop 0
	global_load_dwordx4 v[10:13], v[18:19], off nt
	global_load_dwordx4 v[14:17], v[20:21], off nt
	s_nop 0
	global_load_dwordx4 v[18:21], v[26:27], off nt
	global_load_dwordx4 v[22:25], v[28:29], off nt
	s_nop 0
	global_load_dwordx4 v[26:29], v[34:35], off nt
	global_load_dwordx4 v[30:33], v[36:37], off nt
	v_or_b32_e32 v78, 8, v66
	global_load_dwordx4 v[34:37], v[38:39], off nt
	v_bitop3_b32 v80, v78, 28, v67 bitop3:0x48
	global_load_dwordx4 v[38:41], v[42:43], off nt
	v_lshlrev_b32_e32 v79, 7, v78
	global_load_dwordx4 v[42:45], v[46:47], off nt
	v_lshlrev_b32_e32 v80, 2, v80
	global_load_dwordx4 v[46:49], v[50:51], off nt
	v_lshlrev_b32_e32 v138, 12, v78
	global_load_dwordx4 v[50:53], v[54:55], off nt
	v_or_b32_e32 v78, 16, v66
	global_load_dwordx4 v[54:57], v[58:59], off nt
	v_add3_u32 v135, s14, v79, v80
	global_load_dwordx4 v[58:61], v[62:63], off nt
	v_lshl_add_u64 v[62:63], v[62:63], 0, s[0:1]
	global_load_dwordx4 v[62:65], v[62:63], off nt
	v_bitop3_b32 v80, v78, 28, v67 bitop3:0x48
	v_lshlrev_b32_e32 v68, 9, v0
	v_lshrrev_b32_e32 v69, 2, v194
	v_mov_b32_e32 v70, 0x70
	s_movk_i32 s1, 0x50
	v_lshlrev_b32_e32 v79, 7, v78
	v_lshlrev_b32_e32 v80, 2, v80
	v_lshlrev_b32_e32 v140, 12, v78
	v_or_b32_e32 v78, 24, v66
	v_and_b32_e32 v68, 0x1e00, v68
	v_and_b32_e32 v69, 12, v69
	s_movk_i32 s0, 0x70
	v_bitop3_b32 v75, v1, s1, v70 bitop3:0x6c
	s_movk_i32 s1, 0x60
	v_add3_u32 v152, s14, v79, v80
	v_bitop3_b32 v80, v78, 28, v67 bitop3:0x48
	v_add3_u32 v68, s14, v68, v69
	v_and_b32_e32 v69, 0x70, v1
	v_bitop3_b32 v71, v1, 16, v70 bitop3:0x6c
	v_bitop3_b32 v72, v1, 32, v70 bitop3:0x6c
	v_bitop3_b32 v73, v1, 48, v70 bitop3:0x6c
	v_bitop3_b32 v74, v1, 64, v70 bitop3:0x6c
	v_bitop3_b32 v70, v1, s1, v70 bitop3:0x6c
	v_bitop3_b32 v76, v1, s0, v1 bitop3:0xc
	v_lshlrev_b32_e32 v1, 3, v0
	v_bitop3_b32 v77, v66, 28, v67 bitop3:0x48
	v_lshlrev_b32_e32 v79, 7, v78
	v_lshlrev_b32_e32 v80, 2, v80
	v_lshlrev_b32_e32 v142, 12, v78
	v_or_b32_e32 v78, 32, v66
	v_and_b32_e32 v134, 56, v1
	v_lshlrev_b32_e32 v1, 7, v66
	v_lshlrev_b32_e32 v77, 2, v77
	v_add3_u32 v153, s14, v79, v80
	v_lshlrev_b32_e32 v79, 7, v78
	v_add3_u32 v1, s14, v1, v77
	v_add3_u32 v154, s14, v79, v77
	v_or_b32_e32 v77, 40, v66
	s_add_u32 s29, s92, 0x70800000
	v_bitop3_b32 v79, v77, 28, v67 bitop3:0x48
	s_addc_u32 s30, s93, 0
	v_lshlrev_b32_e32 v136, 12, v66
	v_lshlrev_b32_e32 v144, 12, v78
	v_lshlrev_b32_e32 v78, 7, v77
	v_lshlrev_b32_e32 v79, 2, v79
	v_lshlrev_b32_e32 v146, 12, v77
	v_or_b32_e32 v77, 48, v66
	v_or_b32_e32 v66, 56, v66
	s_add_u32 s31, s92, 0x50800000
	v_add3_u32 v155, s14, v78, v79
	v_bitop3_b32 v79, v77, 28, v67 bitop3:0x48
	v_bitop3_b32 v67, v66, 28, v67 bitop3:0x48
	s_addc_u32 s33, s93, 0
	v_lshlrev_b32_e32 v78, 7, v77
	v_lshlrev_b32_e32 v79, 2, v79
	v_lshlrev_b32_e32 v148, 12, v77
	v_lshlrev_b32_e32 v77, 7, v66
	v_lshlrev_b32_e32 v67, 2, v67
	s_add_u32 s4, s92, 0x200000
	v_mov_b32_e32 v137, v131
	v_mov_b32_e32 v139, v131
	v_mov_b32_e32 v141, v131
	v_mov_b32_e32 v143, v131
	v_mov_b32_e32 v145, v131
	v_mov_b32_e32 v147, v131
	v_add3_u32 v156, s14, v78, v79
	v_mov_b32_e32 v149, v131
	v_add3_u32 v157, s14, v77, v67
	v_lshlrev_b32_e32 v150, 12, v66
	v_mov_b32_e32 v151, v131
	s_addc_u32 s5, s93, 0
	s_lshl_b32 s34, s15, 4
	v_add_u32_e32 v158, v68, v69
	v_add_u32_e32 v159, v68, v71
	v_add_u32_e32 v160, v68, v72
	v_add_u32_e32 v161, v68, v73
	v_add_u32_e32 v162, v68, v74
	v_add_u32_e32 v163, v68, v75
	v_add_u32_e32 v164, v68, v70
	v_add_u32_e32 v165, v68, v76
	s_branch .LBB0_837
; #define LAS __attribute__((address_space(3)))
; #define LDS_WAIT() asm volatile("s_waitcnt lgkmcnt(0)" ::: "memory")
; __device__ __forceinline__ unsigned cvt2bf(float lo, float hi) { const f32x2_t v = {lo, hi}; const bf16x2_t r = __builtin_convertvector(v, bf16x2_t); return __builtin_bit_cast(unsigned, r); }
; __device__ __forceinline__ void tr_store(const TrItem& t, const f32x4 (&ra)[8], const f32x4 (&rb)[8], LAS unsigned* scr, int lane) {
;     const int q = lane >> 4, n4 = lane & 15;
; #pragma unroll
;     for (int i = 0; i < 8; ++i)
; #pragma unroll
;         for (int j = 0; j < 4; ++j) scr[(4 * n4 + j) * 32 + ((i ^ (n4 & 7)) << 2) + q] = cvt2bf(ra[i][j], rb[i][j]);
;     LDS_WAIT(); asm volatile("" ::: "memory");
;     const int nr = lane >> 3, ch = lane & 7;
; #pragma unroll
;     for (int i = 0; i < 8; ++i) { const int n = nr + 8 * i; const v4u v = *(const LAS v4u*)(scr + n * 32 + ((ch ^ ((n >> 2) & 7)) << 2));
;         __builtin_nontemporal_store(v, (v4u*)(t.dst + (size_t)n * DM + 8 * ch)); }
;     LDS_WAIT(); asm volatile("" ::: "memory");
; }
; __device__ __forceinline__ void conv_items(const Args& a, LAS unsigned char* lds, int it0, int it1, int vcu, int G, int lane, int wave) {
;     ...
;         tr_store(nxt, na, nb_, scr, lane);
;         if (!has) break;
;         it = nx;
.Lcvw_6:
	s_waitcnt vmcnt(8)
.LBB0_835:
	v_cvt_pk_bf16_f32 v166, v66, v74
	v_cvt_pk_bf16_f32 v167, v67, v75
	ds_write2_b32 v158, v166, v167 offset1:32
	v_cvt_pk_bf16_f32 v166, v68, v76
	v_cvt_pk_bf16_f32 v167, v69, v77
	ds_write2_b32 v158, v166, v167 offset0:64 offset1:96
	v_cvt_pk_bf16_f32 v166, v70, v86
	v_cvt_pk_bf16_f32 v167, v71, v87
	ds_write2_b32 v159, v166, v167 offset1:32
	v_cvt_pk_bf16_f32 v166, v72, v88
	v_cvt_pk_bf16_f32 v167, v73, v89
	ds_write2_b32 v159, v166, v167 offset0:64 offset1:96
	v_cvt_pk_bf16_f32 v166, v78, v98
	v_cvt_pk_bf16_f32 v167, v79, v99
	ds_write2_b32 v160, v166, v167 offset1:32
	v_cvt_pk_bf16_f32 v166, v80, v100
	v_cvt_pk_bf16_f32 v167, v81, v101
	ds_write2_b32 v160, v166, v167 offset0:64 offset1:96
	v_cvt_pk_bf16_f32 v166, v82, v106
	v_cvt_pk_bf16_f32 v167, v83, v107
	ds_write2_b32 v161, v166, v167 offset1:32
	v_cvt_pk_bf16_f32 v166, v84, v108
	v_cvt_pk_bf16_f32 v167, v85, v109
	ds_write2_b32 v161, v166, v167 offset0:64 offset1:96
	v_cvt_pk_bf16_f32 v166, v90, v114
	v_cvt_pk_bf16_f32 v167, v91, v115
	ds_write2_b32 v162, v166, v167 offset1:32
	v_cvt_pk_bf16_f32 v166, v92, v116
	v_cvt_pk_bf16_f32 v167, v93, v117
	ds_write2_b32 v162, v166, v167 offset0:64 offset1:96
	v_cvt_pk_bf16_f32 v166, v94, v118
	v_cvt_pk_bf16_f32 v167, v95, v119
	ds_write2_b32 v163, v166, v167 offset1:32
	v_cvt_pk_bf16_f32 v166, v96, v120
	v_cvt_pk_bf16_f32 v167, v97, v121
	ds_write2_b32 v163, v166, v167 offset0:64 offset1:96
	v_cvt_pk_bf16_f32 v166, v102, v122
	v_cvt_pk_bf16_f32 v167, v103, v123
	s_lshl_b64 s[0:1], s[0:1], 12
	ds_write2_b32 v164, v166, v167 offset1:32
	v_cvt_pk_bf16_f32 v166, v104, v124
	v_cvt_pk_bf16_f32 v167, v105, v125
	s_add_u32 s2, s18, s0
	ds_write2_b32 v164, v166, v167 offset0:64 offset1:96
	v_cvt_pk_bf16_f32 v166, v110, v126
	v_cvt_pk_bf16_f32 v167, v111, v127
	s_addc_u32 s14, s19, s1
	s_lshl_b64 s[0:1], s[6:7], 1
	ds_write2_b32 v165, v166, v167 offset1:32
	v_cvt_pk_bf16_f32 v166, v112, v128
	v_cvt_pk_bf16_f32 v167, v113, v129
	s_add_u32 s6, s2, s0
	ds_write2_b32 v165, v166, v167 offset0:64 offset1:96
	s_addc_u32 s7, s14, s1
	s_add_i32 s24, s35, s28
	s_lshl_b64 s[0:1], s[8:9], 12
	s_waitcnt lgkmcnt(0)
	s_add_u32 s2, s16, s0
	s_addc_u32 s8, s17, s1
	s_lshl_b64 s[0:1], s[12:13], 1
	ds_read_b128 v[166:169], v1
	ds_read_b128 v[170:173], v135
	s_add_u32 s0, s2, s0
	s_addc_u32 s1, s8, s1
	v_lshl_add_u64 v[178:179], s[0:1], 0, v[130:131]
	v_lshl_add_u64 v[174:175], v[178:179], 0, v[136:137]
	s_waitcnt lgkmcnt(1)
	global_store_dwordx4 v[174:175], v[166:169], off nt
	ds_read_b128 v[166:169], v152
	v_lshl_add_u64 v[174:175], v[178:179], 0, v[138:139]
	s_waitcnt lgkmcnt(1)
	global_store_dwordx4 v[174:175], v[170:173], off nt
	ds_read_b128 v[170:173], v153
	v_lshl_add_u64 v[174:175], v[178:179], 0, v[140:141]
	s_waitcnt lgkmcnt(1)
	global_store_dwordx4 v[174:175], v[166:169], off nt
	ds_read_b128 v[166:169], v154
	v_lshl_add_u64 v[174:175], v[178:179], 0, v[142:143]
	s_waitcnt lgkmcnt(1)
	global_store_dwordx4 v[174:175], v[170:173], off nt
	v_lshl_add_u64 v[174:175], v[178:179], 0, v[144:145]
	ds_read_b128 v[170:173], v155
	s_waitcnt lgkmcnt(1)
	global_store_dwordx4 v[174:175], v[166:169], off nt
	ds_read_b128 v[166:169], v156
	ds_read_b128 v[174:177], v157
	v_lshl_add_u64 v[180:181], v[178:179], 0, v[146:147]
	s_waitcnt lgkmcnt(2)
	global_store_dwordx4 v[180:181], v[170:173], off nt
	s_cmp_gt_i32 s24, 0x10fff
	s_cselect_b64 s[0:1], -1, 0
	v_lshl_add_u64 v[170:171], v[178:179], 0, v[148:149]
	s_waitcnt lgkmcnt(1)
	global_store_dwordx4 v[170:171], v[166:169], off nt
	s_nop 1
	v_lshl_add_u64 v[166:167], v[178:179], 0, v[150:151]
	s_waitcnt lgkmcnt(0)
	global_store_dwordx4 v[166:167], v[174:177], off nt
	s_waitcnt lgkmcnt(0)

; #define LAS __attribute__((address_space(3)))
; __device__ __forceinline__ unsigned cvt2bf(float lo, float hi) { const f32x2_t v = {lo, hi}; const bf16x2_t r = __builtin_convertvector(v, bf16x2_t); return __builtin_bit_cast(unsigned, r); }
; __device__ __forceinline__ void tr_load(const TrItem& t, f32x4 (&ra)[8], f32x4 (&rb)[8], int lane) {
;     const int q = lane >> 4, n4 = lane & 15;
;     const float* p = t.src + (size_t)(2 * q) * t.N + 4 * n4;
; #pragma unroll
;     for (int i = 0; i < 8; ++i) { ra[i] = __builtin_nontemporal_load((const f32x4*)(p + (size_t)(8 * i) * t.N)); rb[i] = __builtin_nontemporal_load((const f32x4*)(p + (size_t)(8 * i + 1) * t.N)); }
; }
; __device__ __forceinline__ void tr_store(const TrItem& t, const f32x4 (&ra)[8], const f32x4 (&rb)[8], LAS unsigned* scr, int lane) {
;     const int q = lane >> 4, n4 = lane & 15;
; #pragma unroll
;     for (int i = 0; i < 8; ++i)
; #pragma unroll
;         for (int j = 0; j < 4; ++j) scr[(4 * n4 + j) * 32 + ((i ^ (n4 & 7)) << 2) + q] = cvt2bf(ra[i][j], rb[i][j]);
; __device__ __forceinline__ void conv_items(const Args& a, LAS unsigned char* lds, int it0, int it1, int vcu, int G, int lane, int wave) {
;     ...
;         TrItem nxt = tr_decode(a, has ? nx : it);
;         if (has) tr_load(nxt, na, nb_, lane);
;         tr_store(cur, ra, rb, scr, lane);
.LBB0_852:
	v_mul_u32_u24_e32 v66, s22, v133
	v_lshlrev_b32_e32 v130, 2, v66
	v_lshl_add_u64 v[66:67], s[20:21], 0, v[130:131]
	v_lshlrev_b32_e32 v130, 2, v132
	v_lshl_add_u64 v[66:67], v[66:67], 0, v[130:131]
	s_lshl_b64 s[14:15], s[22:23], 2
	v_lshl_add_u64 v[70:71], v[66:67], 0, s[14:15]
	s_mul_i32 s2, s22, 28
	global_load_dwordx4 v[66:69], v[66:67], off nt
	s_nop 0
	global_load_dwordx4 v[74:77], v[70:71], off nt
	v_lshl_add_u64 v[70:71], v[70:71], 0, s[2:3]
	v_lshl_add_u64 v[78:79], v[70:71], 0, s[14:15]
	global_load_dwordx4 v[70:73], v[70:71], off nt
	s_nop 0
	global_load_dwordx4 v[86:89], v[78:79], off nt
	v_lshl_add_u64 v[78:79], v[78:79], 0, s[2:3]
	v_lshl_add_u64 v[82:83], v[78:79], 0, s[14:15]
	global_load_dwordx4 v[78:81], v[78:79], off nt
	s_nop 0
	global_load_dwordx4 v[98:101], v[82:83], off nt
	v_lshl_add_u64 v[82:83], v[82:83], 0, s[2:3]
	v_lshl_add_u64 v[90:91], v[82:83], 0, s[14:15]
	v_lshl_add_u64 v[94:95], v[90:91], 0, s[2:3]
	global_load_dwordx4 v[82:85], v[82:83], off nt
	s_nop 0
	global_load_dwordx4 v[106:109], v[90:91], off nt
	s_nop 0
	global_load_dwordx4 v[90:93], v[94:95], off nt
	v_lshl_add_u64 v[94:95], v[94:95], 0, s[14:15]
	v_lshl_add_u64 v[102:103], v[94:95], 0, s[2:3]
	global_load_dwordx4 v[114:117], v[94:95], off nt
	s_nop 0
	global_load_dwordx4 v[94:97], v[102:103], off nt
	v_lshl_add_u64 v[102:103], v[102:103], 0, s[14:15]
	v_lshl_add_u64 v[110:111], v[102:103], 0, s[2:3]
	global_load_dwordx4 v[118:121], v[102:103], off nt
	s_nop 0
	global_load_dwordx4 v[102:105], v[110:111], off nt
	v_lshl_add_u64 v[110:111], v[110:111], 0, s[14:15]
	v_lshl_add_u64 v[126:127], v[110:111], 0, s[2:3]
	global_load_dwordx4 v[122:125], v[110:111], off nt
	s_nop 0
	global_load_dwordx4 v[110:113], v[126:127], off nt
	v_lshl_add_u64 v[126:127], v[126:127], 0, s[14:15]
	global_load_dwordx4 v[126:129], v[126:127], off nt
	s_waitcnt vmcnt(30)
	v_cvt_pk_bf16_f32 v130, v2, v6
	v_cvt_pk_bf16_f32 v166, v3, v7
	ds_write2_b32 v158, v130, v166 offset1:32
	v_cvt_pk_bf16_f32 v130, v4, v8
	v_cvt_pk_bf16_f32 v166, v5, v9
	ds_write2_b32 v158, v130, v166 offset0:64 offset1:96
	s_waitcnt vmcnt(28)
	v_cvt_pk_bf16_f32 v130, v10, v14
	v_cvt_pk_bf16_f32 v166, v11, v15
	ds_write2_b32 v159, v130, v166 offset1:32
	v_cvt_pk_bf16_f32 v130, v12, v16
	v_cvt_pk_bf16_f32 v166, v13, v17
	ds_write2_b32 v159, v130, v166 offset0:64 offset1:96
	s_waitcnt vmcnt(26)
	v_cvt_pk_bf16_f32 v130, v18, v22
	v_cvt_pk_bf16_f32 v166, v19, v23
	ds_write2_b32 v160, v130, v166 offset1:32
	v_cvt_pk_bf16_f32 v130, v20, v24
	v_cvt_pk_bf16_f32 v166, v21, v25
	ds_write2_b32 v160, v130, v166 offset0:64 offset1:96
	s_waitcnt vmcnt(24)
	v_cvt_pk_bf16_f32 v130, v26, v30
	v_cvt_pk_bf16_f32 v166, v27, v31
	ds_write2_b32 v161, v130, v166 offset1:32
	v_cvt_pk_bf16_f32 v130, v28, v32
	v_cvt_pk_bf16_f32 v166, v29, v33
	ds_write2_b32 v161, v130, v166 offset0:64 offset1:96
	s_waitcnt vmcnt(22)
	v_cvt_pk_bf16_f32 v130, v34, v38
	v_cvt_pk_bf16_f32 v166, v35, v39
	ds_write2_b32 v162, v130, v166 offset1:32
	v_cvt_pk_bf16_f32 v130, v36, v40
	v_cvt_pk_bf16_f32 v166, v37, v41
	ds_write2_b32 v162, v130, v166 offset0:64 offset1:96
	s_waitcnt vmcnt(20)
	v_cvt_pk_bf16_f32 v130, v42, v46
	v_cvt_pk_bf16_f32 v166, v43, v47
	ds_write2_b32 v163, v130, v166 offset1:32
	v_cvt_pk_bf16_f32 v130, v44, v48
	v_cvt_pk_bf16_f32 v166, v45, v49
	ds_write2_b32 v163, v130, v166 offset0:64 offset1:96
	s_waitcnt vmcnt(18)
	v_cvt_pk_bf16_f32 v130, v50, v54
	v_cvt_pk_bf16_f32 v166, v51, v55
	ds_write2_b32 v164, v130, v166 offset1:32
	v_cvt_pk_bf16_f32 v130, v52, v56
	v_cvt_pk_bf16_f32 v166, v53, v57
	ds_write2_b32 v164, v130, v166 offset0:64 offset1:96
	s_waitcnt vmcnt(16)
	v_cvt_pk_bf16_f32 v130, v58, v62
	v_cvt_pk_bf16_f32 v166, v59, v63
	ds_write2_b32 v165, v130, v166 offset1:32
	v_cvt_pk_bf16_f32 v130, v60, v64
	v_cvt_pk_bf16_f32 v166, v61, v65
	ds_write2_b32 v165, v130, v166 offset0:64 offset1:96
	s_branch .Lcvj_6

; #define LAS __attribute__((address_space(3)))
; #define LDS_WAIT() asm volatile("s_waitcnt lgkmcnt(0)" ::: "memory")
; __device__ __forceinline__ TrItem tr_decode(const Args& a, int it) {
;     ...
;     if (r < T_IN) { const int kb = r & 31, nb = r >> 5; t.N = INCOLS; t.src = a.in[I_WIN] + (size_t)(64 * kb) * INCOLS + 64 * nb; t.dst = (bf16*)(ws + WS_WIN) + (size_t)(64 * nb) * DM + 64 * kb; return t; } r -= T_IN;
;     if (r < T_OUT) { const int kb = r & 31, nb = r >> 5; t.N = DM; t.src = a.in[I_WOUT] + (size_t)(64 * kb) * DM + 64 * nb; t.dst = (bf16*)(ws + WS_WOUT) + (size_t)(64 * nb) * DM + 64 * kb; return t; } r -= T_OUT;
;     if (r < NEXP * T_GU1) { const int e = r / T_GU1, q = r % T_GU1, kb = q & 31, nb = q >> 5, n0 = 64 * nb;
;         const int drow0 = n0 < 2048 ? (n0 >> 7) * 256 + (n0 & 127) : ((n0 - 2048) >> 7) * 256 + 128 + ((n0 - 2048) & 127);
;         t.N = 4096; t.src = a.in[I_WGU] + (size_t)e * DM * 4096 + (size_t)(64 * kb) * 4096 + n0; t.dst = (bf16*)(ws + WS_WGU) + (size_t)e * 4096 * DM + (size_t)drow0 * DM + 64 * kb; return t; } r -= NEXP * T_GU1;
;     { const int e = r / T_DN1, q = r % T_DN1, kb = q & 31, nb = q >> 5;
;         t.N = DM; t.src = a.in[I_WDN] + (size_t)e * DM * DM + (size_t)(64 * kb) * DM + 64 * nb; t.dst = (bf16*)(ws + WS_WDN) + (size_t)e * DM * DM + (size_t)(64 * nb) * DM + 64 * kb; return t; }
; __device__ __forceinline__ void tr_store(const TrItem& t, const f32x4 (&ra)[8], const f32x4 (&rb)[8], LAS unsigned* scr, int lane) {
;     ...
;     const int nr = lane >> 3, ch = lane & 7;
; #pragma unroll
;     for (int i = 0; i < 8; ++i) { const int n = nr + 8 * i; const v4u v = *(const LAS v4u*)(scr + n * 32 + ((ch ^ ((n >> 2) & 7)) << 2));
;         __builtin_nontemporal_store(v, (v4u*)(t.dst + (size_t)n * DM + 8 * ch)); }
;     LDS_WAIT(); asm volatile("" ::: "memory");
.Lcvj_6:
	s_waitcnt lgkmcnt(0)
	ds_read_b128 v[166:169], v1
	ds_read_b128 v[170:173], v135
	v_lshlrev_b32_e32 v130, 1, v134
	v_lshl_add_u64 v[178:179], s[6:7], 0, v[130:131]
	v_lshl_add_u64 v[174:175], v[178:179], 0, v[136:137]
	s_waitcnt lgkmcnt(1)
	global_store_dwordx4 v[174:175], v[166:169], off nt
	ds_read_b128 v[166:169], v152
	v_lshl_add_u64 v[174:175], v[178:179], 0, v[138:139]
	s_waitcnt lgkmcnt(1)
	global_store_dwordx4 v[174:175], v[170:173], off nt
	ds_read_b128 v[170:173], v153
	v_lshl_add_u64 v[174:175], v[178:179], 0, v[140:141]
	s_waitcnt lgkmcnt(1)
	global_store_dwordx4 v[174:175], v[166:169], off nt
	ds_read_b128 v[166:169], v154
	v_lshl_add_u64 v[174:175], v[178:179], 0, v[142:143]
	s_waitcnt lgkmcnt(1)
	global_store_dwordx4 v[174:175], v[170:173], off nt
	v_lshl_add_u64 v[174:175], v[178:179], 0, v[144:145]
	ds_read_b128 v[170:173], v155
	s_waitcnt lgkmcnt(1)
	global_store_dwordx4 v[174:175], v[166:169], off nt
	ds_read_b128 v[166:169], v156
	ds_read_b128 v[174:177], v157
	v_lshl_add_u64 v[180:181], v[178:179], 0, v[146:147]
	s_waitcnt lgkmcnt(2)
	global_store_dwordx4 v[180:181], v[170:173], off nt
	s_and_b64 vcc, exec, s[0:1]
	s_mov_b64 s[0:1], -1
	v_lshl_add_u64 v[170:171], v[178:179], 0, v[148:149]
	s_waitcnt lgkmcnt(1)
	global_store_dwordx4 v[170:171], v[166:169], off nt
	s_nop 1
	v_lshl_add_u64 v[166:167], v[178:179], 0, v[150:151]
	s_waitcnt lgkmcnt(0)
	global_store_dwordx4 v[166:167], v[174:177], off nt
	s_waitcnt lgkmcnt(0)
	s_cbranch_vccnz .LBB0_836
	s_add_i32 s2, s34, s24
	s_cmp_lt_i32 s2, 0x11000
	s_cselect_b64 s[20:21], -1, 0
	s_and_b64 s[0:1], s[20:21], exec
	s_cselect_b32 s36, s2, s35
	s_cmpk_gt_i32 s36, 0xbff
	s_mov_b64 s[26:27], -1
	s_cbranch_scc0 .LBB0_871
	s_cmpk_gt_u32 s36, 0xfff
	s_cbranch_scc0 .LBB0_865
	s_cmp_gt_u32 s36, 0x10fff
	s_mov_b64 s[24:25], -1
	s_cbranch_scc0 .LBB0_858
	s_add_i32 s0, s36, 0xfffef000
	s_lshr_b32 s2, s0, 10
	s_lshl_b64 s[0:1], s[2:3], 24
	v_readlane_b32 s52, v246, 0
	v_readlane_b32 s53, v246, 1
	s_add_u32 s0, s52, s0
	s_addc_u32 s1, s53, s1
	s_lshl_b32 s6, s36, 6
	s_and_b32 s6, s6, 0x7c0
	s_lshl_b32 s14, s6, 13
	s_add_u32 s14, s0, s14
	s_addc_u32 s15, s1, 0
	s_lshl_b32 s0, s36, 1
	s_and_b32 s0, s0, 0x7c0
	s_lshl_b32 s18, s0, 2
	s_add_u32 s22, s14, s18
	s_addc_u32 s23, s15, 0
	s_lshl_b64 s[14:15], s[2:3], 23
	s_add_u32 s18, s29, s14
	v_readlane_b32 s54, v246, 2
	v_readlane_b32 s55, v246, 3
	v_readlane_b32 s56, v246, 4
	v_readlane_b32 s57, v246, 5
	v_readlane_b32 s58, v246, 6
	v_readlane_b32 s59, v246, 7
	s_mov_b32 s7, s3
	s_mov_b32 s1, s3
	s_addc_u32 s19, s30, s15
	s_mov_b64 s[24:25], 0

; __device__ __forceinline__ void tr_load(const TrItem& t, f32x4 (&ra)[8], f32x4 (&rb)[8], int lane) {
;     const int q = lane >> 4, n4 = lane & 15;
;     const float* p = t.src + (size_t)(2 * q) * t.N + 4 * n4;
; #pragma unroll
;     for (int i = 0; i < 8; ++i) { ra[i] = __builtin_nontemporal_load((const f32x4*)(p + (size_t)(8 * i) * t.N)); rb[i] = __builtin_nontemporal_load((const f32x4*)(p + (size_t)(8 * i + 1) * t.N)); }
; }
; __device__ __forceinline__ void conv_items(const Args& a, LAS unsigned char* lds, int it0, int it1, int vcu, int G, int lane, int wave) {
;     ...
;         it = nx; nx = it + NGW; has = nx < it1;
;         cur = tr_decode(a, has ? nx : it);
;         if (has) tr_load(cur, ra, rb, lane);
;         tr_store(nxt, na, nb_, scr, lane);
.LBB0_873:
	v_mul_u32_u24_e32 v2, s24, v133
	v_lshlrev_b32_e32 v2, 2, v2
	v_mov_b32_e32 v3, v131
	v_lshl_add_u64 v[2:3], s[22:23], 0, v[2:3]
	v_lshlrev_b32_e32 v4, 2, v132
	v_mov_b32_e32 v5, v131
	v_lshl_add_u64 v[2:3], v[2:3], 0, v[4:5]
	s_lshl_b64 s[14:15], s[24:25], 2
	v_lshl_add_u64 v[10:11], v[2:3], 0, s[14:15]
	s_mul_i32 s2, s24, 28
	global_load_dwordx4 v[2:5], v[2:3], off nt
	s_nop 0
	global_load_dwordx4 v[6:9], v[10:11], off nt
	v_lshl_add_u64 v[10:11], v[10:11], 0, s[2:3]
	v_lshl_add_u64 v[18:19], v[10:11], 0, s[14:15]
	global_load_dwordx4 v[10:13], v[10:11], off nt
	s_nop 0
	global_load_dwordx4 v[14:17], v[18:19], off nt
	v_lshl_add_u64 v[18:19], v[18:19], 0, s[2:3]
	v_lshl_add_u64 v[26:27], v[18:19], 0, s[14:15]
	global_load_dwordx4 v[18:21], v[18:19], off nt
	s_nop 0
	global_load_dwordx4 v[22:25], v[26:27], off nt
	v_lshl_add_u64 v[26:27], v[26:27], 0, s[2:3]
	v_lshl_add_u64 v[34:35], v[26:27], 0, s[14:15]
	v_lshl_add_u64 v[38:39], v[34:35], 0, s[2:3]
	v_lshl_add_u64 v[42:43], v[38:39], 0, s[14:15]
	v_lshl_add_u64 v[46:47], v[42:43], 0, s[2:3]
	v_lshl_add_u64 v[50:51], v[46:47], 0, s[14:15]
	v_lshl_add_u64 v[54:55], v[50:51], 0, s[2:3]
	v_lshl_add_u64 v[58:59], v[54:55], 0, s[14:15]
	v_lshl_add_u64 v[62:63], v[58:59], 0, s[2:3]
	global_load_dwordx4 v[26:29], v[26:27], off nt
	s_nop 0
	global_load_dwordx4 v[30:33], v[34:35], off nt
	s_nop 0
	global_load_dwordx4 v[34:37], v[38:39], off nt
	s_nop 0
	global_load_dwordx4 v[38:41], v[42:43], off nt
	s_nop 0
	global_load_dwordx4 v[42:45], v[46:47], off nt
	s_nop 0
	global_load_dwordx4 v[46:49], v[50:51], off nt
	s_nop 0
	global_load_dwordx4 v[50:53], v[54:55], off nt
	s_nop 0
	global_load_dwordx4 v[54:57], v[58:59], off nt
	s_nop 0
	global_load_dwordx4 v[58:61], v[62:63], off nt
	v_lshl_add_u64 v[62:63], v[62:63], 0, s[14:15]
	global_load_dwordx4 v[62:65], v[62:63], off nt
	s_waitcnt vmcnt(24)
	s_branch .LBB0_835

; #define LAS __attribute__((address_space(3)))
; #define LDS_WAIT() asm volatile("s_waitcnt lgkmcnt(0)" ::: "memory")
; __device__ __forceinline__ unsigned cvt2bf(float lo, float hi) { const f32x2_t v = {lo, hi}; const bf16x2_t r = __builtin_convertvector(v, bf16x2_t); return __builtin_bit_cast(unsigned, r); }
; __device__ __forceinline__ void tr_load(const TrItem& t, f32x4 (&ra)[8], f32x4 (&rb)[8], int lane) {
;     const int q = lane >> 4, n4 = lane & 15;
;     const float* p = t.src + (size_t)(2 * q) * t.N + 4 * n4;
; #pragma unroll
;     for (int i = 0; i < 8; ++i) { ra[i] = __builtin_nontemporal_load((const f32x4*)(p + (size_t)(8 * i) * t.N)); rb[i] = __builtin_nontemporal_load((const f32x4*)(p + (size_t)(8 * i + 1) * t.N)); }
; }
; __device__ __forceinline__ void tr_store(const TrItem& t, const f32x4 (&ra)[8], const f32x4 (&rb)[8], LAS unsigned* scr, int lane) {
;     const int q = lane >> 4, n4 = lane & 15;
; #pragma unroll
;     for (int i = 0; i < 8; ++i)
; #pragma unroll
;         for (int j = 0; j < 4; ++j) scr[(4 * n4 + j) * 32 + ((i ^ (n4 & 7)) << 2) + q] = cvt2bf(ra[i][j], rb[i][j]);
;     LDS_WAIT(); asm volatile("" ::: "memory");
;     const int nr = lane >> 3, ch = lane & 7;
; #pragma unroll
;     for (int i = 0; i < 8; ++i) { const int n = nr + 8 * i; const v4u v = *(const LAS v4u*)(scr + n * 32 + ((ch ^ ((n >> 2) & 7)) << 2));
;         __builtin_nontemporal_store(v, (v4u*)(t.dst + (size_t)n * DM + 8 * ch)); }
;     LDS_WAIT(); asm volatile("" ::: "memory");
; }
; __device__ __forceinline__ void conv_items(const Args& a, LAS unsigned char* lds, int it0, int it1, int vcu, int G, int lane, int wave) {
;     LAS unsigned* scr = (LAS unsigned*)(lds + wave * 16384);
;     const int gw = vcu * NWAVES + wave, NGW = G * NWAVES;
;     f32x4 ra[8], rb[8], na[8], nb_[8];
;     int it = it0 + gw;
;     if (it >= it1) return;
;     TrItem cur = tr_decode(a, it);
;     tr_load(cur, ra, rb, lane);
.LBB0_1183:
	s_lshl_b32 s14, s39, 14
	s_waitcnt vmcnt(11)
	v_add_u32_e32 v67, s38, v194
	s_add_i32 s36, s14, 0
	s_lshl_b64 s[2:3], s[2:3], 12
	s_add_u32 s14, s34, s2
	v_ashrrev_i32_e32 v66, 3, v67
	s_addc_u32 s15, s35, s3
	s_lshl_b64 s[2:3], s[28:29], 1
	s_waitcnt vmcnt(0)
	v_and_b32_e32 v130, -2, v66
	s_add_u32 s2, s14, s2
	v_ashrrev_i32_e32 v1, 31, v130
	s_addc_u32 s3, s15, s3
	v_mul_lo_u32 v4, s30, v1
	v_mul_lo_u32 v5, s31, v130
	v_mad_u64_u32 v[2:3], s[14:15], s30, v130, 0
	s_waitcnt vmcnt(9)
	v_lshlrev_b32_e32 v70, 2, v67
	v_add3_u32 v3, v3, v4, v5
	v_and_b32_e32 v132, 60, v70
	v_lshl_add_u64 v[2:3], v[2:3], 2, s[4:5]
	v_lshlrev_b32_e32 v148, 2, v132
	v_lshl_add_u64 v[2:3], v[2:3], 0, v[148:149]
	s_lshl_b64 s[4:5], s[30:31], 2
	v_lshl_add_u64 v[10:11], v[2:3], 0, s[4:5]
	s_mul_i32 s24, s30, 28
	global_load_dwordx4 v[2:5], v[2:3], off nt
	s_nop 0
	global_load_dwordx4 v[6:9], v[10:11], off nt
	v_lshl_add_u64 v[10:11], v[10:11], 0, s[24:25]
	v_lshl_add_u64 v[18:19], v[10:11], 0, s[4:5]
	global_load_dwordx4 v[10:13], v[10:11], off nt
	s_nop 0
	global_load_dwordx4 v[14:17], v[18:19], off nt
	v_lshl_add_u64 v[18:19], v[18:19], 0, s[24:25]
	v_lshl_add_u64 v[26:27], v[18:19], 0, s[4:5]
	global_load_dwordx4 v[18:21], v[18:19], off nt
	s_nop 0
	global_load_dwordx4 v[22:25], v[26:27], off nt
	v_lshl_add_u64 v[26:27], v[26:27], 0, s[24:25]
	v_lshl_add_u64 v[34:35], v[26:27], 0, s[4:5]
	v_lshl_add_u64 v[38:39], v[34:35], 0, s[24:25]
	v_lshl_add_u64 v[42:43], v[38:39], 0, s[4:5]
	v_lshl_add_u64 v[46:47], v[42:43], 0, s[24:25]
	s_waitcnt vmcnt(14)
	v_lshl_add_u64 v[50:51], v[46:47], 0, s[4:5]
	s_waitcnt vmcnt(12)
	v_lshl_add_u64 v[54:55], v[50:51], 0, s[24:25]
	v_lshl_add_u64 v[58:59], v[54:55], 0, s[4:5]
	v_lshl_add_u64 v[62:63], v[58:59], 0, s[24:25]
	global_load_dwordx4 v[26:29], v[26:27], off nt
	s_nop 0
	global_load_dwordx4 v[30:33], v[34:35], off nt
	v_ashrrev_i32_e32 v68, 4, v67
	global_load_dwordx4 v[34:37], v[38:39], off nt
	v_lshlrev_b32_e32 v69, 9, v67
	global_load_dwordx4 v[38:41], v[42:43], off nt
	v_and_b32_e32 v69, 0x1e00, v69
	global_load_dwordx4 v[42:45], v[46:47], off nt
	v_lshlrev_b32_e32 v68, 2, v68
	global_load_dwordx4 v[46:49], v[50:51], off nt
	v_add3_u32 v71, s36, v69, v68
	global_load_dwordx4 v[50:53], v[54:55], off nt
	v_lshlrev_b32_e32 v68, 4, v67
	global_load_dwordx4 v[54:57], v[58:59], off nt
	v_and_b32_e32 v72, 0x70, v68
	global_load_dwordx4 v[58:61], v[62:63], off nt
	v_lshl_add_u64 v[62:63], v[62:63], 0, s[4:5]
	global_load_dwordx4 v[62:65], v[62:63], off nt
	s_movk_i32 s4, 0x50
	v_bitop3_b32 v73, v68, 16, v166 bitop3:0x6c
	v_bitop3_b32 v74, v68, 32, v166 bitop3:0x6c
	v_bitop3_b32 v75, v68, 48, v166 bitop3:0x6c
	v_bitop3_b32 v76, v68, 64, v166 bitop3:0x6c
	v_bitop3_b32 v77, v68, s4, v166 bitop3:0x6c
	v_bitop3_b32 v78, v68, s59, v166 bitop3:0x6c
	v_bitop3_b32 v79, v68, s60, v68 bitop3:0xc
	v_lshlrev_b32_e32 v67, 3, v67
	v_bitop3_b32 v68, v66, 28, v70 bitop3:0x48
	v_and_b32_e32 v134, 56, v67
	v_lshlrev_b32_e32 v67, 7, v66
	v_lshlrev_b32_e32 v80, 2, v68
	v_add_u32_e32 v68, 8, v66
	v_add3_u32 v131, s36, v67, v80
	v_ashrrev_i32_e32 v67, 31, v66
	v_bitop3_b32 v69, v68, 28, v70 bitop3:0x48
	v_lshlrev_b64 v[136:137], 12, v[66:67]
	v_lshlrev_b32_e32 v67, 7, v68
	v_lshlrev_b32_e32 v69, 2, v69
	v_add3_u32 v133, s36, v67, v69
	v_ashrrev_i32_e32 v69, 31, v68
	v_lshlrev_b64 v[138:139], 12, v[68:69]
	v_add_u32_e32 v68, 16, v66
	v_bitop3_b32 v69, v68, 28, v70 bitop3:0x48
	v_lshlrev_b32_e32 v67, 7, v68
	v_lshlrev_b32_e32 v69, 2, v69
	v_add3_u32 v135, s36, v67, v69
	v_ashrrev_i32_e32 v69, 31, v68
	v_lshlrev_b64 v[140:141], 12, v[68:69]
	v_add_u32_e32 v68, 24, v66
	v_bitop3_b32 v69, v68, 28, v70 bitop3:0x48
	v_lshlrev_b32_e32 v67, 7, v68
	v_lshlrev_b32_e32 v69, 2, v69
	v_add3_u32 v168, s36, v67, v69
	v_ashrrev_i32_e32 v69, 31, v68
	v_lshlrev_b64 v[142:143], 12, v[68:69]
	v_add_u32_e32 v68, 32, v66
	v_ashrrev_i32_e32 v69, 31, v68
	v_lshlrev_b32_e32 v67, 7, v68
	v_lshlrev_b64 v[144:145], 12, v[68:69]
	v_add_u32_e32 v68, 40, v66
	v_bitop3_b32 v69, v68, 28, v70 bitop3:0x48
	v_add3_u32 v169, s36, v67, v80
	v_lshlrev_b32_e32 v67, 7, v68
	v_lshlrev_b32_e32 v69, 2, v69
	v_add3_u32 v170, s36, v67, v69
	v_ashrrev_i32_e32 v69, 31, v68
	v_lshlrev_b64 v[152:153], 12, v[68:69]
	v_add_u32_e32 v68, 48, v66
	v_bitop3_b32 v69, v68, 28, v70 bitop3:0x48
	v_lshlrev_b32_e32 v67, 7, v68
	v_lshlrev_b32_e32 v69, 2, v69
	v_add3_u32 v171, s36, v67, v69
	v_ashrrev_i32_e32 v69, 31, v68
	v_add_u32_e32 v66, 56, v66
	v_lshlrev_b64 v[154:155], 12, v[68:69]
	v_bitop3_b32 v68, v66, 28, v70 bitop3:0x48
	v_lshlrev_b32_e32 v67, 7, v66
	v_lshlrev_b32_e32 v68, 2, v68
	v_add3_u32 v172, s36, v67, v68
	v_ashrrev_i32_e32 v67, 31, v66
	v_lshlrev_b64 v[156:157], 12, v[66:67]
	v_add_u32_e32 v173, v71, v72
	v_add_u32_e32 v174, v71, v73
	v_add_u32_e32 v175, v71, v74
	v_add_u32_e32 v176, v71, v75
	v_add_u32_e32 v177, v71, v76
	v_add_u32_e32 v178, v71, v77
	v_add_u32_e32 v179, v71, v78
	v_add_u32_e32 v180, v71, v79
	s_branch .LBB0_1186
; #define LAS __attribute__((address_space(3)))
; #define LDS_WAIT() asm volatile("s_waitcnt lgkmcnt(0)" ::: "memory")
; __device__ __forceinline__ unsigned cvt2bf(float lo, float hi) { const f32x2_t v = {lo, hi}; const bf16x2_t r = __builtin_convertvector(v, bf16x2_t); return __builtin_bit_cast(unsigned, r); }
; __device__ __forceinline__ void tr_store(const TrItem& t, const f32x4 (&ra)[8], const f32x4 (&rb)[8], LAS unsigned* scr, int lane) {
;     const int q = lane >> 4, n4 = lane & 15;
; #pragma unroll
;     for (int i = 0; i < 8; ++i)
; #pragma unroll
;         for (int j = 0; j < 4; ++j) scr[(4 * n4 + j) * 32 + ((i ^ (n4 & 7)) << 2) + q] = cvt2bf(ra[i][j], rb[i][j]);
;     LDS_WAIT(); asm volatile("" ::: "memory");
;     const int nr = lane >> 3, ch = lane & 7;
; #pragma unroll
;     for (int i = 0; i < 8; ++i) { const int n = nr + 8 * i; const v4u v = *(const LAS v4u*)(scr + n * 32 + ((ch ^ ((n >> 2) & 7)) << 2));
;         __builtin_nontemporal_store(v, (v4u*)(t.dst + (size_t)n * DM + 8 * ch)); }
;     LDS_WAIT(); asm volatile("" ::: "memory");
; }
; __device__ __forceinline__ void conv_items(const Args& a, LAS unsigned char* lds, int it0, int it1, int vcu, int G, int lane, int wave) {
;     ...
;         tr_store(nxt, na, nb_, scr, lane);
;         if (!has) break;
;         it = nx;
.Lcvw_7:
	s_waitcnt vmcnt(8)
.LBB0_1184:
	v_cvt_pk_bf16_f32 v181, v66, v74
	v_cvt_pk_bf16_f32 v182, v67, v75
	ds_write2_b32 v173, v181, v182 offset1:32
	v_cvt_pk_bf16_f32 v181, v68, v76
	v_cvt_pk_bf16_f32 v182, v69, v77
	ds_write2_b32 v173, v181, v182 offset0:64 offset1:96
	v_cvt_pk_bf16_f32 v181, v70, v86
	v_cvt_pk_bf16_f32 v182, v71, v87
	ds_write2_b32 v174, v181, v182 offset1:32
	v_cvt_pk_bf16_f32 v181, v72, v88
	v_cvt_pk_bf16_f32 v182, v73, v89
	ds_write2_b32 v174, v181, v182 offset0:64 offset1:96
	v_cvt_pk_bf16_f32 v181, v78, v98
	v_cvt_pk_bf16_f32 v182, v79, v99
	ds_write2_b32 v175, v181, v182 offset1:32
	v_cvt_pk_bf16_f32 v181, v80, v100
	v_cvt_pk_bf16_f32 v182, v81, v101
	ds_write2_b32 v175, v181, v182 offset0:64 offset1:96
	v_cvt_pk_bf16_f32 v181, v82, v106
	v_cvt_pk_bf16_f32 v182, v83, v107
	ds_write2_b32 v176, v181, v182 offset1:32
	v_cvt_pk_bf16_f32 v181, v84, v108
	v_cvt_pk_bf16_f32 v182, v85, v109
	ds_write2_b32 v176, v181, v182 offset0:64 offset1:96
	v_cvt_pk_bf16_f32 v181, v90, v114
	v_cvt_pk_bf16_f32 v182, v91, v115
	ds_write2_b32 v177, v181, v182 offset1:32
	v_cvt_pk_bf16_f32 v181, v92, v116
	v_cvt_pk_bf16_f32 v182, v93, v117
	ds_write2_b32 v177, v181, v182 offset0:64 offset1:96
	v_cvt_pk_bf16_f32 v181, v94, v118
	v_cvt_pk_bf16_f32 v182, v95, v119
	ds_write2_b32 v178, v181, v182 offset1:32
	v_cvt_pk_bf16_f32 v181, v96, v120
	v_cvt_pk_bf16_f32 v182, v97, v121
	ds_write2_b32 v178, v181, v182 offset0:64 offset1:96
	v_cvt_pk_bf16_f32 v181, v102, v122
	v_cvt_pk_bf16_f32 v182, v103, v123
	s_lshl_b64 s[2:3], s[2:3], 12
	ds_write2_b32 v179, v181, v182 offset1:32
	v_cvt_pk_bf16_f32 v181, v104, v124
	v_cvt_pk_bf16_f32 v182, v105, v125
	s_add_u32 s14, s36, s2
	ds_write2_b32 v179, v181, v182 offset0:64 offset1:96
	v_cvt_pk_bf16_f32 v181, v110, v126
	v_cvt_pk_bf16_f32 v182, v111, v127
	s_addc_u32 s15, s37, s3
	s_lshl_b64 s[2:3], s[4:5], 1
	ds_write2_b32 v180, v181, v182 offset1:32
	v_cvt_pk_bf16_f32 v181, v112, v128
	v_cvt_pk_bf16_f32 v182, v113, v129
	s_add_u32 s2, s14, s2
	ds_write2_b32 v180, v181, v182 offset0:64 offset1:96
	s_addc_u32 s3, s15, s3
	s_add_i32 s44, s65, s56
	s_lshl_b64 s[4:5], s[28:29], 12
	s_waitcnt lgkmcnt(0)
	s_add_u32 s14, s34, s4
	s_addc_u32 s15, s35, s5
	s_lshl_b64 s[4:5], s[30:31], 1
	ds_read_b128 v[182:185], v131
	ds_read_b128 v[186:189], v133
	s_add_u32 s4, s14, s4
	s_addc_u32 s5, s15, s5
	v_lshl_add_u64 v[196:197], s[4:5], 0, v[148:149]
	v_lshl_add_u64 v[190:191], v[196:197], 0, v[136:137]
	s_waitcnt lgkmcnt(1)
	global_store_dwordx4 v[190:191], v[182:185], off nt
	ds_read_b128 v[182:185], v135
	v_lshl_add_u64 v[190:191], v[196:197], 0, v[138:139]
	s_waitcnt lgkmcnt(1)
	global_store_dwordx4 v[190:191], v[186:189], off nt
	ds_read_b128 v[186:189], v168
	v_lshl_add_u64 v[190:191], v[196:197], 0, v[140:141]
	s_waitcnt lgkmcnt(1)
	global_store_dwordx4 v[190:191], v[182:185], off nt
	ds_read_b128 v[182:185], v169
	v_lshl_add_u64 v[190:191], v[196:197], 0, v[142:143]
	s_waitcnt lgkmcnt(1)
	global_store_dwordx4 v[190:191], v[186:189], off nt
	v_lshl_add_u64 v[190:191], v[196:197], 0, v[144:145]
	ds_read_b128 v[186:189], v170
	s_waitcnt lgkmcnt(1)
	global_store_dwordx4 v[190:191], v[182:185], off nt
	ds_read_b128 v[182:185], v171
	ds_read_b128 v[190:193], v172
	v_lshl_add_u64 v[198:199], v[196:197], 0, v[152:153]
	s_waitcnt lgkmcnt(2)
	global_store_dwordx4 v[198:199], v[186:189], off nt
	s_cmp_gt_i32 s44, 0x18fff
	s_cselect_b64 s[4:5], -1, 0
	v_lshl_add_u64 v[186:187], v[196:197], 0, v[154:155]
	s_waitcnt lgkmcnt(1)
	global_store_dwordx4 v[186:187], v[182:185], off nt
	s_nop 1
	v_lshl_add_u64 v[182:183], v[196:197], 0, v[156:157]
	s_waitcnt lgkmcnt(0)
	global_store_dwordx4 v[182:183], v[190:193], off nt
	s_waitcnt lgkmcnt(0)

; #define LAS __attribute__((address_space(3)))
; __device__ __forceinline__ unsigned cvt2bf(float lo, float hi) { const f32x2_t v = {lo, hi}; const bf16x2_t r = __builtin_convertvector(v, bf16x2_t); return __builtin_bit_cast(unsigned, r); }
; __device__ __forceinline__ void tr_load(const TrItem& t, f32x4 (&ra)[8], f32x4 (&rb)[8], int lane) {
;     const int q = lane >> 4, n4 = lane & 15;
;     const float* p = t.src + (size_t)(2 * q) * t.N + 4 * n4;
; #pragma unroll
;     for (int i = 0; i < 8; ++i) { ra[i] = __builtin_nontemporal_load((const f32x4*)(p + (size_t)(8 * i) * t.N)); rb[i] = __builtin_nontemporal_load((const f32x4*)(p + (size_t)(8 * i + 1) * t.N)); }
; }
; __device__ __forceinline__ void tr_store(const TrItem& t, const f32x4 (&ra)[8], const f32x4 (&rb)[8], LAS unsigned* scr, int lane) {
;     const int q = lane >> 4, n4 = lane & 15;
; #pragma unroll
;     for (int i = 0; i < 8; ++i)
; #pragma unroll
;         for (int j = 0; j < 4; ++j) scr[(4 * n4 + j) * 32 + ((i ^ (n4 & 7)) << 2) + q] = cvt2bf(ra[i][j], rb[i][j]);
; __device__ __forceinline__ void conv_items(const Args& a, LAS unsigned char* lds, int it0, int it1, int vcu, int G, int lane, int wave) {
;     ...
;         TrItem nxt = tr_decode(a, has ? nx : it);
;         if (has) tr_load(nxt, na, nb_, lane);
;         tr_store(cur, ra, rb, scr, lane);
.LBB0_1201:
	v_mul_lo_u32 v68, s43, v130
	v_mul_lo_u32 v69, s42, v1
	v_mad_u64_u32 v[66:67], s[14:15], s42, v130, 0
	v_add3_u32 v67, v67, v69, v68
	v_lshl_add_u64 v[66:67], v[66:67], 2, s[38:39]
	v_lshlrev_b32_e32 v148, 2, v132
	v_lshl_add_u64 v[66:67], v[66:67], 0, v[148:149]
	s_lshl_b64 s[14:15], s[42:43], 2
	v_lshl_add_u64 v[70:71], v[66:67], 0, s[14:15]
	s_mul_i32 s24, s42, 28
	global_load_dwordx4 v[66:69], v[66:67], off nt
	s_nop 0
	global_load_dwordx4 v[74:77], v[70:71], off nt
	v_lshl_add_u64 v[70:71], v[70:71], 0, s[24:25]
	v_lshl_add_u64 v[78:79], v[70:71], 0, s[14:15]
	global_load_dwordx4 v[70:73], v[70:71], off nt
	s_nop 0
	global_load_dwordx4 v[86:89], v[78:79], off nt
	v_lshl_add_u64 v[78:79], v[78:79], 0, s[24:25]
	v_lshl_add_u64 v[82:83], v[78:79], 0, s[14:15]
	global_load_dwordx4 v[78:81], v[78:79], off nt
	s_nop 0
	global_load_dwordx4 v[98:101], v[82:83], off nt
	v_lshl_add_u64 v[82:83], v[82:83], 0, s[24:25]
	v_lshl_add_u64 v[90:91], v[82:83], 0, s[14:15]
	v_lshl_add_u64 v[94:95], v[90:91], 0, s[24:25]
	global_load_dwordx4 v[82:85], v[82:83], off nt
	s_nop 0
	global_load_dwordx4 v[106:109], v[90:91], off nt
	s_nop 0
	global_load_dwordx4 v[90:93], v[94:95], off nt
	v_lshl_add_u64 v[94:95], v[94:95], 0, s[14:15]
	v_lshl_add_u64 v[102:103], v[94:95], 0, s[24:25]
	global_load_dwordx4 v[114:117], v[94:95], off nt
	s_nop 0
	global_load_dwordx4 v[94:97], v[102:103], off nt
	v_lshl_add_u64 v[102:103], v[102:103], 0, s[14:15]
	v_lshl_add_u64 v[110:111], v[102:103], 0, s[24:25]
	global_load_dwordx4 v[118:121], v[102:103], off nt
	s_nop 0
	global_load_dwordx4 v[102:105], v[110:111], off nt
	v_lshl_add_u64 v[110:111], v[110:111], 0, s[14:15]
	v_lshl_add_u64 v[126:127], v[110:111], 0, s[24:25]
	global_load_dwordx4 v[122:125], v[110:111], off nt
	s_nop 0
	global_load_dwordx4 v[110:113], v[126:127], off nt
	v_lshl_add_u64 v[126:127], v[126:127], 0, s[14:15]
	global_load_dwordx4 v[126:129], v[126:127], off nt
	s_waitcnt vmcnt(30)
	v_cvt_pk_bf16_f32 v148, v2, v6
	v_cvt_pk_bf16_f32 v181, v3, v7
	ds_write2_b32 v173, v148, v181 offset1:32
	v_cvt_pk_bf16_f32 v148, v4, v8
	v_cvt_pk_bf16_f32 v181, v5, v9
	ds_write2_b32 v173, v148, v181 offset0:64 offset1:96
	s_waitcnt vmcnt(28)
	v_cvt_pk_bf16_f32 v148, v10, v14
	v_cvt_pk_bf16_f32 v181, v11, v15
	ds_write2_b32 v174, v148, v181 offset1:32
	v_cvt_pk_bf16_f32 v148, v12, v16
	v_cvt_pk_bf16_f32 v181, v13, v17
	ds_write2_b32 v174, v148, v181 offset0:64 offset1:96
	s_waitcnt vmcnt(26)
	v_cvt_pk_bf16_f32 v148, v18, v22
	v_cvt_pk_bf16_f32 v181, v19, v23
	ds_write2_b32 v175, v148, v181 offset1:32
	v_cvt_pk_bf16_f32 v148, v20, v24
	v_cvt_pk_bf16_f32 v181, v21, v25
	ds_write2_b32 v175, v148, v181 offset0:64 offset1:96
	s_waitcnt vmcnt(24)
	v_cvt_pk_bf16_f32 v148, v26, v30
	v_cvt_pk_bf16_f32 v181, v27, v31
	ds_write2_b32 v176, v148, v181 offset1:32
	v_cvt_pk_bf16_f32 v148, v28, v32
	v_cvt_pk_bf16_f32 v181, v29, v33
	ds_write2_b32 v176, v148, v181 offset0:64 offset1:96
	s_waitcnt vmcnt(22)
	v_cvt_pk_bf16_f32 v148, v34, v38
	v_cvt_pk_bf16_f32 v181, v35, v39
	ds_write2_b32 v177, v148, v181 offset1:32
	v_cvt_pk_bf16_f32 v148, v36, v40
	v_cvt_pk_bf16_f32 v181, v37, v41
	ds_write2_b32 v177, v148, v181 offset0:64 offset1:96
	s_waitcnt vmcnt(20)
	v_cvt_pk_bf16_f32 v148, v42, v46
	v_cvt_pk_bf16_f32 v181, v43, v47
	ds_write2_b32 v178, v148, v181 offset1:32
	v_cvt_pk_bf16_f32 v148, v44, v48
	v_cvt_pk_bf16_f32 v181, v45, v49
	ds_write2_b32 v178, v148, v181 offset0:64 offset1:96
	s_waitcnt vmcnt(18)
	v_cvt_pk_bf16_f32 v148, v50, v54
	v_cvt_pk_bf16_f32 v181, v51, v55
	ds_write2_b32 v179, v148, v181 offset1:32
	v_cvt_pk_bf16_f32 v148, v52, v56
	v_cvt_pk_bf16_f32 v181, v53, v57
	ds_write2_b32 v179, v148, v181 offset0:64 offset1:96
	s_waitcnt vmcnt(16)
	v_cvt_pk_bf16_f32 v148, v58, v62
	v_cvt_pk_bf16_f32 v181, v59, v63
	ds_write2_b32 v180, v148, v181 offset1:32
	v_cvt_pk_bf16_f32 v148, v60, v64
	v_cvt_pk_bf16_f32 v181, v61, v65
	ds_write2_b32 v180, v148, v181 offset0:64 offset1:96
	s_branch .Lcvj_7

; #define LAS __attribute__((address_space(3)))
; #define LDS_WAIT() asm volatile("s_waitcnt lgkmcnt(0)" ::: "memory")
; __device__ __forceinline__ TrItem tr_decode(const Args& a, int it) {
;     ...
;     if (r < T_IN) { const int kb = r & 31, nb = r >> 5; t.N = INCOLS; t.src = a.in[I_WIN] + (size_t)(64 * kb) * INCOLS + 64 * nb; t.dst = (bf16*)(ws + WS_WIN) + (size_t)(64 * nb) * DM + 64 * kb; return t; } r -= T_IN;
;     if (r < T_OUT) { const int kb = r & 31, nb = r >> 5; t.N = DM; t.src = a.in[I_WOUT] + (size_t)(64 * kb) * DM + 64 * nb; t.dst = (bf16*)(ws + WS_WOUT) + (size_t)(64 * nb) * DM + 64 * kb; return t; } r -= T_OUT;
;     if (r < NEXP * T_GU1) { const int e = r / T_GU1, q = r % T_GU1, kb = q & 31, nb = q >> 5, n0 = 64 * nb;
;         const int drow0 = n0 < 2048 ? (n0 >> 7) * 256 + (n0 & 127) : ((n0 - 2048) >> 7) * 256 + 128 + ((n0 - 2048) & 127);
;         t.N = 4096; t.src = a.in[I_WGU] + (size_t)e * DM * 4096 + (size_t)(64 * kb) * 4096 + n0; t.dst = (bf16*)(ws + WS_WGU) + (size_t)e * 4096 * DM + (size_t)drow0 * DM + 64 * kb; return t; } r -= NEXP * T_GU1;
;     { const int e = r / T_DN1, q = r % T_DN1, kb = q & 31, nb = q >> 5;
;         t.N = DM; t.src = a.in[I_WDN] + (size_t)e * DM * DM + (size_t)(64 * kb) * DM + 64 * nb; t.dst = (bf16*)(ws + WS_WDN) + (size_t)e * DM * DM + (size_t)(64 * nb) * DM + 64 * kb; return t; }
; __device__ __forceinline__ void tr_store(const TrItem& t, const f32x4 (&ra)[8], const f32x4 (&rb)[8], LAS unsigned* scr, int lane) {
;     ...
;     const int nr = lane >> 3, ch = lane & 7;
; #pragma unroll
;     for (int i = 0; i < 8; ++i) { const int n = nr + 8 * i; const v4u v = *(const LAS v4u*)(scr + n * 32 + ((ch ^ ((n >> 2) & 7)) << 2));
;         __builtin_nontemporal_store(v, (v4u*)(t.dst + (size_t)n * DM + 8 * ch)); }
;     LDS_WAIT(); asm volatile("" ::: "memory");
.Lcvj_7:
	s_waitcnt lgkmcnt(0)
	ds_read_b128 v[182:185], v131
	ds_read_b128 v[186:189], v133
	v_lshlrev_b32_e32 v148, 1, v134
	v_lshl_add_u64 v[196:197], s[2:3], 0, v[148:149]
	v_lshl_add_u64 v[190:191], v[196:197], 0, v[136:137]
	s_waitcnt lgkmcnt(1)
	global_store_dwordx4 v[190:191], v[182:185], off nt
	ds_read_b128 v[182:185], v135
	v_lshl_add_u64 v[190:191], v[196:197], 0, v[138:139]
	s_waitcnt lgkmcnt(1)
	global_store_dwordx4 v[190:191], v[186:189], off nt
	ds_read_b128 v[186:189], v168
	v_lshl_add_u64 v[190:191], v[196:197], 0, v[140:141]
	s_waitcnt lgkmcnt(1)
	global_store_dwordx4 v[190:191], v[182:185], off nt
	ds_read_b128 v[182:185], v169
	v_lshl_add_u64 v[190:191], v[196:197], 0, v[142:143]
	s_waitcnt lgkmcnt(1)
	global_store_dwordx4 v[190:191], v[186:189], off nt
	v_lshl_add_u64 v[190:191], v[196:197], 0, v[144:145]
	ds_read_b128 v[186:189], v170
	s_waitcnt lgkmcnt(1)
	global_store_dwordx4 v[190:191], v[182:185], off nt
	ds_read_b128 v[182:185], v171
	ds_read_b128 v[190:193], v172
	v_lshl_add_u64 v[198:199], v[196:197], 0, v[152:153]
	s_waitcnt lgkmcnt(2)
	global_store_dwordx4 v[198:199], v[186:189], off nt
	s_and_b64 vcc, exec, s[4:5]
	s_mov_b64 s[4:5], -1
	v_lshl_add_u64 v[186:187], v[196:197], 0, v[154:155]
	s_waitcnt lgkmcnt(1)
	global_store_dwordx4 v[186:187], v[182:185], off nt
	s_nop 1
	v_lshl_add_u64 v[182:183], v[196:197], 0, v[156:157]
	s_waitcnt lgkmcnt(0)
	global_store_dwordx4 v[182:183], v[190:193], off nt
	s_waitcnt lgkmcnt(0)
	s_cbranch_vccnz .LBB0_1185
	s_add_i32 s4, s61, s44
	s_cmp_lt_i32 s4, 0x19000
	s_cselect_b64 s[38:39], -1, 0
	s_and_b64 s[2:3], s[38:39], exec
	s_cselect_b32 s66, s4, s65
	s_cmpk_gt_i32 s66, 0xbff
	s_mov_b64 s[46:47], -1
	s_cbranch_scc0 .LBB0_1220
	s_cmpk_gt_u32 s66, 0xfff
	s_cbranch_scc0 .LBB0_1214
	s_cmp_gt_u32 s66, 0x10fff
	s_mov_b64 s[44:45], -1
	s_cbranch_scc0 .LBB0_1207
	s_add_i32 s2, s66, 0xfffef000
	s_lshr_b32 s24, s2, 10
	s_lshl_b64 s[2:3], s[24:25], 24
	v_readlane_b32 s68, v246, 0
	v_readlane_b32 s69, v246, 1
	s_add_u32 s2, s68, s2
	s_addc_u32 s3, s69, s3
	s_lshl_b32 s4, s66, 6
	s_and_b32 s4, s4, 0x7c0
	s_lshl_b32 s14, s4, 13
	s_add_u32 s14, s2, s14
	s_addc_u32 s15, s3, 0
	s_lshl_b32 s2, s66, 1
	s_and_b32 s2, s2, 0x7c0
	s_lshl_b32 s36, s2, 2
	s_add_u32 s42, s14, s36
	s_addc_u32 s43, s15, 0
	s_lshl_b64 s[14:15], s[24:25], 23
	s_add_u32 s36, s57, s14
	v_readlane_b32 s70, v246, 2
	v_readlane_b32 s71, v246, 3
	v_readlane_b32 s72, v246, 4
	v_readlane_b32 s73, v246, 5
	v_readlane_b32 s74, v246, 6
	v_readlane_b32 s75, v246, 7
	s_mov_b32 s5, s25
	s_mov_b32 s3, s25
	s_addc_u32 s37, s58, s15
	s_mov_b64 s[44:45], 0

; __device__ __forceinline__ void tr_load(const TrItem& t, f32x4 (&ra)[8], f32x4 (&rb)[8], int lane) {
;     const int q = lane >> 4, n4 = lane & 15;
;     const float* p = t.src + (size_t)(2 * q) * t.N + 4 * n4;
; #pragma unroll
;     for (int i = 0; i < 8; ++i) { ra[i] = __builtin_nontemporal_load((const f32x4*)(p + (size_t)(8 * i) * t.N)); rb[i] = __builtin_nontemporal_load((const f32x4*)(p + (size_t)(8 * i + 1) * t.N)); }
; }
; __device__ __forceinline__ void conv_items(const Args& a, LAS unsigned char* lds, int it0, int it1, int vcu, int G, int lane, int wave) {
;     ...
;         it = nx; nx = it + NGW; has = nx < it1;
;         cur = tr_decode(a, has ? nx : it);
;         if (has) tr_load(cur, ra, rb, lane);
;         tr_store(nxt, na, nb_, scr, lane);
.LBB0_1222:
	v_mul_lo_u32 v4, s45, v130
	v_mul_lo_u32 v5, s44, v1
	v_mad_u64_u32 v[2:3], s[14:15], s44, v130, 0
	v_add3_u32 v3, v3, v5, v4
	v_lshl_add_u64 v[2:3], v[2:3], 2, s[42:43]
	v_lshlrev_b32_e32 v4, 2, v132
	v_mov_b32_e32 v5, v149
	v_lshl_add_u64 v[2:3], v[2:3], 0, v[4:5]
	s_lshl_b64 s[14:15], s[44:45], 2
	v_lshl_add_u64 v[10:11], v[2:3], 0, s[14:15]
	s_mul_i32 s24, s44, 28
	global_load_dwordx4 v[2:5], v[2:3], off nt
	s_nop 0
	global_load_dwordx4 v[6:9], v[10:11], off nt
	v_lshl_add_u64 v[10:11], v[10:11], 0, s[24:25]
	v_lshl_add_u64 v[18:19], v[10:11], 0, s[14:15]
	global_load_dwordx4 v[10:13], v[10:11], off nt
	s_nop 0
	global_load_dwordx4 v[14:17], v[18:19], off nt
	v_lshl_add_u64 v[18:19], v[18:19], 0, s[24:25]
	v_lshl_add_u64 v[26:27], v[18:19], 0, s[14:15]
	global_load_dwordx4 v[18:21], v[18:19], off nt
	s_nop 0
	global_load_dwordx4 v[22:25], v[26:27], off nt
	v_lshl_add_u64 v[26:27], v[26:27], 0, s[24:25]
	v_lshl_add_u64 v[34:35], v[26:27], 0, s[14:15]
	v_lshl_add_u64 v[38:39], v[34:35], 0, s[24:25]
	v_lshl_add_u64 v[42:43], v[38:39], 0, s[14:15]
	v_lshl_add_u64 v[46:47], v[42:43], 0, s[24:25]
	v_lshl_add_u64 v[50:51], v[46:47], 0, s[14:15]
	v_lshl_add_u64 v[54:55], v[50:51], 0, s[24:25]
	v_lshl_add_u64 v[58:59], v[54:55], 0, s[14:15]
	v_lshl_add_u64 v[62:63], v[58:59], 0, s[24:25]
	global_load_dwordx4 v[26:29], v[26:27], off nt
	s_nop 0
	global_load_dwordx4 v[30:33], v[34:35], off nt
	s_nop 0
	global_load_dwordx4 v[34:37], v[38:39], off nt
	s_nop 0
	global_load_dwordx4 v[38:41], v[42:43], off nt
	s_nop 0
	global_load_dwordx4 v[42:45], v[46:47], off nt
	s_nop 0
	global_load_dwordx4 v[46:49], v[50:51], off nt
	s_nop 0
	global_load_dwordx4 v[50:53], v[54:55], off nt
	s_nop 0
	global_load_dwordx4 v[54:57], v[58:59], off nt
	s_nop 0
	global_load_dwordx4 v[58:61], v[62:63], off nt
	v_lshl_add_u64 v[62:63], v[62:63], 0, s[14:15]
	global_load_dwordx4 v[62:65], v[62:63], off nt
	s_waitcnt vmcnt(24)
	s_branch .LBB0_1184
